# 64 redundant post-barrier lgkmcnt(0) waits deleted from the GEMM K-loops
# speedup vs baseline: 1.0039x; 1.0039x over previous
.LBB0_261:
	ds_read_b128 v[144:147], v141
	ds_read_b128 v[148:151], v141 offset:1024
	ds_read_b128 v[152:155], v141 offset:2048
	ds_read_b128 v[156:159], v141 offset:3072
	ds_read_b128 v[160:163], v142
	ds_read_b128 v[164:167], v142 offset:1024
	ds_read_b128 v[168:171], v142 offset:2048
	ds_read_b128 v[172:175], v142 offset:3072
	s_add_i32 s0, s67, s10
	s_add_u32 s0, s4, s0
	s_addc_u32 s1, s5, 0
	s_add_i32 m0, s22, 0xc000
	s_add_i32 s30, s22, 0xe000
	s_add_i32 s31, s10, 0xfff80080
	s_cmp_eq_u32 s18, 28
	s_cselect_b32 s19, s45, s67
	s_cselect_b32 s68, s44, s66
	v_lshl_add_u64 v[208:209], s[0:1], 0, v[128:129]
	ds_read_b128 v[176:179], v143
	ds_read_b128 v[180:183], v143 offset:1024
	ds_read_b128 v[184:187], v143 offset:2048
	ds_read_b128 v[188:191], v143 offset:3072
	ds_read_b128 v[192:195], v143 offset:4096
	ds_read_b128 v[196:199], v143 offset:5120
	ds_read_b128 v[200:203], v143 offset:6144
	ds_read_b128 v[204:207], v143 offset:7168
	global_load_lds_dwordx4 v[208:209], off
	v_lshl_add_u64 v[208:209], s[0:1], 0, v[130:131]
	s_mov_b32 m0, s30
	s_nop 0
	global_load_lds_dwordx4 v[208:209], off
	s_waitcnt vmcnt(8)
	s_waitcnt lgkmcnt(0)
	s_barrier
	v_mfma_f32_16x16x32_bf16 v[124:127], v[144:147], v[176:179], v[124:127]
	v_mfma_f32_16x16x32_bf16 v[120:123], v[152:155], v[176:179], v[120:123]
	v_mfma_f32_16x16x32_bf16 v[116:119], v[144:147], v[184:187], v[116:119]
	v_mfma_f32_16x16x32_bf16 v[112:115], v[152:155], v[184:187], v[112:115]
	v_mfma_f32_16x16x32_bf16 v[108:111], v[144:147], v[192:195], v[108:111]
	v_mfma_f32_16x16x32_bf16 v[100:103], v[152:155], v[192:195], v[100:103]
	v_mfma_f32_16x16x32_bf16 v[92:95], v[144:147], v[200:203], v[92:95]
	v_mfma_f32_16x16x32_bf16 v[84:87], v[152:155], v[200:203], v[84:87]
	v_mfma_f32_16x16x32_bf16 v[124:127], v[148:151], v[180:183], v[124:127]
	v_mfma_f32_16x16x32_bf16 v[120:123], v[156:159], v[180:183], v[120:123]
	v_mfma_f32_16x16x32_bf16 v[116:119], v[148:151], v[188:191], v[116:119]
	v_mfma_f32_16x16x32_bf16 v[112:115], v[156:159], v[188:191], v[112:115]
	v_mfma_f32_16x16x32_bf16 v[108:111], v[148:151], v[196:199], v[108:111]
	v_mfma_f32_16x16x32_bf16 v[100:103], v[156:159], v[196:199], v[100:103]
	v_mfma_f32_16x16x32_bf16 v[92:95], v[148:151], v[204:207], v[92:95]
	v_mfma_f32_16x16x32_bf16 v[84:87], v[156:159], v[204:207], v[84:87]
	v_mfma_f32_16x16x32_bf16 v[104:107], v[160:163], v[176:179], v[104:107]
	v_mfma_f32_16x16x32_bf16 v[96:99], v[168:171], v[176:179], v[96:99]
	v_mfma_f32_16x16x32_bf16 v[88:91], v[160:163], v[184:187], v[88:91]
	v_mfma_f32_16x16x32_bf16 v[80:83], v[168:171], v[184:187], v[80:83]
	v_mfma_f32_16x16x32_bf16 v[76:79], v[160:163], v[192:195], v[76:79]
	v_mfma_f32_16x16x32_bf16 v[72:75], v[168:171], v[192:195], v[72:75]
	v_mfma_f32_16x16x32_bf16 v[68:71], v[160:163], v[200:203], v[68:71]
	v_mfma_f32_16x16x32_bf16 v[64:67], v[168:171], v[200:203], v[64:67]
	v_mfma_f32_16x16x32_bf16 v[104:107], v[164:167], v[180:183], v[104:107]
	v_mfma_f32_16x16x32_bf16 v[96:99], v[172:175], v[180:183], v[96:99]
	v_mfma_f32_16x16x32_bf16 v[88:91], v[164:167], v[188:191], v[88:91]
	v_mfma_f32_16x16x32_bf16 v[80:83], v[172:175], v[188:191], v[80:83]
	v_mfma_f32_16x16x32_bf16 v[76:79], v[164:167], v[196:199], v[76:79]
	v_mfma_f32_16x16x32_bf16 v[72:75], v[172:175], v[196:199], v[72:75]
	v_mfma_f32_16x16x32_bf16 v[68:71], v[164:167], v[204:207], v[68:71]
	v_mfma_f32_16x16x32_bf16 v[64:67], v[172:175], v[204:207], v[64:67]
	s_barrier
	s_cselect_b32 s30, 0, s31
	s_add_i32 s0, s30, s68
	s_ashr_i32 s1, s0, 31
	s_add_u32 s0, s6, s0
	s_addc_u32 s1, s7, s1
	s_add_i32 s31, s38, s27
	v_lshl_add_u64 v[208:209], s[0:1], 0, v[128:129]
	s_mov_b32 m0, s31
	ds_read_b128 v[176:179], v143 offset:16384
	ds_read_b128 v[180:183], v143 offset:17408
	ds_read_b128 v[184:187], v143 offset:18432
	ds_read_b128 v[188:191], v143 offset:19456
	ds_read_b128 v[192:195], v143 offset:20480
	ds_read_b128 v[196:199], v143 offset:21504
	ds_read_b128 v[200:203], v143 offset:22528
	ds_read_b128 v[204:207], v143 offset:23552
	global_load_lds_dwordx4 v[208:209], off
	s_add_i32 m0, s31, 0x2000
	s_add_i32 s31, s68, 0x80000
	v_lshl_add_u64 v[208:209], s[0:1], 0, v[130:131]
	s_add_i32 s0, s31, s30
	s_ashr_i32 s1, s0, 31
	s_add_u32 s0, s6, s0
	s_addc_u32 s1, s7, s1
	s_add_i32 s69, s39, s27
	global_load_lds_dwordx4 v[208:209], off
	v_lshl_add_u64 v[208:209], s[0:1], 0, v[128:129]
	s_mov_b32 m0, s69
	s_nop 0
	global_load_lds_dwordx4 v[208:209], off
	s_add_i32 m0, s69, 0x2000
	s_add_i32 s69, s30, s19
	v_lshl_add_u64 v[208:209], s[0:1], 0, v[130:131]
	s_add_u32 s0, s4, s69
	s_addc_u32 s1, s5, 0
	global_load_lds_dwordx4 v[208:209], off
	v_lshl_add_u64 v[208:209], s[0:1], 0, v[128:129]
	s_mov_b32 m0, s22
	s_nop 0
	global_load_lds_dwordx4 v[208:209], off
	v_lshl_add_u64 v[208:209], s[0:1], 0, v[130:131]
	s_mov_b32 m0, s23
	s_nop 0
	global_load_lds_dwordx4 v[208:209], off
	s_waitcnt vmcnt(8)
	s_waitcnt lgkmcnt(0)
	s_barrier
	v_mfma_f32_16x16x32_bf16 v[60:63], v[144:147], v[176:179], v[60:63]
	v_mfma_f32_16x16x32_bf16 v[56:59], v[152:155], v[176:179], v[56:59]
	v_mfma_f32_16x16x32_bf16 v[52:55], v[144:147], v[184:187], v[52:55]
	v_mfma_f32_16x16x32_bf16 v[48:51], v[152:155], v[184:187], v[48:51]
	v_mfma_f32_16x16x32_bf16 v[44:47], v[144:147], v[192:195], v[44:47]
	v_mfma_f32_16x16x32_bf16 v[36:39], v[152:155], v[192:195], v[36:39]
	v_mfma_f32_16x16x32_bf16 v[28:31], v[144:147], v[200:203], v[28:31]
	v_mfma_f32_16x16x32_bf16 v[20:23], v[152:155], v[200:203], v[20:23]
	v_mfma_f32_16x16x32_bf16 v[60:63], v[148:151], v[180:183], v[60:63]
	v_mfma_f32_16x16x32_bf16 v[56:59], v[156:159], v[180:183], v[56:59]
	v_mfma_f32_16x16x32_bf16 v[52:55], v[148:151], v[188:191], v[52:55]
	v_mfma_f32_16x16x32_bf16 v[48:51], v[156:159], v[188:191], v[48:51]
	v_mfma_f32_16x16x32_bf16 v[44:47], v[148:151], v[196:199], v[44:47]
	v_mfma_f32_16x16x32_bf16 v[36:39], v[156:159], v[196:199], v[36:39]
	v_mfma_f32_16x16x32_bf16 v[28:31], v[148:151], v[204:207], v[28:31]
	v_mfma_f32_16x16x32_bf16 v[20:23], v[156:159], v[204:207], v[20:23]
	v_mfma_f32_16x16x32_bf16 v[40:43], v[160:163], v[176:179], v[40:43]
	v_mfma_f32_16x16x32_bf16 v[32:35], v[168:171], v[176:179], v[32:35]
	v_mfma_f32_16x16x32_bf16 v[24:27], v[160:163], v[184:187], v[24:27]
	v_mfma_f32_16x16x32_bf16 v[16:19], v[168:171], v[184:187], v[16:19]
	v_mfma_f32_16x16x32_bf16 v[12:15], v[160:163], v[192:195], v[12:15]
	v_mfma_f32_16x16x32_bf16 v[8:11], v[168:171], v[192:195], v[8:11]
	v_mfma_f32_16x16x32_bf16 v[4:7], v[160:163], v[200:203], v[4:7]
	v_mfma_f32_16x16x32_bf16 v[0:3], v[168:171], v[200:203], v[0:3]
	v_mfma_f32_16x16x32_bf16 v[40:43], v[164:167], v[180:183], v[40:43]
	v_mfma_f32_16x16x32_bf16 v[32:35], v[172:175], v[180:183], v[32:35]
	v_mfma_f32_16x16x32_bf16 v[24:27], v[164:167], v[188:191], v[24:27]
	v_mfma_f32_16x16x32_bf16 v[16:19], v[172:175], v[188:191], v[16:19]
	v_mfma_f32_16x16x32_bf16 v[12:15], v[164:167], v[196:199], v[12:15]
	v_mfma_f32_16x16x32_bf16 v[8:11], v[172:175], v[196:199], v[8:11]
	v_mfma_f32_16x16x32_bf16 v[4:7], v[164:167], v[204:207], v[4:7]
	v_mfma_f32_16x16x32_bf16 v[0:3], v[172:175], v[204:207], v[0:3]
	s_barrier
	s_add_i32 s70, 0, 0x18000
	s_add_i32 s71, 0, 0x1c000
	v_add_u32_e32 v156, s70, v140
	v_add_u32_e32 v172, s71, v140
	ds_read_b128 v[144:147], v156
	ds_read_b128 v[148:151], v156 offset:1024
	ds_read_b128 v[152:155], v156 offset:2048
	ds_read_b128 v[156:159], v156 offset:3072
	ds_read_b128 v[160:163], v172
	ds_read_b128 v[164:167], v172 offset:1024
	ds_read_b128 v[168:171], v172 offset:2048
	ds_read_b128 v[172:175], v172 offset:3072
	s_add_i32 s69, s69, 0x80000
	s_add_u32 s0, s4, s69
	s_addc_u32 s1, s5, 0
	s_mov_b32 m0, s24
	v_lshl_add_u64 v[208:209], s[0:1], 0, v[128:129]
	ds_read_b128 v[176:179], v143 offset:32768
	ds_read_b128 v[180:183], v143 offset:33792
	ds_read_b128 v[184:187], v143 offset:34816
	ds_read_b128 v[188:191], v143 offset:35840
	ds_read_b128 v[192:195], v143 offset:36864
	ds_read_b128 v[196:199], v143 offset:37888
	ds_read_b128 v[200:203], v143 offset:38912
	ds_read_b128 v[204:207], v143 offset:39936
	global_load_lds_dwordx4 v[208:209], off
	v_lshl_add_u64 v[208:209], s[0:1], 0, v[130:131]
	s_mov_b32 m0, s25
	s_nop 0
	global_load_lds_dwordx4 v[208:209], off
	s_waitcnt vmcnt(8)
	s_waitcnt lgkmcnt(0)
	s_barrier
	v_mfma_f32_16x16x32_bf16 v[124:127], v[144:147], v[176:179], v[124:127]
	v_mfma_f32_16x16x32_bf16 v[120:123], v[152:155], v[176:179], v[120:123]
	v_mfma_f32_16x16x32_bf16 v[116:119], v[144:147], v[184:187], v[116:119]
	v_mfma_f32_16x16x32_bf16 v[112:115], v[152:155], v[184:187], v[112:115]
	v_mfma_f32_16x16x32_bf16 v[108:111], v[144:147], v[192:195], v[108:111]
	v_mfma_f32_16x16x32_bf16 v[100:103], v[152:155], v[192:195], v[100:103]
	v_mfma_f32_16x16x32_bf16 v[92:95], v[144:147], v[200:203], v[92:95]
	v_mfma_f32_16x16x32_bf16 v[84:87], v[152:155], v[200:203], v[84:87]
	v_mfma_f32_16x16x32_bf16 v[124:127], v[148:151], v[180:183], v[124:127]
	v_mfma_f32_16x16x32_bf16 v[120:123], v[156:159], v[180:183], v[120:123]
	v_mfma_f32_16x16x32_bf16 v[116:119], v[148:151], v[188:191], v[116:119]
	v_mfma_f32_16x16x32_bf16 v[112:115], v[156:159], v[188:191], v[112:115]
	v_mfma_f32_16x16x32_bf16 v[108:111], v[148:151], v[196:199], v[108:111]
	v_mfma_f32_16x16x32_bf16 v[100:103], v[156:159], v[196:199], v[100:103]
	v_mfma_f32_16x16x32_bf16 v[92:95], v[148:151], v[204:207], v[92:95]
	v_mfma_f32_16x16x32_bf16 v[84:87], v[156:159], v[204:207], v[84:87]
	v_mfma_f32_16x16x32_bf16 v[104:107], v[160:163], v[176:179], v[104:107]
	v_mfma_f32_16x16x32_bf16 v[96:99], v[168:171], v[176:179], v[96:99]
	v_mfma_f32_16x16x32_bf16 v[88:91], v[160:163], v[184:187], v[88:91]
	v_mfma_f32_16x16x32_bf16 v[80:83], v[168:171], v[184:187], v[80:83]
	v_mfma_f32_16x16x32_bf16 v[76:79], v[160:163], v[192:195], v[76:79]
	v_mfma_f32_16x16x32_bf16 v[72:75], v[168:171], v[192:195], v[72:75]
	v_mfma_f32_16x16x32_bf16 v[68:71], v[160:163], v[200:203], v[68:71]
	v_mfma_f32_16x16x32_bf16 v[64:67], v[168:171], v[200:203], v[64:67]
	v_mfma_f32_16x16x32_bf16 v[104:107], v[164:167], v[180:183], v[104:107]
	v_mfma_f32_16x16x32_bf16 v[96:99], v[172:175], v[180:183], v[96:99]
	v_mfma_f32_16x16x32_bf16 v[88:91], v[164:167], v[188:191], v[88:91]
	v_mfma_f32_16x16x32_bf16 v[80:83], v[172:175], v[188:191], v[80:83]
	v_mfma_f32_16x16x32_bf16 v[76:79], v[164:167], v[196:199], v[76:79]
	v_mfma_f32_16x16x32_bf16 v[72:75], v[172:175], v[196:199], v[72:75]
	v_mfma_f32_16x16x32_bf16 v[68:71], v[164:167], v[204:207], v[68:71]
	v_mfma_f32_16x16x32_bf16 v[64:67], v[172:175], v[204:207], v[64:67]
	s_barrier
; template <class Epi, class Sched, class Hook = NoHook>
; __device__ __forceinline__ void gemm_phase_w(LAS unsigned char* lds, const Sched& S, const Epi& E, int wave_id, const Hook& HK = Hook()) {
;     ...
;         if constexpr (!SEG2) {
;             for (int tt = 0; tt < nt; tt += 2) {
;                 if constexpr (GATHER) { if (tt == nt - 2) {
;                     if (has_next) { gnxt_00 = S.grow_l(nxt, lds, nbuf, R0) + (unsigned)(C0 * 2); gnxt_01 = S.grow_l(nxt, lds, nbuf, R1) + (unsigned)(C1 * 2); gnxt_10 = S.grow_l(nxt, lds, nbuf, 128 + R0) + (unsigned)(C0 * 2); gnxt_11 = S.grow_l(nxt, lds, nbuf, 128 + R1) + (unsigned)(C1 * 2); }
;                     else { gnxt_00 = gcur_00; gnxt_01 = gcur_01; gnxt_10 = gcur_10; gnxt_11 = gcur_11; } } }
;                 PG_TRIP(tt, false, false, false);
;             }
	s_bitset1_b32 s30, 7
	s_add_i32 s0, s30, s68
	s_ashr_i32 s1, s0, 31
	s_add_u32 s0, s6, s0
	s_addc_u32 s1, s7, s1
	s_add_i32 s68, s70, s27
	v_lshl_add_u64 v[208:209], s[0:1], 0, v[128:129]
	s_mov_b32 m0, s68
	ds_read_b128 v[176:179], v143 offset:49152
	ds_read_b128 v[180:183], v143 offset:50176
	ds_read_b128 v[184:187], v143 offset:51200
	ds_read_b128 v[188:191], v143 offset:52224
	ds_read_b128 v[192:195], v143 offset:53248
	ds_read_b128 v[196:199], v143 offset:54272
	ds_read_b128 v[200:203], v143 offset:55296
	ds_read_b128 v[204:207], v143 offset:56320
	global_load_lds_dwordx4 v[208:209], off
	v_lshl_add_u64 v[208:209], s[0:1], 0, v[130:131]
	s_add_i32 s0, s30, s31
	s_add_i32 m0, s68, 0x2000
	s_ashr_i32 s1, s0, 31
	s_add_u32 s0, s6, s0
	s_addc_u32 s1, s7, s1
	s_add_i32 s31, s71, s27
	global_load_lds_dwordx4 v[208:209], off
	v_lshl_add_u64 v[208:209], s[0:1], 0, v[128:129]
	s_mov_b32 m0, s31
	s_add_i32 s30, s30, s19
	global_load_lds_dwordx4 v[208:209], off
	s_add_i32 m0, s31, 0x2000
	v_lshl_add_u64 v[208:209], s[0:1], 0, v[130:131]
	s_add_u32 s0, s4, s30
	s_addc_u32 s1, s5, 0
	global_load_lds_dwordx4 v[208:209], off
	v_lshl_add_u64 v[208:209], s[0:1], 0, v[128:129]
	s_mov_b32 m0, s36
	s_nop 0
	global_load_lds_dwordx4 v[208:209], off
	v_lshl_add_u64 v[208:209], s[0:1], 0, v[130:131]
	s_mov_b32 m0, s37
	s_nop 0
	global_load_lds_dwordx4 v[208:209], off
	s_waitcnt vmcnt(8)
	s_waitcnt lgkmcnt(0)
	s_barrier
	v_mfma_f32_16x16x32_bf16 v[60:63], v[144:147], v[176:179], v[60:63]
	v_mfma_f32_16x16x32_bf16 v[56:59], v[152:155], v[176:179], v[56:59]
	v_mfma_f32_16x16x32_bf16 v[52:55], v[144:147], v[184:187], v[52:55]
	v_mfma_f32_16x16x32_bf16 v[48:51], v[152:155], v[184:187], v[48:51]
	v_mfma_f32_16x16x32_bf16 v[44:47], v[144:147], v[192:195], v[44:47]
	v_mfma_f32_16x16x32_bf16 v[36:39], v[152:155], v[192:195], v[36:39]
	v_mfma_f32_16x16x32_bf16 v[28:31], v[144:147], v[200:203], v[28:31]
	v_mfma_f32_16x16x32_bf16 v[20:23], v[152:155], v[200:203], v[20:23]
	v_mfma_f32_16x16x32_bf16 v[60:63], v[148:151], v[180:183], v[60:63]
	v_mfma_f32_16x16x32_bf16 v[56:59], v[156:159], v[180:183], v[56:59]
	v_mfma_f32_16x16x32_bf16 v[52:55], v[148:151], v[188:191], v[52:55]
	v_mfma_f32_16x16x32_bf16 v[48:51], v[156:159], v[188:191], v[48:51]
	v_mfma_f32_16x16x32_bf16 v[44:47], v[148:151], v[196:199], v[44:47]
	v_mfma_f32_16x16x32_bf16 v[36:39], v[156:159], v[196:199], v[36:39]
	v_mfma_f32_16x16x32_bf16 v[28:31], v[148:151], v[204:207], v[28:31]
	v_mfma_f32_16x16x32_bf16 v[20:23], v[156:159], v[204:207], v[20:23]
	v_mfma_f32_16x16x32_bf16 v[40:43], v[160:163], v[176:179], v[40:43]
	v_mfma_f32_16x16x32_bf16 v[32:35], v[168:171], v[176:179], v[32:35]
	v_mfma_f32_16x16x32_bf16 v[24:27], v[160:163], v[184:187], v[24:27]
	v_mfma_f32_16x16x32_bf16 v[16:19], v[168:171], v[184:187], v[16:19]
	v_mfma_f32_16x16x32_bf16 v[12:15], v[160:163], v[192:195], v[12:15]
	v_mfma_f32_16x16x32_bf16 v[8:11], v[168:171], v[192:195], v[8:11]
	v_mfma_f32_16x16x32_bf16 v[4:7], v[160:163], v[200:203], v[4:7]
	v_mfma_f32_16x16x32_bf16 v[0:3], v[168:171], v[200:203], v[0:3]
	v_mfma_f32_16x16x32_bf16 v[40:43], v[164:167], v[180:183], v[40:43]
	v_mfma_f32_16x16x32_bf16 v[32:35], v[172:175], v[180:183], v[32:35]
	v_mfma_f32_16x16x32_bf16 v[24:27], v[164:167], v[188:191], v[24:27]
	v_mfma_f32_16x16x32_bf16 v[16:19], v[172:175], v[188:191], v[16:19]
	v_mfma_f32_16x16x32_bf16 v[12:15], v[164:167], v[196:199], v[12:15]
	v_mfma_f32_16x16x32_bf16 v[8:11], v[172:175], v[196:199], v[8:11]
	v_mfma_f32_16x16x32_bf16 v[4:7], v[164:167], v[204:207], v[4:7]
	v_mfma_f32_16x16x32_bf16 v[0:3], v[172:175], v[204:207], v[0:3]
	s_barrier
	s_addk_i32 s10, 0x100
	s_add_i32 s18, s18, 2
	s_cmp_gt_u32 s18, 29
	s_cbranch_scc0 .LBB0_261
	s_and_b64 vcc, exec, s[14:15]
	s_cbranch_vccz .LBB0_264
	s_barrier

.LBB0_386:
	ds_read_b128 v[142:145], v139
	ds_read_b128 v[146:149], v139 offset:1024
	ds_read_b128 v[150:153], v139 offset:2048
	ds_read_b128 v[154:157], v139 offset:3072
	ds_read_b128 v[158:161], v140
	ds_read_b128 v[162:165], v140 offset:1024
	ds_read_b128 v[166:169], v140 offset:2048
	ds_read_b128 v[170:173], v140 offset:3072
	s_add_i32 s0, s45, s10
	s_add_u32 s0, s4, s0
	s_addc_u32 s1, s5, 0
	s_add_i32 m0, s23, 0xc000
	s_add_i32 s61, s23, 0xe000
	s_add_i32 s66, s10, 0xfff80080
	s_cmp_eq_u32 s18, 28
	s_cselect_b32 s19, s41, s45
	s_cselect_b32 s60, s40, s44
	v_lshl_add_u64 v[206:207], s[0:1], 0, v[128:129]
	ds_read_b128 v[174:177], v141
	ds_read_b128 v[178:181], v141 offset:1024
	ds_read_b128 v[182:185], v141 offset:2048
	ds_read_b128 v[186:189], v141 offset:3072
	ds_read_b128 v[190:193], v141 offset:4096
	ds_read_b128 v[194:197], v141 offset:5120
	ds_read_b128 v[198:201], v141 offset:6144
	ds_read_b128 v[202:205], v141 offset:7168
	global_load_lds_dwordx4 v[206:207], off
	v_lshl_add_u64 v[206:207], s[0:1], 0, v[130:131]
	s_mov_b32 m0, s61
	s_nop 0
	global_load_lds_dwordx4 v[206:207], off
	s_waitcnt vmcnt(8)
	s_waitcnt lgkmcnt(0)
	s_barrier
	v_mfma_f32_16x16x32_bf16 v[124:127], v[142:145], v[174:177], v[124:127]
	v_mfma_f32_16x16x32_bf16 v[120:123], v[150:153], v[174:177], v[120:123]
	v_mfma_f32_16x16x32_bf16 v[116:119], v[142:145], v[182:185], v[116:119]
	v_mfma_f32_16x16x32_bf16 v[112:115], v[150:153], v[182:185], v[112:115]
	v_mfma_f32_16x16x32_bf16 v[108:111], v[142:145], v[190:193], v[108:111]
	v_mfma_f32_16x16x32_bf16 v[100:103], v[150:153], v[190:193], v[100:103]
	v_mfma_f32_16x16x32_bf16 v[92:95], v[142:145], v[198:201], v[92:95]
	v_mfma_f32_16x16x32_bf16 v[84:87], v[150:153], v[198:201], v[84:87]
	v_mfma_f32_16x16x32_bf16 v[124:127], v[146:149], v[178:181], v[124:127]
	v_mfma_f32_16x16x32_bf16 v[120:123], v[154:157], v[178:181], v[120:123]
	v_mfma_f32_16x16x32_bf16 v[116:119], v[146:149], v[186:189], v[116:119]
	v_mfma_f32_16x16x32_bf16 v[112:115], v[154:157], v[186:189], v[112:115]
	v_mfma_f32_16x16x32_bf16 v[108:111], v[146:149], v[194:197], v[108:111]
	v_mfma_f32_16x16x32_bf16 v[100:103], v[154:157], v[194:197], v[100:103]
	v_mfma_f32_16x16x32_bf16 v[92:95], v[146:149], v[202:205], v[92:95]
	v_mfma_f32_16x16x32_bf16 v[84:87], v[154:157], v[202:205], v[84:87]
	v_mfma_f32_16x16x32_bf16 v[104:107], v[158:161], v[174:177], v[104:107]
	v_mfma_f32_16x16x32_bf16 v[96:99], v[166:169], v[174:177], v[96:99]
	v_mfma_f32_16x16x32_bf16 v[88:91], v[158:161], v[182:185], v[88:91]
	v_mfma_f32_16x16x32_bf16 v[80:83], v[166:169], v[182:185], v[80:83]
	v_mfma_f32_16x16x32_bf16 v[76:79], v[158:161], v[190:193], v[76:79]
	v_mfma_f32_16x16x32_bf16 v[72:75], v[166:169], v[190:193], v[72:75]
	v_mfma_f32_16x16x32_bf16 v[68:71], v[158:161], v[198:201], v[68:71]
	v_mfma_f32_16x16x32_bf16 v[64:67], v[166:169], v[198:201], v[64:67]
	v_mfma_f32_16x16x32_bf16 v[104:107], v[162:165], v[178:181], v[104:107]
	v_mfma_f32_16x16x32_bf16 v[96:99], v[170:173], v[178:181], v[96:99]
	v_mfma_f32_16x16x32_bf16 v[88:91], v[162:165], v[186:189], v[88:91]
	v_mfma_f32_16x16x32_bf16 v[80:83], v[170:173], v[186:189], v[80:83]
	v_mfma_f32_16x16x32_bf16 v[76:79], v[162:165], v[194:197], v[76:79]
	v_mfma_f32_16x16x32_bf16 v[72:75], v[170:173], v[194:197], v[72:75]
	v_mfma_f32_16x16x32_bf16 v[68:71], v[162:165], v[202:205], v[68:71]
	v_mfma_f32_16x16x32_bf16 v[64:67], v[170:173], v[202:205], v[64:67]
	s_barrier
	s_cselect_b32 s61, 0, s66
	s_add_i32 s0, s61, s60
	s_ashr_i32 s1, s0, 31
	s_add_u32 s0, s6, s0
	s_addc_u32 s1, s7, s1
	s_add_i32 s66, s30, s27
	v_lshl_add_u64 v[206:207], s[0:1], 0, v[128:129]
	s_mov_b32 m0, s66
	ds_read_b128 v[174:177], v141 offset:16384
	ds_read_b128 v[178:181], v141 offset:17408
	ds_read_b128 v[182:185], v141 offset:18432
	ds_read_b128 v[186:189], v141 offset:19456
	ds_read_b128 v[190:193], v141 offset:20480
	ds_read_b128 v[194:197], v141 offset:21504
	ds_read_b128 v[198:201], v141 offset:22528
	ds_read_b128 v[202:205], v141 offset:23552
	global_load_lds_dwordx4 v[206:207], off
	s_add_i32 m0, s66, 0x2000
	s_add_i32 s66, s60, 0x80000
	v_lshl_add_u64 v[206:207], s[0:1], 0, v[130:131]
	s_add_i32 s0, s66, s61
	s_ashr_i32 s1, s0, 31
	s_add_u32 s0, s6, s0
	s_addc_u32 s1, s7, s1
	s_add_i32 s67, s31, s27
	global_load_lds_dwordx4 v[206:207], off
	v_lshl_add_u64 v[206:207], s[0:1], 0, v[128:129]
	s_mov_b32 m0, s67
	s_nop 0
	global_load_lds_dwordx4 v[206:207], off
	s_add_i32 m0, s67, 0x2000
	s_add_i32 s67, s61, s19
	v_lshl_add_u64 v[206:207], s[0:1], 0, v[130:131]
	s_add_u32 s0, s4, s67
	s_addc_u32 s1, s5, 0
	global_load_lds_dwordx4 v[206:207], off
	v_lshl_add_u64 v[206:207], s[0:1], 0, v[128:129]
	s_mov_b32 m0, s23
	s_nop 0
	global_load_lds_dwordx4 v[206:207], off
	v_lshl_add_u64 v[206:207], s[0:1], 0, v[130:131]
	s_mov_b32 m0, s24
	s_nop 0
	global_load_lds_dwordx4 v[206:207], off
	s_waitcnt vmcnt(8)
	s_waitcnt lgkmcnt(0)
	s_barrier
	v_mfma_f32_16x16x32_bf16 v[60:63], v[142:145], v[174:177], v[60:63]
	v_mfma_f32_16x16x32_bf16 v[56:59], v[150:153], v[174:177], v[56:59]
	v_mfma_f32_16x16x32_bf16 v[52:55], v[142:145], v[182:185], v[52:55]
	v_mfma_f32_16x16x32_bf16 v[48:51], v[150:153], v[182:185], v[48:51]
	v_mfma_f32_16x16x32_bf16 v[44:47], v[142:145], v[190:193], v[44:47]
	v_mfma_f32_16x16x32_bf16 v[36:39], v[150:153], v[190:193], v[36:39]
	v_mfma_f32_16x16x32_bf16 v[28:31], v[142:145], v[198:201], v[28:31]
	v_mfma_f32_16x16x32_bf16 v[20:23], v[150:153], v[198:201], v[20:23]
	v_mfma_f32_16x16x32_bf16 v[60:63], v[146:149], v[178:181], v[60:63]
	v_mfma_f32_16x16x32_bf16 v[56:59], v[154:157], v[178:181], v[56:59]
	v_mfma_f32_16x16x32_bf16 v[52:55], v[146:149], v[186:189], v[52:55]
	v_mfma_f32_16x16x32_bf16 v[48:51], v[154:157], v[186:189], v[48:51]
	v_mfma_f32_16x16x32_bf16 v[44:47], v[146:149], v[194:197], v[44:47]
	v_mfma_f32_16x16x32_bf16 v[36:39], v[154:157], v[194:197], v[36:39]
	v_mfma_f32_16x16x32_bf16 v[28:31], v[146:149], v[202:205], v[28:31]
	v_mfma_f32_16x16x32_bf16 v[20:23], v[154:157], v[202:205], v[20:23]
	v_mfma_f32_16x16x32_bf16 v[40:43], v[158:161], v[174:177], v[40:43]
	v_mfma_f32_16x16x32_bf16 v[32:35], v[166:169], v[174:177], v[32:35]
	v_mfma_f32_16x16x32_bf16 v[24:27], v[158:161], v[182:185], v[24:27]
	v_mfma_f32_16x16x32_bf16 v[16:19], v[166:169], v[182:185], v[16:19]
	v_mfma_f32_16x16x32_bf16 v[12:15], v[158:161], v[190:193], v[12:15]
	v_mfma_f32_16x16x32_bf16 v[8:11], v[166:169], v[190:193], v[8:11]
	v_mfma_f32_16x16x32_bf16 v[4:7], v[158:161], v[198:201], v[4:7]
	v_mfma_f32_16x16x32_bf16 v[0:3], v[166:169], v[198:201], v[0:3]
	v_mfma_f32_16x16x32_bf16 v[40:43], v[162:165], v[178:181], v[40:43]
	v_mfma_f32_16x16x32_bf16 v[32:35], v[170:173], v[178:181], v[32:35]
	v_mfma_f32_16x16x32_bf16 v[24:27], v[162:165], v[186:189], v[24:27]
	v_mfma_f32_16x16x32_bf16 v[16:19], v[170:173], v[186:189], v[16:19]
	v_mfma_f32_16x16x32_bf16 v[12:15], v[162:165], v[194:197], v[12:15]
	v_mfma_f32_16x16x32_bf16 v[8:11], v[170:173], v[194:197], v[8:11]
	v_mfma_f32_16x16x32_bf16 v[4:7], v[162:165], v[202:205], v[4:7]
	v_mfma_f32_16x16x32_bf16 v[0:3], v[170:173], v[202:205], v[0:3]
	s_barrier
	s_add_i32 s68, 0, 0x18000
	s_add_i32 s69, 0, 0x1c000
	v_add_u32_e32 v154, s68, v138
	v_add_u32_e32 v170, s69, v138
	ds_read_b128 v[142:145], v154
	ds_read_b128 v[146:149], v154 offset:1024
	ds_read_b128 v[150:153], v154 offset:2048
	ds_read_b128 v[154:157], v154 offset:3072
	ds_read_b128 v[158:161], v170
	ds_read_b128 v[162:165], v170 offset:1024
	ds_read_b128 v[166:169], v170 offset:2048
	ds_read_b128 v[170:173], v170 offset:3072
	s_add_i32 s67, s67, 0x80000
	s_add_u32 s0, s4, s67
	s_addc_u32 s1, s5, 0
	s_mov_b32 m0, s25
	v_lshl_add_u64 v[206:207], s[0:1], 0, v[128:129]
	ds_read_b128 v[174:177], v141 offset:32768
	ds_read_b128 v[178:181], v141 offset:33792
	ds_read_b128 v[182:185], v141 offset:34816
	ds_read_b128 v[186:189], v141 offset:35840
	ds_read_b128 v[190:193], v141 offset:36864
	ds_read_b128 v[194:197], v141 offset:37888
	ds_read_b128 v[198:201], v141 offset:38912
	ds_read_b128 v[202:205], v141 offset:39936
	global_load_lds_dwordx4 v[206:207], off
	v_lshl_add_u64 v[206:207], s[0:1], 0, v[130:131]
	s_mov_b32 m0, s33
	s_nop 0
	global_load_lds_dwordx4 v[206:207], off
	s_waitcnt vmcnt(8)
	s_waitcnt lgkmcnt(0)
	s_barrier
	v_mfma_f32_16x16x32_bf16 v[124:127], v[142:145], v[174:177], v[124:127]
	v_mfma_f32_16x16x32_bf16 v[120:123], v[150:153], v[174:177], v[120:123]
	v_mfma_f32_16x16x32_bf16 v[116:119], v[142:145], v[182:185], v[116:119]
	v_mfma_f32_16x16x32_bf16 v[112:115], v[150:153], v[182:185], v[112:115]
	v_mfma_f32_16x16x32_bf16 v[108:111], v[142:145], v[190:193], v[108:111]
	v_mfma_f32_16x16x32_bf16 v[100:103], v[150:153], v[190:193], v[100:103]
	v_mfma_f32_16x16x32_bf16 v[92:95], v[142:145], v[198:201], v[92:95]
	v_mfma_f32_16x16x32_bf16 v[84:87], v[150:153], v[198:201], v[84:87]
	v_mfma_f32_16x16x32_bf16 v[124:127], v[146:149], v[178:181], v[124:127]
	v_mfma_f32_16x16x32_bf16 v[120:123], v[154:157], v[178:181], v[120:123]
	v_mfma_f32_16x16x32_bf16 v[116:119], v[146:149], v[186:189], v[116:119]
	v_mfma_f32_16x16x32_bf16 v[112:115], v[154:157], v[186:189], v[112:115]
	v_mfma_f32_16x16x32_bf16 v[108:111], v[146:149], v[194:197], v[108:111]
	v_mfma_f32_16x16x32_bf16 v[100:103], v[154:157], v[194:197], v[100:103]
	v_mfma_f32_16x16x32_bf16 v[92:95], v[146:149], v[202:205], v[92:95]
	v_mfma_f32_16x16x32_bf16 v[84:87], v[154:157], v[202:205], v[84:87]
	v_mfma_f32_16x16x32_bf16 v[104:107], v[158:161], v[174:177], v[104:107]
	v_mfma_f32_16x16x32_bf16 v[96:99], v[166:169], v[174:177], v[96:99]
	v_mfma_f32_16x16x32_bf16 v[88:91], v[158:161], v[182:185], v[88:91]
	v_mfma_f32_16x16x32_bf16 v[80:83], v[166:169], v[182:185], v[80:83]
	v_mfma_f32_16x16x32_bf16 v[76:79], v[158:161], v[190:193], v[76:79]
	v_mfma_f32_16x16x32_bf16 v[72:75], v[166:169], v[190:193], v[72:75]
	v_mfma_f32_16x16x32_bf16 v[68:71], v[158:161], v[198:201], v[68:71]
	v_mfma_f32_16x16x32_bf16 v[64:67], v[166:169], v[198:201], v[64:67]
	v_mfma_f32_16x16x32_bf16 v[104:107], v[162:165], v[178:181], v[104:107]
	v_mfma_f32_16x16x32_bf16 v[96:99], v[170:173], v[178:181], v[96:99]
	v_mfma_f32_16x16x32_bf16 v[88:91], v[162:165], v[186:189], v[88:91]
	v_mfma_f32_16x16x32_bf16 v[80:83], v[170:173], v[186:189], v[80:83]
	v_mfma_f32_16x16x32_bf16 v[76:79], v[162:165], v[194:197], v[76:79]
	v_mfma_f32_16x16x32_bf16 v[72:75], v[170:173], v[194:197], v[72:75]
	v_mfma_f32_16x16x32_bf16 v[68:71], v[162:165], v[202:205], v[68:71]
	v_mfma_f32_16x16x32_bf16 v[64:67], v[170:173], v[202:205], v[64:67]
	s_barrier
; template <class Epi, class Sched, class Hook = NoHook>
; __device__ __forceinline__ void gemm_phase_w(LAS unsigned char* lds, const Sched& S, const Epi& E, int wave_id, const Hook& HK = Hook()) {
;     ...
;         if constexpr (!SEG2) {
;             for (int tt = 0; tt < nt; tt += 2) {
;                 if constexpr (GATHER) { if (tt == nt - 2) {
;                     if (has_next) { gnxt_00 = S.grow_l(nxt, lds, nbuf, R0) + (unsigned)(C0 * 2); gnxt_01 = S.grow_l(nxt, lds, nbuf, R1) + (unsigned)(C1 * 2); gnxt_10 = S.grow_l(nxt, lds, nbuf, 128 + R0) + (unsigned)(C0 * 2); gnxt_11 = S.grow_l(nxt, lds, nbuf, 128 + R1) + (unsigned)(C1 * 2); }
;                     else { gnxt_00 = gcur_00; gnxt_01 = gcur_01; gnxt_10 = gcur_10; gnxt_11 = gcur_11; } } }
;                 PG_TRIP(tt, false, false, false);
;             }
	s_bitset1_b32 s61, 7
	s_add_i32 s0, s61, s60
	s_ashr_i32 s1, s0, 31
	s_add_u32 s0, s6, s0
	s_addc_u32 s1, s7, s1
	s_add_i32 s60, s68, s27
	v_lshl_add_u64 v[206:207], s[0:1], 0, v[128:129]
	s_mov_b32 m0, s60
	ds_read_b128 v[174:177], v141 offset:49152
	ds_read_b128 v[178:181], v141 offset:50176
	ds_read_b128 v[182:185], v141 offset:51200
	ds_read_b128 v[186:189], v141 offset:52224
	ds_read_b128 v[190:193], v141 offset:53248
	ds_read_b128 v[194:197], v141 offset:54272
	ds_read_b128 v[198:201], v141 offset:55296
	ds_read_b128 v[202:205], v141 offset:56320
	global_load_lds_dwordx4 v[206:207], off
	v_lshl_add_u64 v[206:207], s[0:1], 0, v[130:131]
	s_add_i32 s0, s61, s66
	s_add_i32 m0, s60, 0x2000
	s_ashr_i32 s1, s0, 31
	s_add_u32 s0, s6, s0
	s_addc_u32 s1, s7, s1
	s_add_i32 s60, s69, s27
	global_load_lds_dwordx4 v[206:207], off
	v_lshl_add_u64 v[206:207], s[0:1], 0, v[128:129]
	s_mov_b32 m0, s60
	s_add_i32 s61, s61, s19
	global_load_lds_dwordx4 v[206:207], off
	s_add_i32 m0, s60, 0x2000
	v_lshl_add_u64 v[206:207], s[0:1], 0, v[130:131]
	s_add_u32 s0, s4, s61
	s_addc_u32 s1, s5, 0
	global_load_lds_dwordx4 v[206:207], off
	v_lshl_add_u64 v[206:207], s[0:1], 0, v[128:129]
	s_mov_b32 m0, s34
	s_nop 0
	global_load_lds_dwordx4 v[206:207], off
	v_lshl_add_u64 v[206:207], s[0:1], 0, v[130:131]
	s_mov_b32 m0, s35
	s_nop 0
	global_load_lds_dwordx4 v[206:207], off
	s_waitcnt vmcnt(8)
	s_waitcnt lgkmcnt(0)
	s_barrier
	v_mfma_f32_16x16x32_bf16 v[60:63], v[142:145], v[174:177], v[60:63]
	v_mfma_f32_16x16x32_bf16 v[56:59], v[150:153], v[174:177], v[56:59]
	v_mfma_f32_16x16x32_bf16 v[52:55], v[142:145], v[182:185], v[52:55]
	v_mfma_f32_16x16x32_bf16 v[48:51], v[150:153], v[182:185], v[48:51]
	v_mfma_f32_16x16x32_bf16 v[44:47], v[142:145], v[190:193], v[44:47]
	v_mfma_f32_16x16x32_bf16 v[36:39], v[150:153], v[190:193], v[36:39]
	v_mfma_f32_16x16x32_bf16 v[28:31], v[142:145], v[198:201], v[28:31]
	v_mfma_f32_16x16x32_bf16 v[20:23], v[150:153], v[198:201], v[20:23]
	v_mfma_f32_16x16x32_bf16 v[60:63], v[146:149], v[178:181], v[60:63]
	v_mfma_f32_16x16x32_bf16 v[56:59], v[154:157], v[178:181], v[56:59]
	v_mfma_f32_16x16x32_bf16 v[52:55], v[146:149], v[186:189], v[52:55]
	v_mfma_f32_16x16x32_bf16 v[48:51], v[154:157], v[186:189], v[48:51]
	v_mfma_f32_16x16x32_bf16 v[44:47], v[146:149], v[194:197], v[44:47]
	v_mfma_f32_16x16x32_bf16 v[36:39], v[154:157], v[194:197], v[36:39]
	v_mfma_f32_16x16x32_bf16 v[28:31], v[146:149], v[202:205], v[28:31]
	v_mfma_f32_16x16x32_bf16 v[20:23], v[154:157], v[202:205], v[20:23]
	v_mfma_f32_16x16x32_bf16 v[40:43], v[158:161], v[174:177], v[40:43]
	v_mfma_f32_16x16x32_bf16 v[32:35], v[166:169], v[174:177], v[32:35]
	v_mfma_f32_16x16x32_bf16 v[24:27], v[158:161], v[182:185], v[24:27]
	v_mfma_f32_16x16x32_bf16 v[16:19], v[166:169], v[182:185], v[16:19]
	v_mfma_f32_16x16x32_bf16 v[12:15], v[158:161], v[190:193], v[12:15]
	v_mfma_f32_16x16x32_bf16 v[8:11], v[166:169], v[190:193], v[8:11]
	v_mfma_f32_16x16x32_bf16 v[4:7], v[158:161], v[198:201], v[4:7]
	v_mfma_f32_16x16x32_bf16 v[0:3], v[166:169], v[198:201], v[0:3]
	v_mfma_f32_16x16x32_bf16 v[40:43], v[162:165], v[178:181], v[40:43]
	v_mfma_f32_16x16x32_bf16 v[32:35], v[170:173], v[178:181], v[32:35]
	v_mfma_f32_16x16x32_bf16 v[24:27], v[162:165], v[186:189], v[24:27]
	v_mfma_f32_16x16x32_bf16 v[16:19], v[170:173], v[186:189], v[16:19]
	v_mfma_f32_16x16x32_bf16 v[12:15], v[162:165], v[194:197], v[12:15]
	v_mfma_f32_16x16x32_bf16 v[8:11], v[170:173], v[194:197], v[8:11]
	v_mfma_f32_16x16x32_bf16 v[4:7], v[162:165], v[202:205], v[4:7]
	v_mfma_f32_16x16x32_bf16 v[0:3], v[170:173], v[202:205], v[0:3]
	s_barrier
	s_addk_i32 s10, 0x100
	s_add_i32 s18, s18, 2
	s_cmp_gt_u32 s18, 29
	s_cbranch_scc0 .LBB0_386
	s_and_b64 vcc, exec, s[14:15]
	s_cbranch_vccz .LBB0_389
	s_barrier

.LBB0_654:
	ds_read_b128 v[116:119], v157
	ds_read_b128 v[120:123], v157 offset:1024
	ds_read_b128 v[128:131], v157 offset:2048
	ds_read_b128 v[132:135], v157 offset:3072
	ds_read_b128 v[150:153], v158
	ds_read_b128 v[160:163], v158 offset:1024
	ds_read_b128 v[164:167], v158 offset:2048
	ds_read_b128 v[168:171], v158 offset:3072
	s_add_i32 s40, s39, s18
	s_add_u32 s42, s4, s40
	s_addc_u32 s43, s5, 0
	s_add_i32 m0, s23, 0xc000
	s_add_i32 s44, s23, 0xe000
	s_add_i32 s45, s18, 0xfff80080
	s_cmp_eq_u32 s19, 28
	s_cselect_b32 s40, s35, s39
	s_cselect_b32 s41, s34, s38
	v_lshl_add_u64 v[204:205], s[42:43], 0, v[144:145]
	ds_read_b128 v[172:175], v159
	ds_read_b128 v[176:179], v159 offset:1024
	ds_read_b128 v[180:183], v159 offset:2048
	ds_read_b128 v[184:187], v159 offset:3072
	ds_read_b128 v[188:191], v159 offset:4096
	ds_read_b128 v[192:195], v159 offset:5120
	ds_read_b128 v[196:199], v159 offset:6144
	ds_read_b128 v[200:203], v159 offset:7168
	global_load_lds_dwordx4 v[204:205], off
	v_lshl_add_u64 v[204:205], s[42:43], 0, v[146:147]
	s_mov_b32 m0, s44
	s_nop 0
	global_load_lds_dwordx4 v[204:205], off
	s_waitcnt vmcnt(8)
	s_waitcnt lgkmcnt(0)
	s_barrier
	v_mfma_f32_16x16x32_bf16 v[140:143], v[116:119], v[172:175], v[140:143]
	v_mfma_f32_16x16x32_bf16 v[136:139], v[128:131], v[172:175], v[136:139]
	v_mfma_f32_16x16x32_bf16 v[112:115], v[116:119], v[180:183], v[112:115]
	v_mfma_f32_16x16x32_bf16 v[104:107], v[128:131], v[180:183], v[104:107]
	v_mfma_f32_16x16x32_bf16 v[96:99], v[116:119], v[188:191], v[96:99]
	v_mfma_f32_16x16x32_bf16 v[88:91], v[128:131], v[188:191], v[88:91]
	v_mfma_f32_16x16x32_bf16 v[80:83], v[116:119], v[196:199], v[80:83]
	v_mfma_f32_16x16x32_bf16 v[72:75], v[128:131], v[196:199], v[72:75]
	v_mfma_f32_16x16x32_bf16 v[140:143], v[120:123], v[176:179], v[140:143]
	v_mfma_f32_16x16x32_bf16 v[136:139], v[132:135], v[176:179], v[136:139]
	v_mfma_f32_16x16x32_bf16 v[112:115], v[120:123], v[184:187], v[112:115]
	v_mfma_f32_16x16x32_bf16 v[104:107], v[132:135], v[184:187], v[104:107]
	v_mfma_f32_16x16x32_bf16 v[96:99], v[120:123], v[192:195], v[96:99]
	v_mfma_f32_16x16x32_bf16 v[88:91], v[132:135], v[192:195], v[88:91]
	v_mfma_f32_16x16x32_bf16 v[80:83], v[120:123], v[200:203], v[80:83]
	v_mfma_f32_16x16x32_bf16 v[72:75], v[132:135], v[200:203], v[72:75]
	v_mfma_f32_16x16x32_bf16 v[124:127], v[150:153], v[172:175], v[124:127]
	v_mfma_f32_16x16x32_bf16 v[108:111], v[164:167], v[172:175], v[108:111]
	v_mfma_f32_16x16x32_bf16 v[100:103], v[150:153], v[180:183], v[100:103]
	v_mfma_f32_16x16x32_bf16 v[92:95], v[164:167], v[180:183], v[92:95]
	v_mfma_f32_16x16x32_bf16 v[84:87], v[150:153], v[188:191], v[84:87]
	v_mfma_f32_16x16x32_bf16 v[76:79], v[164:167], v[188:191], v[76:79]
	v_mfma_f32_16x16x32_bf16 v[68:71], v[150:153], v[196:199], v[68:71]
	v_mfma_f32_16x16x32_bf16 v[64:67], v[164:167], v[196:199], v[64:67]
	v_mfma_f32_16x16x32_bf16 v[124:127], v[160:163], v[176:179], v[124:127]
	v_mfma_f32_16x16x32_bf16 v[108:111], v[168:171], v[176:179], v[108:111]
	v_mfma_f32_16x16x32_bf16 v[100:103], v[160:163], v[184:187], v[100:103]
	v_mfma_f32_16x16x32_bf16 v[92:95], v[168:171], v[184:187], v[92:95]
	v_mfma_f32_16x16x32_bf16 v[84:87], v[160:163], v[192:195], v[84:87]
	v_mfma_f32_16x16x32_bf16 v[76:79], v[168:171], v[192:195], v[76:79]
	v_mfma_f32_16x16x32_bf16 v[68:71], v[160:163], v[200:203], v[68:71]
	v_mfma_f32_16x16x32_bf16 v[64:67], v[168:171], v[200:203], v[64:67]
	s_barrier
	s_cselect_b32 s44, 0, s45
	s_add_i32 s42, s44, s41
	s_ashr_i32 s43, s42, 31
	s_add_u32 s42, s20, s42
	s_addc_u32 s43, s21, s43
	s_add_i32 s45, s29, s22
	v_lshl_add_u64 v[204:205], s[42:43], 0, v[144:145]
	s_mov_b32 m0, s45
	ds_read_b128 v[172:175], v159 offset:16384
	ds_read_b128 v[176:179], v159 offset:17408
	ds_read_b128 v[180:183], v159 offset:18432
	ds_read_b128 v[184:187], v159 offset:19456
	ds_read_b128 v[188:191], v159 offset:20480
	ds_read_b128 v[192:195], v159 offset:21504
	ds_read_b128 v[196:199], v159 offset:22528
	ds_read_b128 v[200:203], v159 offset:23552
	global_load_lds_dwordx4 v[204:205], off
	s_add_i32 m0, s45, 0x2000
	s_add_i32 s45, s41, 0x80000
	v_lshl_add_u64 v[204:205], s[42:43], 0, v[146:147]
	s_add_i32 s42, s45, s44
	s_ashr_i32 s43, s42, 31
	s_add_u32 s42, s20, s42
	s_addc_u32 s43, s21, s43
	s_add_i32 s58, s30, s22
	global_load_lds_dwordx4 v[204:205], off
	v_lshl_add_u64 v[204:205], s[42:43], 0, v[144:145]
	s_mov_b32 m0, s58
	s_nop 0
	global_load_lds_dwordx4 v[204:205], off
	s_add_i32 m0, s58, 0x2000
	s_add_i32 s58, s44, s40
	v_lshl_add_u64 v[204:205], s[42:43], 0, v[146:147]
	s_add_u32 s42, s4, s58
	s_addc_u32 s43, s5, 0
	global_load_lds_dwordx4 v[204:205], off
	v_lshl_add_u64 v[204:205], s[42:43], 0, v[144:145]
	s_mov_b32 m0, s23
	s_nop 0
	global_load_lds_dwordx4 v[204:205], off
	v_lshl_add_u64 v[204:205], s[42:43], 0, v[146:147]
	s_mov_b32 m0, s24
	s_nop 0
	global_load_lds_dwordx4 v[204:205], off
	s_waitcnt vmcnt(8)
	s_waitcnt lgkmcnt(0)
	s_barrier
	v_mfma_f32_16x16x32_bf16 v[60:63], v[116:119], v[172:175], v[60:63]
	v_mfma_f32_16x16x32_bf16 v[56:59], v[128:131], v[172:175], v[56:59]
	v_mfma_f32_16x16x32_bf16 v[48:51], v[116:119], v[180:183], v[48:51]
	v_mfma_f32_16x16x32_bf16 v[40:43], v[128:131], v[180:183], v[40:43]
	v_mfma_f32_16x16x32_bf16 v[32:35], v[116:119], v[188:191], v[32:35]
	v_mfma_f32_16x16x32_bf16 v[24:27], v[128:131], v[188:191], v[24:27]
	v_mfma_f32_16x16x32_bf16 v[16:19], v[116:119], v[196:199], v[16:19]
	v_mfma_f32_16x16x32_bf16 v[8:11], v[128:131], v[196:199], v[8:11]
	v_mfma_f32_16x16x32_bf16 v[60:63], v[120:123], v[176:179], v[60:63]
	v_mfma_f32_16x16x32_bf16 v[56:59], v[132:135], v[176:179], v[56:59]
	v_mfma_f32_16x16x32_bf16 v[48:51], v[120:123], v[184:187], v[48:51]
	v_mfma_f32_16x16x32_bf16 v[40:43], v[132:135], v[184:187], v[40:43]
	v_mfma_f32_16x16x32_bf16 v[32:35], v[120:123], v[192:195], v[32:35]
	v_mfma_f32_16x16x32_bf16 v[24:27], v[132:135], v[192:195], v[24:27]
	v_mfma_f32_16x16x32_bf16 v[16:19], v[120:123], v[200:203], v[16:19]
	v_mfma_f32_16x16x32_bf16 v[8:11], v[132:135], v[200:203], v[8:11]
	v_mfma_f32_16x16x32_bf16 v[52:55], v[150:153], v[172:175], v[52:55]
	v_mfma_f32_16x16x32_bf16 v[44:47], v[164:167], v[172:175], v[44:47]
	v_mfma_f32_16x16x32_bf16 v[36:39], v[150:153], v[180:183], v[36:39]
	v_mfma_f32_16x16x32_bf16 v[28:31], v[164:167], v[180:183], v[28:31]
	v_mfma_f32_16x16x32_bf16 v[20:23], v[150:153], v[188:191], v[20:23]
	v_mfma_f32_16x16x32_bf16 v[12:15], v[164:167], v[188:191], v[12:15]
	v_mfma_f32_16x16x32_bf16 v[4:7], v[150:153], v[196:199], v[4:7]
	v_mfma_f32_16x16x32_bf16 v[0:3], v[164:167], v[196:199], v[0:3]
	v_mfma_f32_16x16x32_bf16 v[52:55], v[160:163], v[176:179], v[52:55]
	v_mfma_f32_16x16x32_bf16 v[44:47], v[168:171], v[176:179], v[44:47]
	v_mfma_f32_16x16x32_bf16 v[36:39], v[160:163], v[184:187], v[36:39]
	v_mfma_f32_16x16x32_bf16 v[28:31], v[168:171], v[184:187], v[28:31]
	v_mfma_f32_16x16x32_bf16 v[20:23], v[160:163], v[192:195], v[20:23]
	v_mfma_f32_16x16x32_bf16 v[12:15], v[168:171], v[192:195], v[12:15]
	v_mfma_f32_16x16x32_bf16 v[4:7], v[160:163], v[200:203], v[4:7]
	v_mfma_f32_16x16x32_bf16 v[0:3], v[168:171], v[200:203], v[0:3]
	s_barrier
	s_add_i32 s59, 0, 0x18000
	s_add_i32 s60, 0, 0x1c000
	v_add_u32_e32 v132, s59, v155
	v_add_u32_e32 v168, s60, v155
	ds_read_b128 v[116:119], v132
	ds_read_b128 v[120:123], v132 offset:1024
	ds_read_b128 v[128:131], v132 offset:2048
	ds_read_b128 v[132:135], v132 offset:3072
	ds_read_b128 v[150:153], v168
	ds_read_b128 v[160:163], v168 offset:1024
	ds_read_b128 v[164:167], v168 offset:2048
	ds_read_b128 v[168:171], v168 offset:3072
	s_add_i32 s58, s58, 0x80000
	s_add_u32 s42, s4, s58
	s_addc_u32 s43, s5, 0
	s_mov_b32 m0, s25
	v_lshl_add_u64 v[204:205], s[42:43], 0, v[144:145]
	ds_read_b128 v[172:175], v159 offset:32768
	ds_read_b128 v[176:179], v159 offset:33792
	ds_read_b128 v[180:183], v159 offset:34816
	ds_read_b128 v[184:187], v159 offset:35840
	ds_read_b128 v[188:191], v159 offset:36864
	ds_read_b128 v[192:195], v159 offset:37888
	ds_read_b128 v[196:199], v159 offset:38912
	ds_read_b128 v[200:203], v159 offset:39936
	global_load_lds_dwordx4 v[204:205], off
	v_lshl_add_u64 v[204:205], s[42:43], 0, v[146:147]
	s_mov_b32 m0, s26
	s_nop 0
	global_load_lds_dwordx4 v[204:205], off
	s_waitcnt vmcnt(8)
	s_waitcnt lgkmcnt(0)
	s_barrier
	v_mfma_f32_16x16x32_bf16 v[140:143], v[116:119], v[172:175], v[140:143]
	v_mfma_f32_16x16x32_bf16 v[136:139], v[128:131], v[172:175], v[136:139]
	v_mfma_f32_16x16x32_bf16 v[112:115], v[116:119], v[180:183], v[112:115]
	v_mfma_f32_16x16x32_bf16 v[104:107], v[128:131], v[180:183], v[104:107]
	v_mfma_f32_16x16x32_bf16 v[96:99], v[116:119], v[188:191], v[96:99]
	v_mfma_f32_16x16x32_bf16 v[88:91], v[128:131], v[188:191], v[88:91]
	v_mfma_f32_16x16x32_bf16 v[80:83], v[116:119], v[196:199], v[80:83]
	v_mfma_f32_16x16x32_bf16 v[72:75], v[128:131], v[196:199], v[72:75]
	v_mfma_f32_16x16x32_bf16 v[140:143], v[120:123], v[176:179], v[140:143]
	v_mfma_f32_16x16x32_bf16 v[136:139], v[132:135], v[176:179], v[136:139]
	v_mfma_f32_16x16x32_bf16 v[112:115], v[120:123], v[184:187], v[112:115]
	v_mfma_f32_16x16x32_bf16 v[104:107], v[132:135], v[184:187], v[104:107]
	v_mfma_f32_16x16x32_bf16 v[96:99], v[120:123], v[192:195], v[96:99]
	v_mfma_f32_16x16x32_bf16 v[88:91], v[132:135], v[192:195], v[88:91]
	v_mfma_f32_16x16x32_bf16 v[80:83], v[120:123], v[200:203], v[80:83]
	v_mfma_f32_16x16x32_bf16 v[72:75], v[132:135], v[200:203], v[72:75]
	v_mfma_f32_16x16x32_bf16 v[124:127], v[150:153], v[172:175], v[124:127]
	v_mfma_f32_16x16x32_bf16 v[108:111], v[164:167], v[172:175], v[108:111]
	v_mfma_f32_16x16x32_bf16 v[100:103], v[150:153], v[180:183], v[100:103]
	v_mfma_f32_16x16x32_bf16 v[92:95], v[164:167], v[180:183], v[92:95]
	v_mfma_f32_16x16x32_bf16 v[84:87], v[150:153], v[188:191], v[84:87]
	v_mfma_f32_16x16x32_bf16 v[76:79], v[164:167], v[188:191], v[76:79]
	v_mfma_f32_16x16x32_bf16 v[68:71], v[150:153], v[196:199], v[68:71]
	v_mfma_f32_16x16x32_bf16 v[64:67], v[164:167], v[196:199], v[64:67]
	v_mfma_f32_16x16x32_bf16 v[124:127], v[160:163], v[176:179], v[124:127]
	v_mfma_f32_16x16x32_bf16 v[108:111], v[168:171], v[176:179], v[108:111]
	v_mfma_f32_16x16x32_bf16 v[100:103], v[160:163], v[184:187], v[100:103]
	v_mfma_f32_16x16x32_bf16 v[92:95], v[168:171], v[184:187], v[92:95]
	v_mfma_f32_16x16x32_bf16 v[84:87], v[160:163], v[192:195], v[84:87]
	v_mfma_f32_16x16x32_bf16 v[76:79], v[168:171], v[192:195], v[76:79]
	v_mfma_f32_16x16x32_bf16 v[68:71], v[160:163], v[200:203], v[68:71]
	v_mfma_f32_16x16x32_bf16 v[64:67], v[168:171], v[200:203], v[64:67]
	s_barrier
; template <class Epi, class Sched, class Hook = NoHook>
; __device__ __forceinline__ void gemm_phase_w(LAS unsigned char* lds, const Sched& S, const Epi& E, int wave_id, const Hook& HK = Hook()) {
;     ...
;         if constexpr (!SEG2) {
;             for (int tt = 0; tt < nt; tt += 2) {
;                 if constexpr (GATHER) { if (tt == nt - 2) {
;                     if (has_next) { gnxt_00 = S.grow_l(nxt, lds, nbuf, R0) + (unsigned)(C0 * 2); gnxt_01 = S.grow_l(nxt, lds, nbuf, R1) + (unsigned)(C1 * 2); gnxt_10 = S.grow_l(nxt, lds, nbuf, 128 + R0) + (unsigned)(C0 * 2); gnxt_11 = S.grow_l(nxt, lds, nbuf, 128 + R1) + (unsigned)(C1 * 2); }
;                     else { gnxt_00 = gcur_00; gnxt_01 = gcur_01; gnxt_10 = gcur_10; gnxt_11 = gcur_11; } } }
;                 PG_TRIP(tt, false, false, false);
;             }
	s_bitset1_b32 s44, 7
	s_add_i32 s41, s44, s41
	s_ashr_i32 s43, s41, 31
	s_add_u32 s42, s20, s41
	s_addc_u32 s43, s21, s43
	s_add_i32 s41, s59, s22
	v_lshl_add_u64 v[204:205], s[42:43], 0, v[144:145]
	s_mov_b32 m0, s41
	ds_read_b128 v[172:175], v159 offset:49152
	ds_read_b128 v[176:179], v159 offset:50176
	ds_read_b128 v[180:183], v159 offset:51200
	ds_read_b128 v[184:187], v159 offset:52224
	ds_read_b128 v[188:191], v159 offset:53248
	ds_read_b128 v[192:195], v159 offset:54272
	ds_read_b128 v[196:199], v159 offset:55296
	ds_read_b128 v[200:203], v159 offset:56320
	global_load_lds_dwordx4 v[204:205], off
	s_add_i32 m0, s41, 0x2000
	s_add_i32 s41, s44, s45
	v_lshl_add_u64 v[204:205], s[42:43], 0, v[146:147]
	s_ashr_i32 s43, s41, 31
	s_add_u32 s42, s20, s41
	s_addc_u32 s43, s21, s43
	s_add_i32 s41, s60, s22
	global_load_lds_dwordx4 v[204:205], off
	v_lshl_add_u64 v[204:205], s[42:43], 0, v[144:145]
	s_mov_b32 m0, s41
	s_add_i32 s44, s44, s40
	global_load_lds_dwordx4 v[204:205], off
	s_add_i32 m0, s41, 0x2000
	s_add_u32 s40, s4, s44
	v_lshl_add_u64 v[204:205], s[42:43], 0, v[146:147]
	s_addc_u32 s41, s5, 0
	global_load_lds_dwordx4 v[204:205], off
	v_lshl_add_u64 v[204:205], s[40:41], 0, v[144:145]
	s_mov_b32 m0, s28
	s_nop 0
	global_load_lds_dwordx4 v[204:205], off
	v_lshl_add_u64 v[204:205], s[40:41], 0, v[146:147]
	s_mov_b32 m0, s6
	s_nop 0
	global_load_lds_dwordx4 v[204:205], off
	s_waitcnt vmcnt(8)
	s_waitcnt lgkmcnt(0)
	s_barrier
	v_mfma_f32_16x16x32_bf16 v[60:63], v[116:119], v[172:175], v[60:63]
	v_mfma_f32_16x16x32_bf16 v[56:59], v[128:131], v[172:175], v[56:59]
	v_mfma_f32_16x16x32_bf16 v[48:51], v[116:119], v[180:183], v[48:51]
	v_mfma_f32_16x16x32_bf16 v[40:43], v[128:131], v[180:183], v[40:43]
	v_mfma_f32_16x16x32_bf16 v[32:35], v[116:119], v[188:191], v[32:35]
	v_mfma_f32_16x16x32_bf16 v[24:27], v[128:131], v[188:191], v[24:27]
	v_mfma_f32_16x16x32_bf16 v[16:19], v[116:119], v[196:199], v[16:19]
	v_mfma_f32_16x16x32_bf16 v[8:11], v[128:131], v[196:199], v[8:11]
	v_mfma_f32_16x16x32_bf16 v[60:63], v[120:123], v[176:179], v[60:63]
	v_mfma_f32_16x16x32_bf16 v[56:59], v[132:135], v[176:179], v[56:59]
	v_mfma_f32_16x16x32_bf16 v[48:51], v[120:123], v[184:187], v[48:51]
	v_mfma_f32_16x16x32_bf16 v[40:43], v[132:135], v[184:187], v[40:43]
	v_mfma_f32_16x16x32_bf16 v[32:35], v[120:123], v[192:195], v[32:35]
	v_mfma_f32_16x16x32_bf16 v[24:27], v[132:135], v[192:195], v[24:27]
	v_mfma_f32_16x16x32_bf16 v[16:19], v[120:123], v[200:203], v[16:19]
	v_mfma_f32_16x16x32_bf16 v[8:11], v[132:135], v[200:203], v[8:11]
	v_mfma_f32_16x16x32_bf16 v[52:55], v[150:153], v[172:175], v[52:55]
	v_mfma_f32_16x16x32_bf16 v[44:47], v[164:167], v[172:175], v[44:47]
	v_mfma_f32_16x16x32_bf16 v[36:39], v[150:153], v[180:183], v[36:39]
	v_mfma_f32_16x16x32_bf16 v[28:31], v[164:167], v[180:183], v[28:31]
	v_mfma_f32_16x16x32_bf16 v[20:23], v[150:153], v[188:191], v[20:23]
	v_mfma_f32_16x16x32_bf16 v[12:15], v[164:167], v[188:191], v[12:15]
	v_mfma_f32_16x16x32_bf16 v[4:7], v[150:153], v[196:199], v[4:7]
	v_mfma_f32_16x16x32_bf16 v[0:3], v[164:167], v[196:199], v[0:3]
	v_mfma_f32_16x16x32_bf16 v[52:55], v[160:163], v[176:179], v[52:55]
	v_mfma_f32_16x16x32_bf16 v[44:47], v[168:171], v[176:179], v[44:47]
	v_mfma_f32_16x16x32_bf16 v[36:39], v[160:163], v[184:187], v[36:39]
	v_mfma_f32_16x16x32_bf16 v[28:31], v[168:171], v[184:187], v[28:31]
	v_mfma_f32_16x16x32_bf16 v[20:23], v[160:163], v[192:195], v[20:23]
	v_mfma_f32_16x16x32_bf16 v[12:15], v[168:171], v[192:195], v[12:15]
	v_mfma_f32_16x16x32_bf16 v[4:7], v[160:163], v[200:203], v[4:7]
	v_mfma_f32_16x16x32_bf16 v[0:3], v[168:171], v[200:203], v[0:3]
	s_barrier
	s_addk_i32 s18, 0x100
	s_add_i32 s19, s19, 2
	s_cmp_gt_u32 s19, 29
	s_cbranch_scc0 .LBB0_654
	s_and_b64 vcc, exec, s[14:15]
	s_cbranch_vccz .LBB0_657
	s_barrier

.LBB0_827:
	v_add_u32_e32 v147, s73, v166
	ds_read_b128 v[186:189], v147
	ds_read_b128 v[190:193], v147 offset:1024
	ds_read_b128 v[194:197], v147 offset:2048
	ds_read_b128 v[198:201], v147 offset:3072
	v_add_u32_e32 v147, s74, v166
	ds_read_b128 v[202:205], v147
	ds_read_b128 v[206:209], v147 offset:1024
	ds_read_b128 v[210:213], v147 offset:2048
	ds_read_b128 v[214:217], v147 offset:3072
	v_lshl_add_u64 v[250:251], s[38:39], 0, v[130:131]
	s_add_i32 m0, s62, 0xc000
	ds_read_b128 v[218:221], v182
	ds_read_b128 v[222:225], v182 offset:1024
	ds_read_b128 v[226:229], v182 offset:2048
	ds_read_b128 v[230:233], v182 offset:3072
	ds_read_b128 v[234:237], v182 offset:4096
	ds_read_b128 v[238:241], v182 offset:5120
	ds_read_b128 v[242:245], v182 offset:6144
	ds_read_b128 v[246:249], v182 offset:7168
	global_load_lds_dwordx4 v[250:251], off
	v_lshl_add_u64 v[250:251], s[38:39], 0, v[132:133]
	s_add_i32 m0, s62, 0xe000
	s_nop 0
	global_load_lds_dwordx4 v[250:251], off
	s_waitcnt vmcnt(8)
	s_waitcnt lgkmcnt(0)
	s_barrier
	v_mfma_f32_16x16x32_bf16 v[124:127], v[186:189], v[218:221], v[124:127]
	v_mfma_f32_16x16x32_bf16 v[120:123], v[194:197], v[218:221], v[120:123]
	v_mfma_f32_16x16x32_bf16 v[108:111], v[186:189], v[226:229], v[108:111]
	v_mfma_f32_16x16x32_bf16 v[104:107], v[194:197], v[226:229], v[104:107]
	v_mfma_f32_16x16x32_bf16 v[92:95], v[186:189], v[234:237], v[92:95]
	v_mfma_f32_16x16x32_bf16 v[88:91], v[194:197], v[234:237], v[88:91]
	v_mfma_f32_16x16x32_bf16 v[76:79], v[186:189], v[242:245], v[76:79]
	v_mfma_f32_16x16x32_bf16 v[72:75], v[194:197], v[242:245], v[72:75]
	v_mfma_f32_16x16x32_bf16 v[124:127], v[190:193], v[222:225], v[124:127]
	v_mfma_f32_16x16x32_bf16 v[120:123], v[198:201], v[222:225], v[120:123]
	v_mfma_f32_16x16x32_bf16 v[108:111], v[190:193], v[230:233], v[108:111]
	v_mfma_f32_16x16x32_bf16 v[104:107], v[198:201], v[230:233], v[104:107]
	v_mfma_f32_16x16x32_bf16 v[92:95], v[190:193], v[238:241], v[92:95]
	v_mfma_f32_16x16x32_bf16 v[88:91], v[198:201], v[238:241], v[88:91]
	v_mfma_f32_16x16x32_bf16 v[76:79], v[190:193], v[246:249], v[76:79]
	v_mfma_f32_16x16x32_bf16 v[72:75], v[198:201], v[246:249], v[72:75]
	v_mfma_f32_16x16x32_bf16 v[116:119], v[202:205], v[218:221], v[116:119]
	v_mfma_f32_16x16x32_bf16 v[112:115], v[210:213], v[218:221], v[112:115]
	v_mfma_f32_16x16x32_bf16 v[100:103], v[202:205], v[226:229], v[100:103]
	v_mfma_f32_16x16x32_bf16 v[96:99], v[210:213], v[226:229], v[96:99]
	v_mfma_f32_16x16x32_bf16 v[84:87], v[202:205], v[234:237], v[84:87]
	v_mfma_f32_16x16x32_bf16 v[80:83], v[210:213], v[234:237], v[80:83]
	v_mfma_f32_16x16x32_bf16 v[68:71], v[202:205], v[242:245], v[68:71]
	v_mfma_f32_16x16x32_bf16 v[64:67], v[210:213], v[242:245], v[64:67]
	v_mfma_f32_16x16x32_bf16 v[116:119], v[206:209], v[222:225], v[116:119]
	v_mfma_f32_16x16x32_bf16 v[112:115], v[214:217], v[222:225], v[112:115]
	v_mfma_f32_16x16x32_bf16 v[100:103], v[206:209], v[230:233], v[100:103]
	v_mfma_f32_16x16x32_bf16 v[96:99], v[214:217], v[230:233], v[96:99]
	v_mfma_f32_16x16x32_bf16 v[84:87], v[206:209], v[238:241], v[84:87]
	v_mfma_f32_16x16x32_bf16 v[80:83], v[214:217], v[238:241], v[80:83]
	v_mfma_f32_16x16x32_bf16 v[68:71], v[206:209], v[246:249], v[68:71]
	v_mfma_f32_16x16x32_bf16 v[64:67], v[214:217], v[246:249], v[64:67]
	s_barrier
	s_and_b64 s[40:41], s[40:41], exec
	s_cselect_b32 s22, 0, s97
	s_add_i32 s48, vcc_lo, s22
	s_ashr_i32 s41, s48, 31
	s_add_u32 s40, s16, s48
	s_addc_u32 s41, s17, s41
	s_add_i32 s49, s73, s44
	v_lshl_add_u64 v[250:251], s[40:41], 0, v[136:137]
	s_mov_b32 m0, s49
	s_add_i32 s48, s48, 0x80000
	ds_read_b128 v[218:221], v182 offset:16384
	ds_read_b128 v[222:225], v182 offset:17408
	ds_read_b128 v[226:229], v182 offset:18432
	ds_read_b128 v[230:233], v182 offset:19456
	ds_read_b128 v[234:237], v182 offset:20480
	ds_read_b128 v[238:241], v182 offset:21504
	ds_read_b128 v[242:245], v182 offset:22528
	ds_read_b128 v[246:249], v182 offset:23552
	global_load_lds_dwordx4 v[250:251], off
	v_lshl_add_u64 v[250:251], s[40:41], 0, v[138:139]
	s_add_i32 m0, s49, 0x2000
	s_ashr_i32 s41, s48, 31
	s_add_u32 s40, s16, s48
	s_addc_u32 s41, s17, s41
	s_add_i32 s48, s74, s44
	global_load_lds_dwordx4 v[250:251], off
	v_lshl_add_u64 v[250:251], s[40:41], 0, v[136:137]
	s_mov_b32 m0, s48
	v_mov_b32_e32 v147, v141
	global_load_lds_dwordx4 v[250:251], off
	s_add_i32 m0, s48, 0x2000
	v_lshl_add_u64 v[250:251], s[40:41], 0, v[138:139]
	s_add_u32 s40, s14, s22
	global_load_lds_dwordx4 v[250:251], off
	s_addc_u32 s41, s15, 0
	s_mov_b32 m0, s62
	s_nop 0
	global_load_lds_dwordx4 v140, s[40:41]
	s_mov_b32 m0, s63
	s_nop 0
	global_load_lds_dwordx4 v146, s[40:41]
	s_waitcnt vmcnt(8)
	s_waitcnt lgkmcnt(0)
	s_barrier
	v_mfma_f32_16x16x32_bf16 v[60:63], v[186:189], v[218:221], v[60:63]
	v_mfma_f32_16x16x32_bf16 v[56:59], v[194:197], v[218:221], v[56:59]
	v_mfma_f32_16x16x32_bf16 v[44:47], v[186:189], v[226:229], v[44:47]
	v_mfma_f32_16x16x32_bf16 v[40:43], v[194:197], v[226:229], v[40:43]
	v_mfma_f32_16x16x32_bf16 v[28:31], v[186:189], v[234:237], v[28:31]
	v_mfma_f32_16x16x32_bf16 v[24:27], v[194:197], v[234:237], v[24:27]
	v_mfma_f32_16x16x32_bf16 v[12:15], v[186:189], v[242:245], v[12:15]
	v_mfma_f32_16x16x32_bf16 v[8:11], v[194:197], v[242:245], v[8:11]
	v_mfma_f32_16x16x32_bf16 v[60:63], v[190:193], v[222:225], v[60:63]
	v_mfma_f32_16x16x32_bf16 v[56:59], v[198:201], v[222:225], v[56:59]
	v_mfma_f32_16x16x32_bf16 v[44:47], v[190:193], v[230:233], v[44:47]
	v_mfma_f32_16x16x32_bf16 v[40:43], v[198:201], v[230:233], v[40:43]
	v_mfma_f32_16x16x32_bf16 v[28:31], v[190:193], v[238:241], v[28:31]
	v_mfma_f32_16x16x32_bf16 v[24:27], v[198:201], v[238:241], v[24:27]
	v_mfma_f32_16x16x32_bf16 v[12:15], v[190:193], v[246:249], v[12:15]
	v_mfma_f32_16x16x32_bf16 v[8:11], v[198:201], v[246:249], v[8:11]
	v_mfma_f32_16x16x32_bf16 v[52:55], v[202:205], v[218:221], v[52:55]
	v_mfma_f32_16x16x32_bf16 v[48:51], v[210:213], v[218:221], v[48:51]
	v_mfma_f32_16x16x32_bf16 v[36:39], v[202:205], v[226:229], v[36:39]
	v_mfma_f32_16x16x32_bf16 v[32:35], v[210:213], v[226:229], v[32:35]
	v_mfma_f32_16x16x32_bf16 v[20:23], v[202:205], v[234:237], v[20:23]
	v_mfma_f32_16x16x32_bf16 v[16:19], v[210:213], v[234:237], v[16:19]
	v_mfma_f32_16x16x32_bf16 v[4:7], v[202:205], v[242:245], v[4:7]
	v_mfma_f32_16x16x32_bf16 v[0:3], v[210:213], v[242:245], v[0:3]
	v_mfma_f32_16x16x32_bf16 v[52:55], v[206:209], v[222:225], v[52:55]
	v_mfma_f32_16x16x32_bf16 v[48:51], v[214:217], v[222:225], v[48:51]
	v_mfma_f32_16x16x32_bf16 v[36:39], v[206:209], v[230:233], v[36:39]
	v_mfma_f32_16x16x32_bf16 v[32:35], v[214:217], v[230:233], v[32:35]
	v_mfma_f32_16x16x32_bf16 v[20:23], v[206:209], v[238:241], v[20:23]
	v_mfma_f32_16x16x32_bf16 v[16:19], v[214:217], v[238:241], v[16:19]
	v_mfma_f32_16x16x32_bf16 v[4:7], v[206:209], v[246:249], v[4:7]
	v_mfma_f32_16x16x32_bf16 v[0:3], v[214:217], v[246:249], v[0:3]
	s_barrier
	s_add_i32 s48, 0, 0x18000
	v_add_u32_e32 v185, s48, v166
	s_add_i32 s49, 0, 0x1c000
	ds_read_b128 v[186:189], v185
	ds_read_b128 v[190:193], v185 offset:1024
	ds_read_b128 v[194:197], v185 offset:2048
	ds_read_b128 v[198:201], v185 offset:3072
	v_add_u32_e32 v185, s49, v166
	ds_read_b128 v[202:205], v185
	ds_read_b128 v[206:209], v185 offset:1024
	ds_read_b128 v[210:213], v185 offset:2048
	ds_read_b128 v[214:217], v185 offset:3072
	s_mov_b32 m0, s66
	v_lshl_add_u64 v[148:149], s[40:41], 0, v[148:149]
	ds_read_b128 v[218:221], v182 offset:32768
	ds_read_b128 v[222:225], v182 offset:33792
	ds_read_b128 v[226:229], v182 offset:34816
	ds_read_b128 v[230:233], v182 offset:35840
	ds_read_b128 v[234:237], v182 offset:36864
	ds_read_b128 v[238:241], v182 offset:37888
	ds_read_b128 v[242:245], v182 offset:38912
	ds_read_b128 v[246:249], v182 offset:39936
	global_load_lds_dwordx4 v[148:149], off
	v_lshl_add_u64 v[148:149], s[40:41], 0, v[150:151]
	s_mov_b32 m0, s67
	s_nop 0
	global_load_lds_dwordx4 v[148:149], off
	s_waitcnt vmcnt(8)
	s_waitcnt lgkmcnt(0)
	s_barrier
	v_mfma_f32_16x16x32_bf16 v[124:127], v[186:189], v[218:221], v[124:127]
	v_mfma_f32_16x16x32_bf16 v[120:123], v[194:197], v[218:221], v[120:123]
	v_mfma_f32_16x16x32_bf16 v[108:111], v[186:189], v[226:229], v[108:111]
	v_mfma_f32_16x16x32_bf16 v[104:107], v[194:197], v[226:229], v[104:107]
	v_mfma_f32_16x16x32_bf16 v[92:95], v[186:189], v[234:237], v[92:95]
	v_mfma_f32_16x16x32_bf16 v[88:91], v[194:197], v[234:237], v[88:91]
	v_mfma_f32_16x16x32_bf16 v[76:79], v[186:189], v[242:245], v[76:79]
	v_mfma_f32_16x16x32_bf16 v[72:75], v[194:197], v[242:245], v[72:75]
	v_mfma_f32_16x16x32_bf16 v[124:127], v[190:193], v[222:225], v[124:127]
	v_mfma_f32_16x16x32_bf16 v[120:123], v[198:201], v[222:225], v[120:123]
	v_mfma_f32_16x16x32_bf16 v[108:111], v[190:193], v[230:233], v[108:111]
	v_mfma_f32_16x16x32_bf16 v[104:107], v[198:201], v[230:233], v[104:107]
	v_mfma_f32_16x16x32_bf16 v[92:95], v[190:193], v[238:241], v[92:95]
	v_mfma_f32_16x16x32_bf16 v[88:91], v[198:201], v[238:241], v[88:91]
	v_mfma_f32_16x16x32_bf16 v[76:79], v[190:193], v[246:249], v[76:79]
	v_mfma_f32_16x16x32_bf16 v[72:75], v[198:201], v[246:249], v[72:75]
	v_mfma_f32_16x16x32_bf16 v[116:119], v[202:205], v[218:221], v[116:119]
	v_mfma_f32_16x16x32_bf16 v[112:115], v[210:213], v[218:221], v[112:115]
	v_mfma_f32_16x16x32_bf16 v[100:103], v[202:205], v[226:229], v[100:103]
	v_mfma_f32_16x16x32_bf16 v[96:99], v[210:213], v[226:229], v[96:99]
	v_mfma_f32_16x16x32_bf16 v[84:87], v[202:205], v[234:237], v[84:87]
	v_mfma_f32_16x16x32_bf16 v[80:83], v[210:213], v[234:237], v[80:83]
	v_mfma_f32_16x16x32_bf16 v[68:71], v[202:205], v[242:245], v[68:71]
	v_mfma_f32_16x16x32_bf16 v[64:67], v[210:213], v[242:245], v[64:67]
	v_mfma_f32_16x16x32_bf16 v[116:119], v[206:209], v[222:225], v[116:119]
	v_mfma_f32_16x16x32_bf16 v[112:115], v[214:217], v[222:225], v[112:115]
	v_mfma_f32_16x16x32_bf16 v[100:103], v[206:209], v[230:233], v[100:103]
	v_mfma_f32_16x16x32_bf16 v[96:99], v[214:217], v[230:233], v[96:99]
	v_mfma_f32_16x16x32_bf16 v[84:87], v[206:209], v[238:241], v[84:87]
	v_mfma_f32_16x16x32_bf16 v[80:83], v[214:217], v[238:241], v[80:83]
	v_mfma_f32_16x16x32_bf16 v[68:71], v[206:209], v[246:249], v[68:71]
	v_mfma_f32_16x16x32_bf16 v[64:67], v[214:217], v[246:249], v[64:67]
	s_barrier
; template <class Epi, class Sched, class Hook = NoHook>
; __device__ __forceinline__ void gemm_phase_w(LAS unsigned char* lds, const Sched& S, const Epi& E, int wave_id, const Hook& HK = Hook()) {
;     ...
;         if constexpr (!SEG2) {
;             for (int tt = 0; tt < nt; tt += 2) {
;                 if constexpr (GATHER) { if (tt == nt - 2) {
;                     if (has_next) { gnxt_00 = S.grow_l(nxt, lds, nbuf, R0) + (unsigned)(C0 * 2); gnxt_01 = S.grow_l(nxt, lds, nbuf, R1) + (unsigned)(C1 * 2); gnxt_10 = S.grow_l(nxt, lds, nbuf, 128 + R0) + (unsigned)(C0 * 2); gnxt_11 = S.grow_l(nxt, lds, nbuf, 128 + R1) + (unsigned)(C1 * 2); }
;                     else { gnxt_00 = gcur_00; gnxt_01 = gcur_01; gnxt_10 = gcur_10; gnxt_11 = gcur_11; } } }
;                 PG_TRIP(tt, false, false, false);
;             }
	s_bitset1_b32 s22, 7
	s_add_i32 vcc_lo, vcc_lo, s22
	s_ashr_i32 s41, vcc_lo, 31
	s_add_u32 s40, s16, vcc_lo
	s_addc_u32 s41, s17, s41
	s_add_i32 s48, s48, s44
	v_lshl_add_u64 v[246:247], s[40:41], 0, v[136:137]
	s_mov_b32 m0, s48
	s_add_i32 vcc_lo, vcc_lo, 0x80000
	ds_read_b128 v[148:151], v182 offset:49152
	ds_read_b128 v[218:221], v182 offset:50176
	ds_read_b128 v[222:225], v182 offset:51200
	ds_read_b128 v[226:229], v182 offset:52224
	ds_read_b128 v[230:233], v182 offset:53248
	ds_read_b128 v[234:237], v182 offset:54272
	ds_read_b128 v[238:241], v182 offset:55296
	ds_read_b128 v[242:245], v182 offset:56320
	global_load_lds_dwordx4 v[246:247], off
	v_lshl_add_u64 v[246:247], s[40:41], 0, v[138:139]
	s_add_i32 m0, s48, 0x2000
	s_ashr_i32 s41, vcc_lo, 31
	s_add_u32 s40, s16, vcc_lo
	s_addc_u32 s41, s17, s41
	s_add_i32 s48, s49, s44
	global_load_lds_dwordx4 v[246:247], off
	v_lshl_add_u64 v[246:247], s[40:41], 0, v[136:137]
	s_mov_b32 m0, s48
	v_lshl_add_u64 v[146:147], s[14:15], 0, v[146:147]
	global_load_lds_dwordx4 v[246:247], off
	v_lshl_add_u64 v[246:247], s[40:41], 0, v[138:139]
	s_add_i32 m0, s48, 0x2000
	v_lshl_add_u64 v[146:147], v[146:147], 0, s[22:23]
	global_load_lds_dwordx4 v[246:247], off
	v_lshl_add_u64 v[246:247], s[14:15], 0, v[140:141]
	v_lshl_add_u64 v[246:247], v[246:247], 0, s[22:23]
	s_mov_b32 m0, s68
	s_nop 0
	global_load_lds_dwordx4 v[246:247], off
	s_mov_b32 m0, s69
	s_nop 0
	global_load_lds_dwordx4 v[146:147], off
	s_waitcnt vmcnt(8)
	s_waitcnt lgkmcnt(0)
	s_barrier
	v_mfma_f32_16x16x32_bf16 v[60:63], v[186:189], v[148:151], v[60:63]
	v_mfma_f32_16x16x32_bf16 v[56:59], v[194:197], v[148:151], v[56:59]
	v_mfma_f32_16x16x32_bf16 v[44:47], v[186:189], v[222:225], v[44:47]
	v_mfma_f32_16x16x32_bf16 v[40:43], v[194:197], v[222:225], v[40:43]
	v_mfma_f32_16x16x32_bf16 v[28:31], v[186:189], v[230:233], v[28:31]
	v_mfma_f32_16x16x32_bf16 v[24:27], v[194:197], v[230:233], v[24:27]
	v_mfma_f32_16x16x32_bf16 v[12:15], v[186:189], v[238:241], v[12:15]
	v_mfma_f32_16x16x32_bf16 v[8:11], v[194:197], v[238:241], v[8:11]
	v_mfma_f32_16x16x32_bf16 v[60:63], v[190:193], v[218:221], v[60:63]
	v_mfma_f32_16x16x32_bf16 v[56:59], v[198:201], v[218:221], v[56:59]
	v_mfma_f32_16x16x32_bf16 v[44:47], v[190:193], v[226:229], v[44:47]
	v_mfma_f32_16x16x32_bf16 v[40:43], v[198:201], v[226:229], v[40:43]
	v_mfma_f32_16x16x32_bf16 v[28:31], v[190:193], v[234:237], v[28:31]
	v_mfma_f32_16x16x32_bf16 v[24:27], v[198:201], v[234:237], v[24:27]
	v_mfma_f32_16x16x32_bf16 v[12:15], v[190:193], v[242:245], v[12:15]
	v_mfma_f32_16x16x32_bf16 v[8:11], v[198:201], v[242:245], v[8:11]
	v_mfma_f32_16x16x32_bf16 v[52:55], v[202:205], v[148:151], v[52:55]
	v_mfma_f32_16x16x32_bf16 v[48:51], v[210:213], v[148:151], v[48:51]
	v_mfma_f32_16x16x32_bf16 v[36:39], v[202:205], v[222:225], v[36:39]
	v_mfma_f32_16x16x32_bf16 v[32:35], v[210:213], v[222:225], v[32:35]
	v_mfma_f32_16x16x32_bf16 v[20:23], v[202:205], v[230:233], v[20:23]
	v_mfma_f32_16x16x32_bf16 v[16:19], v[210:213], v[230:233], v[16:19]
	v_mfma_f32_16x16x32_bf16 v[4:7], v[202:205], v[238:241], v[4:7]
	v_mfma_f32_16x16x32_bf16 v[0:3], v[210:213], v[238:241], v[0:3]
	v_mfma_f32_16x16x32_bf16 v[52:55], v[206:209], v[218:221], v[52:55]
	v_mfma_f32_16x16x32_bf16 v[48:51], v[214:217], v[218:221], v[48:51]
	v_mfma_f32_16x16x32_bf16 v[36:39], v[206:209], v[226:229], v[36:39]
	v_mfma_f32_16x16x32_bf16 v[32:35], v[214:217], v[226:229], v[32:35]
	v_mfma_f32_16x16x32_bf16 v[20:23], v[206:209], v[234:237], v[20:23]
	v_mfma_f32_16x16x32_bf16 v[16:19], v[214:217], v[234:237], v[16:19]
	v_mfma_f32_16x16x32_bf16 v[4:7], v[206:209], v[242:245], v[4:7]
	v_mfma_f32_16x16x32_bf16 v[0:3], v[214:217], v[242:245], v[0:3]
	s_barrier
	s_add_i32 s89, s89, 2
	s_addk_i32 s97, 0x100
	s_add_u32 s38, s38, 0x100
	s_addc_u32 s39, s39, 0
	s_cmp_gt_u32 s89, 29
	s_cbranch_scc1 .LBB0_831

.LBB0_1082:
	v_add_u32_e32 v147, s49, v163
	ds_read_b128 v[182:185], v147
	ds_read_b128 v[186:189], v147 offset:1024
	ds_read_b128 v[190:193], v147 offset:2048
	ds_read_b128 v[194:197], v147 offset:3072
	v_add_u32_e32 v147, s58, v163
	ds_read_b128 v[198:201], v147
	ds_read_b128 v[202:205], v147 offset:1024
	ds_read_b128 v[206:209], v147 offset:2048
	ds_read_b128 v[210:213], v147 offset:3072
	v_lshl_add_u64 v[246:247], s[38:39], 0, v[130:131]
	s_add_i32 m0, s63, 0xc000
	ds_read_b128 v[214:217], v179
	ds_read_b128 v[218:221], v179 offset:1024
	ds_read_b128 v[222:225], v179 offset:2048
	ds_read_b128 v[226:229], v179 offset:3072
	ds_read_b128 v[230:233], v179 offset:4096
	ds_read_b128 v[234:237], v179 offset:5120
	ds_read_b128 v[238:241], v179 offset:6144
	ds_read_b128 v[242:245], v179 offset:7168
	global_load_lds_dwordx4 v[246:247], off
	v_lshl_add_u64 v[246:247], s[38:39], 0, v[132:133]
	s_add_i32 m0, s63, 0xe000
	s_nop 0
	global_load_lds_dwordx4 v[246:247], off
	s_waitcnt vmcnt(8)
	s_waitcnt lgkmcnt(0)
	s_barrier
	v_mfma_f32_16x16x32_bf16 v[124:127], v[182:185], v[214:217], v[124:127]
	v_mfma_f32_16x16x32_bf16 v[120:123], v[190:193], v[214:217], v[120:123]
	v_mfma_f32_16x16x32_bf16 v[108:111], v[182:185], v[222:225], v[108:111]
	v_mfma_f32_16x16x32_bf16 v[104:107], v[190:193], v[222:225], v[104:107]
	v_mfma_f32_16x16x32_bf16 v[92:95], v[182:185], v[230:233], v[92:95]
	v_mfma_f32_16x16x32_bf16 v[88:91], v[190:193], v[230:233], v[88:91]
	v_mfma_f32_16x16x32_bf16 v[76:79], v[182:185], v[238:241], v[76:79]
	v_mfma_f32_16x16x32_bf16 v[72:75], v[190:193], v[238:241], v[72:75]
	v_mfma_f32_16x16x32_bf16 v[124:127], v[186:189], v[218:221], v[124:127]
	v_mfma_f32_16x16x32_bf16 v[120:123], v[194:197], v[218:221], v[120:123]
	v_mfma_f32_16x16x32_bf16 v[108:111], v[186:189], v[226:229], v[108:111]
	v_mfma_f32_16x16x32_bf16 v[104:107], v[194:197], v[226:229], v[104:107]
	v_mfma_f32_16x16x32_bf16 v[92:95], v[186:189], v[234:237], v[92:95]
	v_mfma_f32_16x16x32_bf16 v[88:91], v[194:197], v[234:237], v[88:91]
	v_mfma_f32_16x16x32_bf16 v[76:79], v[186:189], v[242:245], v[76:79]
	v_mfma_f32_16x16x32_bf16 v[72:75], v[194:197], v[242:245], v[72:75]
	v_mfma_f32_16x16x32_bf16 v[116:119], v[198:201], v[214:217], v[116:119]
	v_mfma_f32_16x16x32_bf16 v[112:115], v[206:209], v[214:217], v[112:115]
	v_mfma_f32_16x16x32_bf16 v[100:103], v[198:201], v[222:225], v[100:103]
	v_mfma_f32_16x16x32_bf16 v[96:99], v[206:209], v[222:225], v[96:99]
	v_mfma_f32_16x16x32_bf16 v[84:87], v[198:201], v[230:233], v[84:87]
	v_mfma_f32_16x16x32_bf16 v[80:83], v[206:209], v[230:233], v[80:83]
	v_mfma_f32_16x16x32_bf16 v[68:71], v[198:201], v[238:241], v[68:71]
	v_mfma_f32_16x16x32_bf16 v[64:67], v[206:209], v[238:241], v[64:67]
	v_mfma_f32_16x16x32_bf16 v[116:119], v[202:205], v[218:221], v[116:119]
	v_mfma_f32_16x16x32_bf16 v[112:115], v[210:213], v[218:221], v[112:115]
	v_mfma_f32_16x16x32_bf16 v[100:103], v[202:205], v[226:229], v[100:103]
	v_mfma_f32_16x16x32_bf16 v[96:99], v[210:213], v[226:229], v[96:99]
	v_mfma_f32_16x16x32_bf16 v[84:87], v[202:205], v[234:237], v[84:87]
	v_mfma_f32_16x16x32_bf16 v[80:83], v[210:213], v[234:237], v[80:83]
	v_mfma_f32_16x16x32_bf16 v[68:71], v[202:205], v[242:245], v[68:71]
	v_mfma_f32_16x16x32_bf16 v[64:67], v[210:213], v[242:245], v[64:67]
	s_barrier
	s_and_b64 s[40:41], s[40:41], exec
	s_cselect_b32 s22, 0, s78
	s_add_i32 s84, s79, s22
	s_ashr_i32 s41, s84, 31
	s_add_u32 s40, s16, s84
	s_addc_u32 s41, s17, s41
	s_add_i32 s85, s49, s44
	v_lshl_add_u64 v[246:247], s[40:41], 0, v[136:137]
	s_mov_b32 m0, s85
	s_add_i32 s84, s84, 0x80000
	ds_read_b128 v[214:217], v179 offset:16384
	ds_read_b128 v[218:221], v179 offset:17408
	ds_read_b128 v[222:225], v179 offset:18432
	ds_read_b128 v[226:229], v179 offset:19456
	ds_read_b128 v[230:233], v179 offset:20480
	ds_read_b128 v[234:237], v179 offset:21504
	ds_read_b128 v[238:241], v179 offset:22528
	ds_read_b128 v[242:245], v179 offset:23552
	global_load_lds_dwordx4 v[246:247], off
	v_lshl_add_u64 v[246:247], s[40:41], 0, v[138:139]
	s_add_i32 m0, s85, 0x2000
	s_ashr_i32 s41, s84, 31
	s_add_u32 s40, s16, s84
	s_addc_u32 s41, s17, s41
	s_add_i32 s84, s58, s44
	global_load_lds_dwordx4 v[246:247], off
	v_lshl_add_u64 v[246:247], s[40:41], 0, v[136:137]
	s_mov_b32 m0, s84
	v_mov_b32_e32 v147, v141
	global_load_lds_dwordx4 v[246:247], off
	s_add_i32 m0, s84, 0x2000
	v_lshl_add_u64 v[246:247], s[40:41], 0, v[138:139]
	s_add_u32 s40, s14, s22
	global_load_lds_dwordx4 v[246:247], off
	s_addc_u32 s41, s15, 0
	s_mov_b32 m0, s63
	s_nop 0
	global_load_lds_dwordx4 v140, s[40:41]
	s_mov_b32 m0, s66
	s_nop 0
	global_load_lds_dwordx4 v146, s[40:41]
	s_waitcnt vmcnt(8)
	s_waitcnt lgkmcnt(0)
	s_barrier
	v_mfma_f32_16x16x32_bf16 v[60:63], v[182:185], v[214:217], v[60:63]
	v_mfma_f32_16x16x32_bf16 v[56:59], v[190:193], v[214:217], v[56:59]
	v_mfma_f32_16x16x32_bf16 v[44:47], v[182:185], v[222:225], v[44:47]
	v_mfma_f32_16x16x32_bf16 v[40:43], v[190:193], v[222:225], v[40:43]
	v_mfma_f32_16x16x32_bf16 v[28:31], v[182:185], v[230:233], v[28:31]
	v_mfma_f32_16x16x32_bf16 v[24:27], v[190:193], v[230:233], v[24:27]
	v_mfma_f32_16x16x32_bf16 v[12:15], v[182:185], v[238:241], v[12:15]
	v_mfma_f32_16x16x32_bf16 v[8:11], v[190:193], v[238:241], v[8:11]
	v_mfma_f32_16x16x32_bf16 v[60:63], v[186:189], v[218:221], v[60:63]
	v_mfma_f32_16x16x32_bf16 v[56:59], v[194:197], v[218:221], v[56:59]
	v_mfma_f32_16x16x32_bf16 v[44:47], v[186:189], v[226:229], v[44:47]
	v_mfma_f32_16x16x32_bf16 v[40:43], v[194:197], v[226:229], v[40:43]
	v_mfma_f32_16x16x32_bf16 v[28:31], v[186:189], v[234:237], v[28:31]
	v_mfma_f32_16x16x32_bf16 v[24:27], v[194:197], v[234:237], v[24:27]
	v_mfma_f32_16x16x32_bf16 v[12:15], v[186:189], v[242:245], v[12:15]
	v_mfma_f32_16x16x32_bf16 v[8:11], v[194:197], v[242:245], v[8:11]
	v_mfma_f32_16x16x32_bf16 v[52:55], v[198:201], v[214:217], v[52:55]
	v_mfma_f32_16x16x32_bf16 v[48:51], v[206:209], v[214:217], v[48:51]
	v_mfma_f32_16x16x32_bf16 v[36:39], v[198:201], v[222:225], v[36:39]
	v_mfma_f32_16x16x32_bf16 v[32:35], v[206:209], v[222:225], v[32:35]
	v_mfma_f32_16x16x32_bf16 v[20:23], v[198:201], v[230:233], v[20:23]
	v_mfma_f32_16x16x32_bf16 v[16:19], v[206:209], v[230:233], v[16:19]
	v_mfma_f32_16x16x32_bf16 v[4:7], v[198:201], v[238:241], v[4:7]
	v_mfma_f32_16x16x32_bf16 v[0:3], v[206:209], v[238:241], v[0:3]
	v_mfma_f32_16x16x32_bf16 v[52:55], v[202:205], v[218:221], v[52:55]
	v_mfma_f32_16x16x32_bf16 v[48:51], v[210:213], v[218:221], v[48:51]
	v_mfma_f32_16x16x32_bf16 v[36:39], v[202:205], v[226:229], v[36:39]
	v_mfma_f32_16x16x32_bf16 v[32:35], v[210:213], v[226:229], v[32:35]
	v_mfma_f32_16x16x32_bf16 v[20:23], v[202:205], v[234:237], v[20:23]
	v_mfma_f32_16x16x32_bf16 v[16:19], v[210:213], v[234:237], v[16:19]
	v_mfma_f32_16x16x32_bf16 v[4:7], v[202:205], v[242:245], v[4:7]
	v_mfma_f32_16x16x32_bf16 v[0:3], v[210:213], v[242:245], v[0:3]
	s_barrier
	s_add_i32 s84, 0, 0x18000
	s_add_i32 s85, 0, 0x1c000
	v_add_u32_e32 v194, s84, v163
	v_add_u32_e32 v210, s85, v163
	ds_read_b128 v[182:185], v194
	ds_read_b128 v[186:189], v194 offset:1024
	ds_read_b128 v[190:193], v194 offset:2048
	ds_read_b128 v[194:197], v194 offset:3072
	ds_read_b128 v[198:201], v210
	ds_read_b128 v[202:205], v210 offset:1024
	ds_read_b128 v[206:209], v210 offset:2048
	ds_read_b128 v[210:213], v210 offset:3072
	s_mov_b32 m0, s67
	v_lshl_add_u64 v[148:149], s[40:41], 0, v[148:149]
	ds_read_b128 v[214:217], v179 offset:32768
	ds_read_b128 v[218:221], v179 offset:33792
	ds_read_b128 v[222:225], v179 offset:34816
	ds_read_b128 v[226:229], v179 offset:35840
	ds_read_b128 v[230:233], v179 offset:36864
	ds_read_b128 v[234:237], v179 offset:37888
	ds_read_b128 v[238:241], v179 offset:38912
	ds_read_b128 v[242:245], v179 offset:39936
	global_load_lds_dwordx4 v[148:149], off
	v_lshl_add_u64 v[148:149], s[40:41], 0, v[150:151]
	s_mov_b32 m0, s68
	s_nop 0
	global_load_lds_dwordx4 v[148:149], off
	s_waitcnt vmcnt(8)
	s_waitcnt lgkmcnt(0)
	s_barrier
	v_mfma_f32_16x16x32_bf16 v[124:127], v[182:185], v[214:217], v[124:127]
	v_mfma_f32_16x16x32_bf16 v[120:123], v[190:193], v[214:217], v[120:123]
	v_mfma_f32_16x16x32_bf16 v[108:111], v[182:185], v[222:225], v[108:111]
	v_mfma_f32_16x16x32_bf16 v[104:107], v[190:193], v[222:225], v[104:107]
	v_mfma_f32_16x16x32_bf16 v[92:95], v[182:185], v[230:233], v[92:95]
	v_mfma_f32_16x16x32_bf16 v[88:91], v[190:193], v[230:233], v[88:91]
	v_mfma_f32_16x16x32_bf16 v[76:79], v[182:185], v[238:241], v[76:79]
	v_mfma_f32_16x16x32_bf16 v[72:75], v[190:193], v[238:241], v[72:75]
	v_mfma_f32_16x16x32_bf16 v[124:127], v[186:189], v[218:221], v[124:127]
	v_mfma_f32_16x16x32_bf16 v[120:123], v[194:197], v[218:221], v[120:123]
	v_mfma_f32_16x16x32_bf16 v[108:111], v[186:189], v[226:229], v[108:111]
	v_mfma_f32_16x16x32_bf16 v[104:107], v[194:197], v[226:229], v[104:107]
	v_mfma_f32_16x16x32_bf16 v[92:95], v[186:189], v[234:237], v[92:95]
	v_mfma_f32_16x16x32_bf16 v[88:91], v[194:197], v[234:237], v[88:91]
	v_mfma_f32_16x16x32_bf16 v[76:79], v[186:189], v[242:245], v[76:79]
	v_mfma_f32_16x16x32_bf16 v[72:75], v[194:197], v[242:245], v[72:75]
	v_mfma_f32_16x16x32_bf16 v[116:119], v[198:201], v[214:217], v[116:119]
	v_mfma_f32_16x16x32_bf16 v[112:115], v[206:209], v[214:217], v[112:115]
	v_mfma_f32_16x16x32_bf16 v[100:103], v[198:201], v[222:225], v[100:103]
	v_mfma_f32_16x16x32_bf16 v[96:99], v[206:209], v[222:225], v[96:99]
	v_mfma_f32_16x16x32_bf16 v[84:87], v[198:201], v[230:233], v[84:87]
	v_mfma_f32_16x16x32_bf16 v[80:83], v[206:209], v[230:233], v[80:83]
	v_mfma_f32_16x16x32_bf16 v[68:71], v[198:201], v[238:241], v[68:71]
	v_mfma_f32_16x16x32_bf16 v[64:67], v[206:209], v[238:241], v[64:67]
	v_mfma_f32_16x16x32_bf16 v[116:119], v[202:205], v[218:221], v[116:119]
	v_mfma_f32_16x16x32_bf16 v[112:115], v[210:213], v[218:221], v[112:115]
	v_mfma_f32_16x16x32_bf16 v[100:103], v[202:205], v[226:229], v[100:103]
	v_mfma_f32_16x16x32_bf16 v[96:99], v[210:213], v[226:229], v[96:99]
	v_mfma_f32_16x16x32_bf16 v[84:87], v[202:205], v[234:237], v[84:87]
	v_mfma_f32_16x16x32_bf16 v[80:83], v[210:213], v[234:237], v[80:83]
	v_mfma_f32_16x16x32_bf16 v[68:71], v[202:205], v[242:245], v[68:71]
	v_mfma_f32_16x16x32_bf16 v[64:67], v[210:213], v[242:245], v[64:67]
	s_barrier
; template <class Epi, class Sched, class Hook = NoHook>
; __device__ __forceinline__ void gemm_phase_w(LAS unsigned char* lds, const Sched& S, const Epi& E, int wave_id, const Hook& HK = Hook()) {
;     ...
;         if constexpr (!SEG2) {
;             for (int tt = 0; tt < nt; tt += 2) {
;                 if constexpr (GATHER) { if (tt == nt - 2) {
;                     if (has_next) { gnxt_00 = S.grow_l(nxt, lds, nbuf, R0) + (unsigned)(C0 * 2); gnxt_01 = S.grow_l(nxt, lds, nbuf, R1) + (unsigned)(C1 * 2); gnxt_10 = S.grow_l(nxt, lds, nbuf, 128 + R0) + (unsigned)(C0 * 2); gnxt_11 = S.grow_l(nxt, lds, nbuf, 128 + R1) + (unsigned)(C1 * 2); }
;                     else { gnxt_00 = gcur_00; gnxt_01 = gcur_01; gnxt_10 = gcur_10; gnxt_11 = gcur_11; } } }
;                 PG_TRIP(tt, false, false, false);
;             }
	s_bitset1_b32 s22, 7
	s_add_i32 s79, s79, s22
	s_ashr_i32 s41, s79, 31
	s_add_u32 s40, s16, s79
	s_addc_u32 s41, s17, s41
	s_add_i32 s84, s84, s44
	v_lshl_add_u64 v[242:243], s[40:41], 0, v[136:137]
	s_mov_b32 m0, s84
	s_add_i32 s79, s79, 0x80000
	ds_read_b128 v[148:151], v179 offset:49152
	ds_read_b128 v[214:217], v179 offset:50176
	ds_read_b128 v[218:221], v179 offset:51200
	ds_read_b128 v[222:225], v179 offset:52224
	ds_read_b128 v[226:229], v179 offset:53248
	ds_read_b128 v[230:233], v179 offset:54272
	ds_read_b128 v[234:237], v179 offset:55296
	ds_read_b128 v[238:241], v179 offset:56320
	global_load_lds_dwordx4 v[242:243], off
	v_lshl_add_u64 v[242:243], s[40:41], 0, v[138:139]
	s_add_i32 m0, s84, 0x2000
	s_ashr_i32 s41, s79, 31
	s_add_u32 s40, s16, s79
	s_addc_u32 s41, s17, s41
	s_add_i32 s79, s85, s44
	global_load_lds_dwordx4 v[242:243], off
	v_lshl_add_u64 v[242:243], s[40:41], 0, v[136:137]
	s_mov_b32 m0, s79
	v_lshl_add_u64 v[146:147], s[14:15], 0, v[146:147]
	global_load_lds_dwordx4 v[242:243], off
	v_lshl_add_u64 v[242:243], s[40:41], 0, v[138:139]
	s_add_i32 m0, s79, 0x2000
	v_lshl_add_u64 v[146:147], v[146:147], 0, s[22:23]
	global_load_lds_dwordx4 v[242:243], off
	v_lshl_add_u64 v[242:243], s[14:15], 0, v[140:141]
	v_lshl_add_u64 v[242:243], v[242:243], 0, s[22:23]
	s_mov_b32 m0, s59
	s_nop 0
	global_load_lds_dwordx4 v[242:243], off
	s_mov_b32 m0, s69
	s_nop 0
	global_load_lds_dwordx4 v[146:147], off
	s_waitcnt vmcnt(8)
	s_waitcnt lgkmcnt(0)
	s_barrier
	v_mfma_f32_16x16x32_bf16 v[60:63], v[182:185], v[148:151], v[60:63]
	v_mfma_f32_16x16x32_bf16 v[56:59], v[190:193], v[148:151], v[56:59]
	v_mfma_f32_16x16x32_bf16 v[44:47], v[182:185], v[218:221], v[44:47]
	v_mfma_f32_16x16x32_bf16 v[40:43], v[190:193], v[218:221], v[40:43]
	v_mfma_f32_16x16x32_bf16 v[28:31], v[182:185], v[226:229], v[28:31]
	v_mfma_f32_16x16x32_bf16 v[24:27], v[190:193], v[226:229], v[24:27]
	v_mfma_f32_16x16x32_bf16 v[12:15], v[182:185], v[234:237], v[12:15]
	v_mfma_f32_16x16x32_bf16 v[8:11], v[190:193], v[234:237], v[8:11]
	v_mfma_f32_16x16x32_bf16 v[60:63], v[186:189], v[214:217], v[60:63]
	v_mfma_f32_16x16x32_bf16 v[56:59], v[194:197], v[214:217], v[56:59]
	v_mfma_f32_16x16x32_bf16 v[44:47], v[186:189], v[222:225], v[44:47]
	v_mfma_f32_16x16x32_bf16 v[40:43], v[194:197], v[222:225], v[40:43]
	v_mfma_f32_16x16x32_bf16 v[28:31], v[186:189], v[230:233], v[28:31]
	v_mfma_f32_16x16x32_bf16 v[24:27], v[194:197], v[230:233], v[24:27]
	v_mfma_f32_16x16x32_bf16 v[12:15], v[186:189], v[238:241], v[12:15]
	v_mfma_f32_16x16x32_bf16 v[8:11], v[194:197], v[238:241], v[8:11]
	v_mfma_f32_16x16x32_bf16 v[52:55], v[198:201], v[148:151], v[52:55]
	v_mfma_f32_16x16x32_bf16 v[48:51], v[206:209], v[148:151], v[48:51]
	v_mfma_f32_16x16x32_bf16 v[36:39], v[198:201], v[218:221], v[36:39]
	v_mfma_f32_16x16x32_bf16 v[32:35], v[206:209], v[218:221], v[32:35]
	v_mfma_f32_16x16x32_bf16 v[20:23], v[198:201], v[226:229], v[20:23]
	v_mfma_f32_16x16x32_bf16 v[16:19], v[206:209], v[226:229], v[16:19]
	v_mfma_f32_16x16x32_bf16 v[4:7], v[198:201], v[234:237], v[4:7]
	v_mfma_f32_16x16x32_bf16 v[0:3], v[206:209], v[234:237], v[0:3]
	v_mfma_f32_16x16x32_bf16 v[52:55], v[202:205], v[214:217], v[52:55]
	v_mfma_f32_16x16x32_bf16 v[48:51], v[210:213], v[214:217], v[48:51]
	v_mfma_f32_16x16x32_bf16 v[36:39], v[202:205], v[222:225], v[36:39]
	v_mfma_f32_16x16x32_bf16 v[32:35], v[210:213], v[222:225], v[32:35]
	v_mfma_f32_16x16x32_bf16 v[20:23], v[202:205], v[230:233], v[20:23]
	v_mfma_f32_16x16x32_bf16 v[16:19], v[210:213], v[230:233], v[16:19]
	v_mfma_f32_16x16x32_bf16 v[4:7], v[202:205], v[238:241], v[4:7]
	v_mfma_f32_16x16x32_bf16 v[0:3], v[210:213], v[238:241], v[0:3]
	s_barrier
	s_add_i32 s77, s77, 2
	s_addk_i32 s78, 0x100
	s_add_u32 s38, s38, 0x100
	s_addc_u32 s39, s39, 0
	s_cmp_gt_u32 s77, 29
	s_cbranch_scc1 .LBB0_1086

.LBB0_1194:
	ds_read_b128 v[160:163], v156
	ds_read_b128 v[164:167], v156 offset:1024
	ds_read_b128 v[168:171], v156 offset:2048
	ds_read_b128 v[172:175], v156 offset:3072
	ds_read_b128 v[176:179], v157
	ds_read_b128 v[180:183], v157 offset:1024
	ds_read_b128 v[184:187], v157 offset:2048
	ds_read_b128 v[188:191], v157 offset:3072
	s_add_i32 s22, s68, s12
	s_add_u32 s36, s28, s22
	s_addc_u32 s37, s29, 0
	s_add_i32 m0, s26, 0xc000
	s_add_i32 s71, s26, 0xe000
	s_add_i32 s72, s12, 0xfffc0080
	s_cmp_eq_u32 s19, 12
	s_cselect_b32 s22, s63, s68
	s_cselect_b32 s23, s66, s69
	v_lshl_add_u64 v[224:225], s[36:37], 0, v[130:131]
	ds_read_b128 v[192:195], v158
	ds_read_b128 v[196:199], v158 offset:1024
	ds_read_b128 v[200:203], v158 offset:2048
	ds_read_b128 v[204:207], v158 offset:3072
	ds_read_b128 v[208:211], v158 offset:4096
	ds_read_b128 v[212:215], v158 offset:5120
	ds_read_b128 v[216:219], v158 offset:6144
	ds_read_b128 v[220:223], v158 offset:7168
	global_load_lds_dwordx4 v[224:225], off
	v_lshl_add_u64 v[224:225], s[36:37], 0, v[132:133]
	s_mov_b32 m0, s71
	s_nop 0
	global_load_lds_dwordx4 v[224:225], off
	s_waitcnt vmcnt(8)
	s_waitcnt lgkmcnt(0)
	s_barrier
	v_mfma_f32_16x16x32_bf16 v[124:127], v[160:163], v[192:195], v[124:127]
	v_mfma_f32_16x16x32_bf16 v[120:123], v[168:171], v[192:195], v[120:123]
	v_mfma_f32_16x16x32_bf16 v[108:111], v[160:163], v[200:203], v[108:111]
	v_mfma_f32_16x16x32_bf16 v[104:107], v[168:171], v[200:203], v[104:107]
	v_mfma_f32_16x16x32_bf16 v[92:95], v[160:163], v[208:211], v[92:95]
	v_mfma_f32_16x16x32_bf16 v[88:91], v[168:171], v[208:211], v[88:91]
	v_mfma_f32_16x16x32_bf16 v[76:79], v[160:163], v[216:219], v[76:79]
	v_mfma_f32_16x16x32_bf16 v[72:75], v[168:171], v[216:219], v[72:75]
	v_mfma_f32_16x16x32_bf16 v[124:127], v[164:167], v[196:199], v[124:127]
	v_mfma_f32_16x16x32_bf16 v[120:123], v[172:175], v[196:199], v[120:123]
	v_mfma_f32_16x16x32_bf16 v[108:111], v[164:167], v[204:207], v[108:111]
	v_mfma_f32_16x16x32_bf16 v[104:107], v[172:175], v[204:207], v[104:107]
	v_mfma_f32_16x16x32_bf16 v[92:95], v[164:167], v[212:215], v[92:95]
	v_mfma_f32_16x16x32_bf16 v[88:91], v[172:175], v[212:215], v[88:91]
	v_mfma_f32_16x16x32_bf16 v[76:79], v[164:167], v[220:223], v[76:79]
	v_mfma_f32_16x16x32_bf16 v[72:75], v[172:175], v[220:223], v[72:75]
	v_mfma_f32_16x16x32_bf16 v[116:119], v[176:179], v[192:195], v[116:119]
	v_mfma_f32_16x16x32_bf16 v[112:115], v[184:187], v[192:195], v[112:115]
	v_mfma_f32_16x16x32_bf16 v[100:103], v[176:179], v[200:203], v[100:103]
	v_mfma_f32_16x16x32_bf16 v[96:99], v[184:187], v[200:203], v[96:99]
	v_mfma_f32_16x16x32_bf16 v[84:87], v[176:179], v[208:211], v[84:87]
	v_mfma_f32_16x16x32_bf16 v[80:83], v[184:187], v[208:211], v[80:83]
	v_mfma_f32_16x16x32_bf16 v[68:71], v[176:179], v[216:219], v[68:71]
	v_mfma_f32_16x16x32_bf16 v[64:67], v[184:187], v[216:219], v[64:67]
	v_mfma_f32_16x16x32_bf16 v[116:119], v[180:183], v[196:199], v[116:119]
	v_mfma_f32_16x16x32_bf16 v[112:115], v[188:191], v[196:199], v[112:115]
	v_mfma_f32_16x16x32_bf16 v[100:103], v[180:183], v[204:207], v[100:103]
	v_mfma_f32_16x16x32_bf16 v[96:99], v[188:191], v[204:207], v[96:99]
	v_mfma_f32_16x16x32_bf16 v[84:87], v[180:183], v[212:215], v[84:87]
	v_mfma_f32_16x16x32_bf16 v[80:83], v[188:191], v[212:215], v[80:83]
	v_mfma_f32_16x16x32_bf16 v[68:71], v[180:183], v[220:223], v[68:71]
	v_mfma_f32_16x16x32_bf16 v[64:67], v[188:191], v[220:223], v[64:67]
	s_barrier
	s_cselect_b32 s71, 0, s72
	s_add_i32 s36, s71, s23
	s_ashr_i32 s37, s36, 31
	s_add_u32 s36, s10, s36
	s_addc_u32 s37, s11, s37
	s_add_i32 s72, s49, s34
	v_lshl_add_u64 v[224:225], s[36:37], 0, v[130:131]
	s_mov_b32 m0, s72
	ds_read_b128 v[192:195], v158 offset:16384
	ds_read_b128 v[196:199], v158 offset:17408
	ds_read_b128 v[200:203], v158 offset:18432
	ds_read_b128 v[204:207], v158 offset:19456
	ds_read_b128 v[208:211], v158 offset:20480
	ds_read_b128 v[212:215], v158 offset:21504
	ds_read_b128 v[216:219], v158 offset:22528
	ds_read_b128 v[220:223], v158 offset:23552
	global_load_lds_dwordx4 v[224:225], off
	s_add_i32 m0, s72, 0x2000
	s_add_i32 s72, s23, 0x40000
	v_lshl_add_u64 v[224:225], s[36:37], 0, v[132:133]
	s_add_i32 s36, s72, s71
	s_ashr_i32 s37, s36, 31
	s_add_u32 s36, s10, s36
	s_addc_u32 s37, s11, s37
	s_add_i32 s73, s58, s34
	global_load_lds_dwordx4 v[224:225], off
	v_lshl_add_u64 v[224:225], s[36:37], 0, v[130:131]
	s_mov_b32 m0, s73
	s_nop 0
	global_load_lds_dwordx4 v[224:225], off
	s_add_i32 m0, s73, 0x2000
	s_add_i32 s73, s71, s22
	v_lshl_add_u64 v[224:225], s[36:37], 0, v[132:133]
	s_add_u32 s36, s28, s73
	s_addc_u32 s37, s29, 0
	global_load_lds_dwordx4 v[224:225], off
	v_lshl_add_u64 v[224:225], s[36:37], 0, v[130:131]
	s_mov_b32 m0, s26
	s_nop 0
	global_load_lds_dwordx4 v[224:225], off
	v_lshl_add_u64 v[224:225], s[36:37], 0, v[132:133]
	s_mov_b32 m0, s27
	s_nop 0
	global_load_lds_dwordx4 v[224:225], off
	s_waitcnt vmcnt(8)
	s_waitcnt lgkmcnt(0)
	s_barrier
	v_mfma_f32_16x16x32_bf16 v[60:63], v[160:163], v[192:195], v[60:63]
	v_mfma_f32_16x16x32_bf16 v[56:59], v[168:171], v[192:195], v[56:59]
	v_mfma_f32_16x16x32_bf16 v[44:47], v[160:163], v[200:203], v[44:47]
	v_mfma_f32_16x16x32_bf16 v[40:43], v[168:171], v[200:203], v[40:43]
	v_mfma_f32_16x16x32_bf16 v[28:31], v[160:163], v[208:211], v[28:31]
	v_mfma_f32_16x16x32_bf16 v[24:27], v[168:171], v[208:211], v[24:27]
	v_mfma_f32_16x16x32_bf16 v[12:15], v[160:163], v[216:219], v[12:15]
	v_mfma_f32_16x16x32_bf16 v[8:11], v[168:171], v[216:219], v[8:11]
	v_mfma_f32_16x16x32_bf16 v[60:63], v[164:167], v[196:199], v[60:63]
	v_mfma_f32_16x16x32_bf16 v[56:59], v[172:175], v[196:199], v[56:59]
	v_mfma_f32_16x16x32_bf16 v[44:47], v[164:167], v[204:207], v[44:47]
	v_mfma_f32_16x16x32_bf16 v[40:43], v[172:175], v[204:207], v[40:43]
	v_mfma_f32_16x16x32_bf16 v[28:31], v[164:167], v[212:215], v[28:31]
	v_mfma_f32_16x16x32_bf16 v[24:27], v[172:175], v[212:215], v[24:27]
	v_mfma_f32_16x16x32_bf16 v[12:15], v[164:167], v[220:223], v[12:15]
	v_mfma_f32_16x16x32_bf16 v[8:11], v[172:175], v[220:223], v[8:11]
	v_mfma_f32_16x16x32_bf16 v[52:55], v[176:179], v[192:195], v[52:55]
	v_mfma_f32_16x16x32_bf16 v[48:51], v[184:187], v[192:195], v[48:51]
	v_mfma_f32_16x16x32_bf16 v[36:39], v[176:179], v[200:203], v[36:39]
	v_mfma_f32_16x16x32_bf16 v[32:35], v[184:187], v[200:203], v[32:35]
	v_mfma_f32_16x16x32_bf16 v[20:23], v[176:179], v[208:211], v[20:23]
	v_mfma_f32_16x16x32_bf16 v[16:19], v[184:187], v[208:211], v[16:19]
	v_mfma_f32_16x16x32_bf16 v[4:7], v[176:179], v[216:219], v[4:7]
	v_mfma_f32_16x16x32_bf16 v[0:3], v[184:187], v[216:219], v[0:3]
	v_mfma_f32_16x16x32_bf16 v[52:55], v[180:183], v[196:199], v[52:55]
	v_mfma_f32_16x16x32_bf16 v[48:51], v[188:191], v[196:199], v[48:51]
	v_mfma_f32_16x16x32_bf16 v[36:39], v[180:183], v[204:207], v[36:39]
	v_mfma_f32_16x16x32_bf16 v[32:35], v[188:191], v[204:207], v[32:35]
	v_mfma_f32_16x16x32_bf16 v[20:23], v[180:183], v[212:215], v[20:23]
	v_mfma_f32_16x16x32_bf16 v[16:19], v[188:191], v[212:215], v[16:19]
	v_mfma_f32_16x16x32_bf16 v[4:7], v[180:183], v[220:223], v[4:7]
	v_mfma_f32_16x16x32_bf16 v[0:3], v[188:191], v[220:223], v[0:3]
	s_barrier
	s_add_i32 s74, 0, 0x18000
	v_add_u32_e32 v159, s74, v140
	s_add_i32 s75, 0, 0x1c000
	ds_read_b128 v[160:163], v159
	ds_read_b128 v[164:167], v159 offset:1024
	ds_read_b128 v[168:171], v159 offset:2048
	ds_read_b128 v[172:175], v159 offset:3072
	v_add_u32_e32 v159, s75, v140
	ds_read_b128 v[176:179], v159
	ds_read_b128 v[180:183], v159 offset:1024
	ds_read_b128 v[184:187], v159 offset:2048
	ds_read_b128 v[188:191], v159 offset:3072
	s_add_i32 s73, s73, 0x40000
	s_add_u32 s36, s28, s73
	s_addc_u32 s37, s29, 0
	s_mov_b32 m0, s33
	v_lshl_add_u64 v[224:225], s[36:37], 0, v[130:131]
	ds_read_b128 v[192:195], v158 offset:32768
	ds_read_b128 v[196:199], v158 offset:33792
	ds_read_b128 v[200:203], v158 offset:34816
	ds_read_b128 v[204:207], v158 offset:35840
	ds_read_b128 v[208:211], v158 offset:36864
	ds_read_b128 v[212:215], v158 offset:37888
	ds_read_b128 v[216:219], v158 offset:38912
	ds_read_b128 v[220:223], v158 offset:39936
	global_load_lds_dwordx4 v[224:225], off
	v_lshl_add_u64 v[224:225], s[36:37], 0, v[132:133]
	s_mov_b32 m0, s41
	s_nop 0
	global_load_lds_dwordx4 v[224:225], off
	s_waitcnt vmcnt(8)
	s_waitcnt lgkmcnt(0)
	s_barrier
	v_mfma_f32_16x16x32_bf16 v[124:127], v[160:163], v[192:195], v[124:127]
	v_mfma_f32_16x16x32_bf16 v[120:123], v[168:171], v[192:195], v[120:123]
	v_mfma_f32_16x16x32_bf16 v[108:111], v[160:163], v[200:203], v[108:111]
	v_mfma_f32_16x16x32_bf16 v[104:107], v[168:171], v[200:203], v[104:107]
	v_mfma_f32_16x16x32_bf16 v[92:95], v[160:163], v[208:211], v[92:95]
	v_mfma_f32_16x16x32_bf16 v[88:91], v[168:171], v[208:211], v[88:91]
	v_mfma_f32_16x16x32_bf16 v[76:79], v[160:163], v[216:219], v[76:79]
	v_mfma_f32_16x16x32_bf16 v[72:75], v[168:171], v[216:219], v[72:75]
	v_mfma_f32_16x16x32_bf16 v[124:127], v[164:167], v[196:199], v[124:127]
	v_mfma_f32_16x16x32_bf16 v[120:123], v[172:175], v[196:199], v[120:123]
	v_mfma_f32_16x16x32_bf16 v[108:111], v[164:167], v[204:207], v[108:111]
	v_mfma_f32_16x16x32_bf16 v[104:107], v[172:175], v[204:207], v[104:107]
	v_mfma_f32_16x16x32_bf16 v[92:95], v[164:167], v[212:215], v[92:95]
	v_mfma_f32_16x16x32_bf16 v[88:91], v[172:175], v[212:215], v[88:91]
	v_mfma_f32_16x16x32_bf16 v[76:79], v[164:167], v[220:223], v[76:79]
	v_mfma_f32_16x16x32_bf16 v[72:75], v[172:175], v[220:223], v[72:75]
	v_mfma_f32_16x16x32_bf16 v[116:119], v[176:179], v[192:195], v[116:119]
	v_mfma_f32_16x16x32_bf16 v[112:115], v[184:187], v[192:195], v[112:115]
	v_mfma_f32_16x16x32_bf16 v[100:103], v[176:179], v[200:203], v[100:103]
	v_mfma_f32_16x16x32_bf16 v[96:99], v[184:187], v[200:203], v[96:99]
	v_mfma_f32_16x16x32_bf16 v[84:87], v[176:179], v[208:211], v[84:87]
	v_mfma_f32_16x16x32_bf16 v[80:83], v[184:187], v[208:211], v[80:83]
	v_mfma_f32_16x16x32_bf16 v[68:71], v[176:179], v[216:219], v[68:71]
	v_mfma_f32_16x16x32_bf16 v[64:67], v[184:187], v[216:219], v[64:67]
	v_mfma_f32_16x16x32_bf16 v[116:119], v[180:183], v[196:199], v[116:119]
	v_mfma_f32_16x16x32_bf16 v[112:115], v[188:191], v[196:199], v[112:115]
	v_mfma_f32_16x16x32_bf16 v[100:103], v[180:183], v[204:207], v[100:103]
	v_mfma_f32_16x16x32_bf16 v[96:99], v[188:191], v[204:207], v[96:99]
	v_mfma_f32_16x16x32_bf16 v[84:87], v[180:183], v[212:215], v[84:87]
	v_mfma_f32_16x16x32_bf16 v[80:83], v[188:191], v[212:215], v[80:83]
	v_mfma_f32_16x16x32_bf16 v[68:71], v[180:183], v[220:223], v[68:71]
	v_mfma_f32_16x16x32_bf16 v[64:67], v[188:191], v[220:223], v[64:67]
	s_barrier
; template <class Epi, class Sched, class Hook = NoHook>
; __device__ __forceinline__ void gemm_phase_w(LAS unsigned char* lds, const Sched& S, const Epi& E, int wave_id, const Hook& HK = Hook()) {
;     ...
;         if constexpr (!SEG2) {
;             for (int tt = 0; tt < nt; tt += 2) {
;                 if constexpr (GATHER) { if (tt == nt - 2) {
;                     if (has_next) { gnxt_00 = S.grow_l(nxt, lds, nbuf, R0) + (unsigned)(C0 * 2); gnxt_01 = S.grow_l(nxt, lds, nbuf, R1) + (unsigned)(C1 * 2); gnxt_10 = S.grow_l(nxt, lds, nbuf, 128 + R0) + (unsigned)(C0 * 2); gnxt_11 = S.grow_l(nxt, lds, nbuf, 128 + R1) + (unsigned)(C1 * 2); }
;                     else { gnxt_00 = gcur_00; gnxt_01 = gcur_01; gnxt_10 = gcur_10; gnxt_11 = gcur_11; } } }
;                 PG_TRIP(tt, false, false, false);
;             }
	s_bitset1_b32 s71, 7
	s_add_i32 s23, s71, s23
	s_ashr_i32 s37, s23, 31
	s_add_u32 s36, s10, s23
	s_addc_u32 s37, s11, s37
	s_add_i32 s23, s74, s34
	v_lshl_add_u64 v[224:225], s[36:37], 0, v[130:131]
	s_mov_b32 m0, s23
	ds_read_b128 v[192:195], v158 offset:49152
	ds_read_b128 v[196:199], v158 offset:50176
	ds_read_b128 v[200:203], v158 offset:51200
	ds_read_b128 v[204:207], v158 offset:52224
	ds_read_b128 v[208:211], v158 offset:53248
	ds_read_b128 v[212:215], v158 offset:54272
	ds_read_b128 v[216:219], v158 offset:55296
	ds_read_b128 v[220:223], v158 offset:56320
	global_load_lds_dwordx4 v[224:225], off
	s_add_i32 m0, s23, 0x2000
	s_add_i32 s23, s71, s72
	v_lshl_add_u64 v[224:225], s[36:37], 0, v[132:133]
	s_ashr_i32 s37, s23, 31
	s_add_u32 s36, s10, s23
	s_addc_u32 s37, s11, s37
	s_add_i32 s23, s75, s34
	global_load_lds_dwordx4 v[224:225], off
	v_lshl_add_u64 v[224:225], s[36:37], 0, v[130:131]
	s_mov_b32 m0, s23
	s_add_i32 s71, s71, s22
	global_load_lds_dwordx4 v[224:225], off
	s_add_i32 m0, s23, 0x2000
	s_add_u32 s22, s28, s71
	v_lshl_add_u64 v[224:225], s[36:37], 0, v[132:133]
	s_addc_u32 s23, s29, 0
	global_load_lds_dwordx4 v[224:225], off
	v_lshl_add_u64 v[224:225], s[22:23], 0, v[130:131]
	s_mov_b32 m0, s42
	s_nop 0
	global_load_lds_dwordx4 v[224:225], off
	v_lshl_add_u64 v[224:225], s[22:23], 0, v[132:133]
	s_mov_b32 m0, s43
	s_nop 0
	global_load_lds_dwordx4 v[224:225], off
	s_waitcnt vmcnt(8)
	s_waitcnt lgkmcnt(0)
	s_barrier
	v_mfma_f32_16x16x32_bf16 v[60:63], v[160:163], v[192:195], v[60:63]
	v_mfma_f32_16x16x32_bf16 v[56:59], v[168:171], v[192:195], v[56:59]
	v_mfma_f32_16x16x32_bf16 v[44:47], v[160:163], v[200:203], v[44:47]
	v_mfma_f32_16x16x32_bf16 v[40:43], v[168:171], v[200:203], v[40:43]
	v_mfma_f32_16x16x32_bf16 v[28:31], v[160:163], v[208:211], v[28:31]
	v_mfma_f32_16x16x32_bf16 v[24:27], v[168:171], v[208:211], v[24:27]
	v_mfma_f32_16x16x32_bf16 v[12:15], v[160:163], v[216:219], v[12:15]
	v_mfma_f32_16x16x32_bf16 v[8:11], v[168:171], v[216:219], v[8:11]
	v_mfma_f32_16x16x32_bf16 v[60:63], v[164:167], v[196:199], v[60:63]
	v_mfma_f32_16x16x32_bf16 v[56:59], v[172:175], v[196:199], v[56:59]
	v_mfma_f32_16x16x32_bf16 v[44:47], v[164:167], v[204:207], v[44:47]
	v_mfma_f32_16x16x32_bf16 v[40:43], v[172:175], v[204:207], v[40:43]
	v_mfma_f32_16x16x32_bf16 v[28:31], v[164:167], v[212:215], v[28:31]
	v_mfma_f32_16x16x32_bf16 v[24:27], v[172:175], v[212:215], v[24:27]
	v_mfma_f32_16x16x32_bf16 v[12:15], v[164:167], v[220:223], v[12:15]
	v_mfma_f32_16x16x32_bf16 v[8:11], v[172:175], v[220:223], v[8:11]
	v_mfma_f32_16x16x32_bf16 v[52:55], v[176:179], v[192:195], v[52:55]
	v_mfma_f32_16x16x32_bf16 v[48:51], v[184:187], v[192:195], v[48:51]
	v_mfma_f32_16x16x32_bf16 v[36:39], v[176:179], v[200:203], v[36:39]
	v_mfma_f32_16x16x32_bf16 v[32:35], v[184:187], v[200:203], v[32:35]
	v_mfma_f32_16x16x32_bf16 v[20:23], v[176:179], v[208:211], v[20:23]
	v_mfma_f32_16x16x32_bf16 v[16:19], v[184:187], v[208:211], v[16:19]
	v_mfma_f32_16x16x32_bf16 v[4:7], v[176:179], v[216:219], v[4:7]
	v_mfma_f32_16x16x32_bf16 v[0:3], v[184:187], v[216:219], v[0:3]
	v_mfma_f32_16x16x32_bf16 v[52:55], v[180:183], v[196:199], v[52:55]
	v_mfma_f32_16x16x32_bf16 v[48:51], v[188:191], v[196:199], v[48:51]
	v_mfma_f32_16x16x32_bf16 v[36:39], v[180:183], v[204:207], v[36:39]
	v_mfma_f32_16x16x32_bf16 v[32:35], v[188:191], v[204:207], v[32:35]
	v_mfma_f32_16x16x32_bf16 v[20:23], v[180:183], v[212:215], v[20:23]
	v_mfma_f32_16x16x32_bf16 v[16:19], v[188:191], v[212:215], v[16:19]
	v_mfma_f32_16x16x32_bf16 v[4:7], v[180:183], v[220:223], v[4:7]
	v_mfma_f32_16x16x32_bf16 v[0:3], v[188:191], v[220:223], v[0:3]
	s_barrier
	s_addk_i32 s12, 0x100
	s_add_i32 s19, s19, 2
	s_cmp_gt_u32 s19, 13
	s_cbranch_scc0 .LBB0_1194
	s_and_b64 vcc, exec, s[0:1]
	s_cbranch_vccz .LBB0_1197
	s_barrier

.LBB0_1442:
	ds_read_b128 v[156:159], v153
	ds_read_b128 v[160:163], v153 offset:1024
	ds_read_b128 v[164:167], v153 offset:2048
	ds_read_b128 v[168:171], v153 offset:3072
	ds_read_b128 v[172:175], v154
	ds_read_b128 v[176:179], v154 offset:1024
	ds_read_b128 v[180:183], v154 offset:2048
	ds_read_b128 v[184:187], v154 offset:3072
	s_add_i32 s22, s61, s12
	s_add_u32 s66, s28, s22
	s_addc_u32 s67, s29, 0
	s_add_i32 m0, s33, 0xc000
	s_add_i32 s68, s33, 0xe000
	s_add_i32 s69, s12, 0xfffc0080
	s_cmp_eq_u32 s19, 12
	s_cselect_b32 s22, s58, s61
	s_cselect_b32 s23, s59, s62
	v_lshl_add_u64 v[220:221], s[66:67], 0, v[130:131]
	ds_read_b128 v[188:191], v155
	ds_read_b128 v[192:195], v155 offset:1024
	ds_read_b128 v[196:199], v155 offset:2048
	ds_read_b128 v[200:203], v155 offset:3072
	ds_read_b128 v[204:207], v155 offset:4096
	ds_read_b128 v[208:211], v155 offset:5120
	ds_read_b128 v[212:215], v155 offset:6144
	ds_read_b128 v[216:219], v155 offset:7168
	global_load_lds_dwordx4 v[220:221], off
	v_lshl_add_u64 v[220:221], s[66:67], 0, v[132:133]
	s_mov_b32 m0, s68
	s_nop 0
	global_load_lds_dwordx4 v[220:221], off
	s_waitcnt vmcnt(8)
	s_waitcnt lgkmcnt(0)
	s_barrier
	v_mfma_f32_16x16x32_bf16 v[124:127], v[156:159], v[188:191], v[124:127]
	v_mfma_f32_16x16x32_bf16 v[120:123], v[164:167], v[188:191], v[120:123]
	v_mfma_f32_16x16x32_bf16 v[108:111], v[156:159], v[196:199], v[108:111]
	v_mfma_f32_16x16x32_bf16 v[104:107], v[164:167], v[196:199], v[104:107]
	v_mfma_f32_16x16x32_bf16 v[92:95], v[156:159], v[204:207], v[92:95]
	v_mfma_f32_16x16x32_bf16 v[88:91], v[164:167], v[204:207], v[88:91]
	v_mfma_f32_16x16x32_bf16 v[76:79], v[156:159], v[212:215], v[76:79]
	v_mfma_f32_16x16x32_bf16 v[72:75], v[164:167], v[212:215], v[72:75]
	v_mfma_f32_16x16x32_bf16 v[124:127], v[160:163], v[192:195], v[124:127]
	v_mfma_f32_16x16x32_bf16 v[120:123], v[168:171], v[192:195], v[120:123]
	v_mfma_f32_16x16x32_bf16 v[108:111], v[160:163], v[200:203], v[108:111]
	v_mfma_f32_16x16x32_bf16 v[104:107], v[168:171], v[200:203], v[104:107]
	v_mfma_f32_16x16x32_bf16 v[92:95], v[160:163], v[208:211], v[92:95]
	v_mfma_f32_16x16x32_bf16 v[88:91], v[168:171], v[208:211], v[88:91]
	v_mfma_f32_16x16x32_bf16 v[76:79], v[160:163], v[216:219], v[76:79]
	v_mfma_f32_16x16x32_bf16 v[72:75], v[168:171], v[216:219], v[72:75]
	v_mfma_f32_16x16x32_bf16 v[116:119], v[172:175], v[188:191], v[116:119]
	v_mfma_f32_16x16x32_bf16 v[112:115], v[180:183], v[188:191], v[112:115]
	v_mfma_f32_16x16x32_bf16 v[100:103], v[172:175], v[196:199], v[100:103]
	v_mfma_f32_16x16x32_bf16 v[96:99], v[180:183], v[196:199], v[96:99]
	v_mfma_f32_16x16x32_bf16 v[84:87], v[172:175], v[204:207], v[84:87]
	v_mfma_f32_16x16x32_bf16 v[80:83], v[180:183], v[204:207], v[80:83]
	v_mfma_f32_16x16x32_bf16 v[68:71], v[172:175], v[212:215], v[68:71]
	v_mfma_f32_16x16x32_bf16 v[64:67], v[180:183], v[212:215], v[64:67]
	v_mfma_f32_16x16x32_bf16 v[116:119], v[176:179], v[192:195], v[116:119]
	v_mfma_f32_16x16x32_bf16 v[112:115], v[184:187], v[192:195], v[112:115]
	v_mfma_f32_16x16x32_bf16 v[100:103], v[176:179], v[200:203], v[100:103]
	v_mfma_f32_16x16x32_bf16 v[96:99], v[184:187], v[200:203], v[96:99]
	v_mfma_f32_16x16x32_bf16 v[84:87], v[176:179], v[208:211], v[84:87]
	v_mfma_f32_16x16x32_bf16 v[80:83], v[184:187], v[208:211], v[80:83]
	v_mfma_f32_16x16x32_bf16 v[68:71], v[176:179], v[216:219], v[68:71]
	v_mfma_f32_16x16x32_bf16 v[64:67], v[184:187], v[216:219], v[64:67]
	s_barrier
	s_cselect_b32 s68, 0, s69
	s_add_i32 s66, s68, s23
	s_ashr_i32 s67, s66, 31
	s_add_u32 s66, s10, s66
	s_addc_u32 s67, s11, s67
	s_add_i32 s69, s37, s34
	v_lshl_add_u64 v[220:221], s[66:67], 0, v[130:131]
	s_mov_b32 m0, s69
	ds_read_b128 v[188:191], v155 offset:16384
	ds_read_b128 v[192:195], v155 offset:17408
	ds_read_b128 v[196:199], v155 offset:18432
	ds_read_b128 v[200:203], v155 offset:19456
	ds_read_b128 v[204:207], v155 offset:20480
	ds_read_b128 v[208:211], v155 offset:21504
	ds_read_b128 v[212:215], v155 offset:22528
	ds_read_b128 v[216:219], v155 offset:23552
	global_load_lds_dwordx4 v[220:221], off
	s_add_i32 m0, s69, 0x2000
	s_add_i32 s69, s23, 0x40000
	v_lshl_add_u64 v[220:221], s[66:67], 0, v[132:133]
	s_add_i32 s66, s69, s68
	s_ashr_i32 s67, s66, 31
	s_add_u32 s66, s10, s66
	s_addc_u32 s67, s11, s67
	s_add_i32 s70, s38, s34
	global_load_lds_dwordx4 v[220:221], off
	v_lshl_add_u64 v[220:221], s[66:67], 0, v[130:131]
	s_mov_b32 m0, s70
	s_nop 0
	global_load_lds_dwordx4 v[220:221], off
	s_add_i32 m0, s70, 0x2000
	s_add_i32 s70, s68, s22
	v_lshl_add_u64 v[220:221], s[66:67], 0, v[132:133]
	s_add_u32 s66, s28, s70
	s_addc_u32 s67, s29, 0
	global_load_lds_dwordx4 v[220:221], off
	v_lshl_add_u64 v[220:221], s[66:67], 0, v[130:131]
	s_mov_b32 m0, s33
	s_nop 0
	global_load_lds_dwordx4 v[220:221], off
	v_lshl_add_u64 v[220:221], s[66:67], 0, v[132:133]
	s_mov_b32 m0, s40
	s_nop 0
	global_load_lds_dwordx4 v[220:221], off
	s_waitcnt vmcnt(8)
	s_waitcnt lgkmcnt(0)
	s_barrier
	v_mfma_f32_16x16x32_bf16 v[60:63], v[156:159], v[188:191], v[60:63]
	v_mfma_f32_16x16x32_bf16 v[56:59], v[164:167], v[188:191], v[56:59]
	v_mfma_f32_16x16x32_bf16 v[44:47], v[156:159], v[196:199], v[44:47]
	v_mfma_f32_16x16x32_bf16 v[40:43], v[164:167], v[196:199], v[40:43]
	v_mfma_f32_16x16x32_bf16 v[28:31], v[156:159], v[204:207], v[28:31]
	v_mfma_f32_16x16x32_bf16 v[24:27], v[164:167], v[204:207], v[24:27]
	v_mfma_f32_16x16x32_bf16 v[12:15], v[156:159], v[212:215], v[12:15]
	v_mfma_f32_16x16x32_bf16 v[8:11], v[164:167], v[212:215], v[8:11]
	v_mfma_f32_16x16x32_bf16 v[60:63], v[160:163], v[192:195], v[60:63]
	v_mfma_f32_16x16x32_bf16 v[56:59], v[168:171], v[192:195], v[56:59]
	v_mfma_f32_16x16x32_bf16 v[44:47], v[160:163], v[200:203], v[44:47]
	v_mfma_f32_16x16x32_bf16 v[40:43], v[168:171], v[200:203], v[40:43]
	v_mfma_f32_16x16x32_bf16 v[28:31], v[160:163], v[208:211], v[28:31]
	v_mfma_f32_16x16x32_bf16 v[24:27], v[168:171], v[208:211], v[24:27]
	v_mfma_f32_16x16x32_bf16 v[12:15], v[160:163], v[216:219], v[12:15]
	v_mfma_f32_16x16x32_bf16 v[8:11], v[168:171], v[216:219], v[8:11]
	v_mfma_f32_16x16x32_bf16 v[52:55], v[172:175], v[188:191], v[52:55]
	v_mfma_f32_16x16x32_bf16 v[48:51], v[180:183], v[188:191], v[48:51]
	v_mfma_f32_16x16x32_bf16 v[36:39], v[172:175], v[196:199], v[36:39]
	v_mfma_f32_16x16x32_bf16 v[32:35], v[180:183], v[196:199], v[32:35]
	v_mfma_f32_16x16x32_bf16 v[20:23], v[172:175], v[204:207], v[20:23]
	v_mfma_f32_16x16x32_bf16 v[16:19], v[180:183], v[204:207], v[16:19]
	v_mfma_f32_16x16x32_bf16 v[4:7], v[172:175], v[212:215], v[4:7]
	v_mfma_f32_16x16x32_bf16 v[0:3], v[180:183], v[212:215], v[0:3]
	v_mfma_f32_16x16x32_bf16 v[52:55], v[176:179], v[192:195], v[52:55]
	v_mfma_f32_16x16x32_bf16 v[48:51], v[184:187], v[192:195], v[48:51]
	v_mfma_f32_16x16x32_bf16 v[36:39], v[176:179], v[200:203], v[36:39]
	v_mfma_f32_16x16x32_bf16 v[32:35], v[184:187], v[200:203], v[32:35]
	v_mfma_f32_16x16x32_bf16 v[20:23], v[176:179], v[208:211], v[20:23]
	v_mfma_f32_16x16x32_bf16 v[16:19], v[184:187], v[208:211], v[16:19]
	v_mfma_f32_16x16x32_bf16 v[4:7], v[176:179], v[216:219], v[4:7]
	v_mfma_f32_16x16x32_bf16 v[0:3], v[184:187], v[216:219], v[0:3]
	s_barrier
	s_add_i32 s71, 0, 0x18000
	s_add_i32 s72, 0, 0x1c000
	v_add_u32_e32 v168, s71, v137
	v_add_u32_e32 v184, s72, v137
	ds_read_b128 v[156:159], v168
	ds_read_b128 v[160:163], v168 offset:1024
	ds_read_b128 v[164:167], v168 offset:2048
	ds_read_b128 v[168:171], v168 offset:3072
	ds_read_b128 v[172:175], v184
	ds_read_b128 v[176:179], v184 offset:1024
	ds_read_b128 v[180:183], v184 offset:2048
	ds_read_b128 v[184:187], v184 offset:3072
	s_add_i32 s70, s70, 0x40000
	s_add_u32 s66, s28, s70
	s_addc_u32 s67, s29, 0
	s_mov_b32 m0, s41
	v_lshl_add_u64 v[220:221], s[66:67], 0, v[130:131]
	ds_read_b128 v[188:191], v155 offset:32768
	ds_read_b128 v[192:195], v155 offset:33792
	ds_read_b128 v[196:199], v155 offset:34816
	ds_read_b128 v[200:203], v155 offset:35840
	ds_read_b128 v[204:207], v155 offset:36864
	ds_read_b128 v[208:211], v155 offset:37888
	ds_read_b128 v[212:215], v155 offset:38912
	ds_read_b128 v[216:219], v155 offset:39936
	global_load_lds_dwordx4 v[220:221], off
	v_lshl_add_u64 v[220:221], s[66:67], 0, v[132:133]
	s_mov_b32 m0, s42
	s_nop 0
	global_load_lds_dwordx4 v[220:221], off
	s_waitcnt vmcnt(8)
	s_waitcnt lgkmcnt(0)
	s_barrier
	v_mfma_f32_16x16x32_bf16 v[124:127], v[156:159], v[188:191], v[124:127]
	v_mfma_f32_16x16x32_bf16 v[120:123], v[164:167], v[188:191], v[120:123]
	v_mfma_f32_16x16x32_bf16 v[108:111], v[156:159], v[196:199], v[108:111]
	v_mfma_f32_16x16x32_bf16 v[104:107], v[164:167], v[196:199], v[104:107]
	v_mfma_f32_16x16x32_bf16 v[92:95], v[156:159], v[204:207], v[92:95]
	v_mfma_f32_16x16x32_bf16 v[88:91], v[164:167], v[204:207], v[88:91]
	v_mfma_f32_16x16x32_bf16 v[76:79], v[156:159], v[212:215], v[76:79]
	v_mfma_f32_16x16x32_bf16 v[72:75], v[164:167], v[212:215], v[72:75]
	v_mfma_f32_16x16x32_bf16 v[124:127], v[160:163], v[192:195], v[124:127]
	v_mfma_f32_16x16x32_bf16 v[120:123], v[168:171], v[192:195], v[120:123]
	v_mfma_f32_16x16x32_bf16 v[108:111], v[160:163], v[200:203], v[108:111]
	v_mfma_f32_16x16x32_bf16 v[104:107], v[168:171], v[200:203], v[104:107]
	v_mfma_f32_16x16x32_bf16 v[92:95], v[160:163], v[208:211], v[92:95]
	v_mfma_f32_16x16x32_bf16 v[88:91], v[168:171], v[208:211], v[88:91]
	v_mfma_f32_16x16x32_bf16 v[76:79], v[160:163], v[216:219], v[76:79]
	v_mfma_f32_16x16x32_bf16 v[72:75], v[168:171], v[216:219], v[72:75]
	v_mfma_f32_16x16x32_bf16 v[116:119], v[172:175], v[188:191], v[116:119]
	v_mfma_f32_16x16x32_bf16 v[112:115], v[180:183], v[188:191], v[112:115]
	v_mfma_f32_16x16x32_bf16 v[100:103], v[172:175], v[196:199], v[100:103]
	v_mfma_f32_16x16x32_bf16 v[96:99], v[180:183], v[196:199], v[96:99]
	v_mfma_f32_16x16x32_bf16 v[84:87], v[172:175], v[204:207], v[84:87]
	v_mfma_f32_16x16x32_bf16 v[80:83], v[180:183], v[204:207], v[80:83]
	v_mfma_f32_16x16x32_bf16 v[68:71], v[172:175], v[212:215], v[68:71]
	v_mfma_f32_16x16x32_bf16 v[64:67], v[180:183], v[212:215], v[64:67]
	v_mfma_f32_16x16x32_bf16 v[116:119], v[176:179], v[192:195], v[116:119]
	v_mfma_f32_16x16x32_bf16 v[112:115], v[184:187], v[192:195], v[112:115]
	v_mfma_f32_16x16x32_bf16 v[100:103], v[176:179], v[200:203], v[100:103]
	v_mfma_f32_16x16x32_bf16 v[96:99], v[184:187], v[200:203], v[96:99]
	v_mfma_f32_16x16x32_bf16 v[84:87], v[176:179], v[208:211], v[84:87]
	v_mfma_f32_16x16x32_bf16 v[80:83], v[184:187], v[208:211], v[80:83]
	v_mfma_f32_16x16x32_bf16 v[68:71], v[176:179], v[216:219], v[68:71]
	v_mfma_f32_16x16x32_bf16 v[64:67], v[184:187], v[216:219], v[64:67]
	s_barrier
; #define PG_BAR __builtin_amdgcn_s_barrier()
; template <class Epi, class Sched, class Hook = NoHook>
; __device__ __forceinline__ void gemm_phase_w(LAS unsigned char* lds, const Sched& S, const Epi& E, int wave_id, const Hook& HK = Hook()) {
;     ...
;         if constexpr (!SEG2) {
;             for (int tt = 0; tt < nt; tt += 2) {
;                 if constexpr (GATHER) { if (tt == nt - 2) {
;                     if (has_next) { gnxt_00 = S.grow_l(nxt, lds, nbuf, R0) + (unsigned)(C0 * 2); gnxt_01 = S.grow_l(nxt, lds, nbuf, R1) + (unsigned)(C1 * 2); gnxt_10 = S.grow_l(nxt, lds, nbuf, 128 + R0) + (unsigned)(C0 * 2); gnxt_11 = S.grow_l(nxt, lds, nbuf, 128 + R1) + (unsigned)(C1 * 2); }
;                     else { gnxt_00 = gcur_00; gnxt_01 = gcur_01; gnxt_10 = gcur_10; gnxt_11 = gcur_11; } } }
;                 PG_TRIP(tt, false, false, false);
;             }
;         } else {
;             for (int tt = 0; tt < nt - 4; tt += 2) PG_TRIP(tt, false, false, false);
;             PG_TRIP(nt - 4, false, true, false);
;             PG_TRIP(nt - 2, true, false, true);
;         }
;     ...
;         if (wr == 0) PG_BAR;
	s_bitset1_b32 s68, 7
	s_add_i32 s23, s68, s23
	s_ashr_i32 s67, s23, 31
	s_add_u32 s66, s10, s23
	s_addc_u32 s67, s11, s67
	s_add_i32 s23, s71, s34
	v_lshl_add_u64 v[220:221], s[66:67], 0, v[130:131]
	s_mov_b32 m0, s23
	ds_read_b128 v[188:191], v155 offset:49152
	ds_read_b128 v[192:195], v155 offset:50176
	ds_read_b128 v[196:199], v155 offset:51200
	ds_read_b128 v[200:203], v155 offset:52224
	ds_read_b128 v[204:207], v155 offset:53248
	ds_read_b128 v[208:211], v155 offset:54272
	ds_read_b128 v[212:215], v155 offset:55296
	ds_read_b128 v[216:219], v155 offset:56320
	global_load_lds_dwordx4 v[220:221], off
	s_add_i32 m0, s23, 0x2000
	s_add_i32 s23, s68, s69
	v_lshl_add_u64 v[220:221], s[66:67], 0, v[132:133]
	s_ashr_i32 s67, s23, 31
	s_add_u32 s66, s10, s23
	s_addc_u32 s67, s11, s67
	s_add_i32 s23, s72, s34
	global_load_lds_dwordx4 v[220:221], off
	v_lshl_add_u64 v[220:221], s[66:67], 0, v[130:131]
	s_mov_b32 m0, s23
	s_add_i32 s68, s68, s22
	global_load_lds_dwordx4 v[220:221], off
	s_add_i32 m0, s23, 0x2000
	s_add_u32 s22, s28, s68
	v_lshl_add_u64 v[220:221], s[66:67], 0, v[132:133]
	s_addc_u32 s23, s29, 0
	global_load_lds_dwordx4 v[220:221], off
	v_lshl_add_u64 v[220:221], s[22:23], 0, v[130:131]
	s_mov_b32 m0, s39
	s_nop 0
	global_load_lds_dwordx4 v[220:221], off
	v_lshl_add_u64 v[220:221], s[22:23], 0, v[132:133]
	s_mov_b32 m0, s43
	s_nop 0
	global_load_lds_dwordx4 v[220:221], off
	s_waitcnt vmcnt(8)
	s_waitcnt lgkmcnt(0)
	s_barrier
	v_mfma_f32_16x16x32_bf16 v[60:63], v[156:159], v[188:191], v[60:63]
	v_mfma_f32_16x16x32_bf16 v[56:59], v[164:167], v[188:191], v[56:59]
	v_mfma_f32_16x16x32_bf16 v[44:47], v[156:159], v[196:199], v[44:47]
	v_mfma_f32_16x16x32_bf16 v[40:43], v[164:167], v[196:199], v[40:43]
	v_mfma_f32_16x16x32_bf16 v[28:31], v[156:159], v[204:207], v[28:31]
	v_mfma_f32_16x16x32_bf16 v[24:27], v[164:167], v[204:207], v[24:27]
	v_mfma_f32_16x16x32_bf16 v[12:15], v[156:159], v[212:215], v[12:15]
	v_mfma_f32_16x16x32_bf16 v[8:11], v[164:167], v[212:215], v[8:11]
	v_mfma_f32_16x16x32_bf16 v[60:63], v[160:163], v[192:195], v[60:63]
	v_mfma_f32_16x16x32_bf16 v[56:59], v[168:171], v[192:195], v[56:59]
	v_mfma_f32_16x16x32_bf16 v[44:47], v[160:163], v[200:203], v[44:47]
	v_mfma_f32_16x16x32_bf16 v[40:43], v[168:171], v[200:203], v[40:43]
	v_mfma_f32_16x16x32_bf16 v[28:31], v[160:163], v[208:211], v[28:31]
	v_mfma_f32_16x16x32_bf16 v[24:27], v[168:171], v[208:211], v[24:27]
	v_mfma_f32_16x16x32_bf16 v[12:15], v[160:163], v[216:219], v[12:15]
	v_mfma_f32_16x16x32_bf16 v[8:11], v[168:171], v[216:219], v[8:11]
	v_mfma_f32_16x16x32_bf16 v[52:55], v[172:175], v[188:191], v[52:55]
	v_mfma_f32_16x16x32_bf16 v[48:51], v[180:183], v[188:191], v[48:51]
	v_mfma_f32_16x16x32_bf16 v[36:39], v[172:175], v[196:199], v[36:39]
	v_mfma_f32_16x16x32_bf16 v[32:35], v[180:183], v[196:199], v[32:35]
	v_mfma_f32_16x16x32_bf16 v[20:23], v[172:175], v[204:207], v[20:23]
	v_mfma_f32_16x16x32_bf16 v[16:19], v[180:183], v[204:207], v[16:19]
	v_mfma_f32_16x16x32_bf16 v[4:7], v[172:175], v[212:215], v[4:7]
	v_mfma_f32_16x16x32_bf16 v[0:3], v[180:183], v[212:215], v[0:3]
	v_mfma_f32_16x16x32_bf16 v[52:55], v[176:179], v[192:195], v[52:55]
	v_mfma_f32_16x16x32_bf16 v[48:51], v[184:187], v[192:195], v[48:51]
	v_mfma_f32_16x16x32_bf16 v[36:39], v[176:179], v[200:203], v[36:39]
	v_mfma_f32_16x16x32_bf16 v[32:35], v[184:187], v[200:203], v[32:35]
	v_mfma_f32_16x16x32_bf16 v[20:23], v[176:179], v[208:211], v[20:23]
	v_mfma_f32_16x16x32_bf16 v[16:19], v[184:187], v[208:211], v[16:19]
	v_mfma_f32_16x16x32_bf16 v[4:7], v[176:179], v[216:219], v[4:7]
	v_mfma_f32_16x16x32_bf16 v[0:3], v[184:187], v[216:219], v[0:3]
	s_barrier
	s_addk_i32 s12, 0x100
	s_add_i32 s19, s19, 2
	s_cmp_gt_u32 s19, 13
	s_cbranch_scc0 .LBB0_1442
	s_and_b64 vcc, exec, s[0:1]
	s_cbranch_vccz .LBB0_1445
	s_barrier

.LBB0_1585:
	ds_read_b128 v[82:85], v75
	ds_read_b128 v[86:89], v75 offset:1024
	ds_read_b128 v[90:93], v75 offset:2048
	ds_read_b128 v[94:97], v75 offset:3072
	s_add_i32 s61, s39, s20
	s_add_u32 s62, s8, s61
	s_addc_u32 s63, s9, 0
	s_add_i32 s61, s20, 0xfffe0080
	s_cmp_eq_u32 s21, 4
	s_cselect_b32 s66, s59, s39
	s_cselect_b32 s67, s51, s60
	s_cselect_b32 s68, s58, s38
	s_mov_b32 m0, s40
	v_lshl_add_u64 v[130:131], s[62:63], 0, v[64:65]
	ds_read_b128 v[98:101], v76
	ds_read_b128 v[102:105], v76 offset:1024
	ds_read_b128 v[106:109], v76 offset:2048
	ds_read_b128 v[110:113], v76 offset:3072
	ds_read_b128 v[114:117], v76 offset:4096
	ds_read_b128 v[118:121], v76 offset:5120
	ds_read_b128 v[122:125], v76 offset:6144
	ds_read_b128 v[126:129], v76 offset:7168
	global_load_lds_dwordx4 v[130:131], off
	v_lshl_add_u64 v[130:131], s[62:63], 0, v[66:67]
	s_mov_b32 m0, s41
	s_nop 0
	global_load_lds_dwordx4 v[130:131], off
	s_waitcnt vmcnt(8)
	s_waitcnt lgkmcnt(0)
	s_barrier
	v_mfma_f32_16x16x32_bf16 v[60:63], v[82:85], v[98:101], v[60:63]
	v_mfma_f32_16x16x32_bf16 v[56:59], v[90:93], v[98:101], v[56:59]
	v_mfma_f32_16x16x32_bf16 v[52:55], v[82:85], v[106:109], v[52:55]
	v_mfma_f32_16x16x32_bf16 v[48:51], v[90:93], v[106:109], v[48:51]
	v_mfma_f32_16x16x32_bf16 v[44:47], v[82:85], v[114:117], v[44:47]
	v_mfma_f32_16x16x32_bf16 v[40:43], v[90:93], v[114:117], v[40:43]
	v_mfma_f32_16x16x32_bf16 v[36:39], v[82:85], v[122:125], v[36:39]
	v_mfma_f32_16x16x32_bf16 v[32:35], v[90:93], v[122:125], v[32:35]
	v_mfma_f32_16x16x32_bf16 v[60:63], v[86:89], v[102:105], v[60:63]
	v_mfma_f32_16x16x32_bf16 v[56:59], v[94:97], v[102:105], v[56:59]
	v_mfma_f32_16x16x32_bf16 v[52:55], v[86:89], v[110:113], v[52:55]
	v_mfma_f32_16x16x32_bf16 v[48:51], v[94:97], v[110:113], v[48:51]
	v_mfma_f32_16x16x32_bf16 v[44:47], v[86:89], v[118:121], v[44:47]
	v_mfma_f32_16x16x32_bf16 v[40:43], v[94:97], v[118:121], v[40:43]
	v_mfma_f32_16x16x32_bf16 v[36:39], v[86:89], v[126:129], v[36:39]
	v_mfma_f32_16x16x32_bf16 v[32:35], v[94:97], v[126:129], v[32:35]
	s_barrier
	s_cselect_b32 s61, 0, s61
	s_add_i32 s62, s61, s68
	s_ashr_i32 s63, s62, 31
	s_add_u32 s62, s3, s62
	s_addc_u32 s63, s22, s63
	s_mov_b32 m0, s42
	v_lshl_add_u64 v[130:131], s[62:63], 0, v[64:65]
	s_add_i32 s67, s68, s67
	ds_read_b128 v[98:101], v76 offset:16384
	ds_read_b128 v[102:105], v76 offset:17408
	ds_read_b128 v[106:109], v76 offset:18432
	ds_read_b128 v[110:113], v76 offset:19456
	ds_read_b128 v[114:117], v76 offset:20480
	ds_read_b128 v[118:121], v76 offset:21504
	ds_read_b128 v[122:125], v76 offset:22528
	ds_read_b128 v[126:129], v76 offset:23552
	global_load_lds_dwordx4 v[130:131], off
	v_lshl_add_u64 v[130:131], s[62:63], 0, v[66:67]
	s_add_i32 s62, s67, s61
	s_ashr_i32 s63, s62, 31
	s_add_u32 s62, s3, s62
	s_mov_b32 m0, s43
	s_addc_u32 s63, s22, s63
	global_load_lds_dwordx4 v[130:131], off
	v_lshl_add_u64 v[130:131], s[62:63], 0, v[64:65]
	s_mov_b32 m0, s24
	s_add_i32 s69, s61, s66
	global_load_lds_dwordx4 v[130:131], off
	v_lshl_add_u64 v[130:131], s[62:63], 0, v[66:67]
	s_add_u32 s62, s8, s69
	s_mov_b32 m0, s25
	s_addc_u32 s63, s9, 0
	global_load_lds_dwordx4 v[130:131], off
	v_lshl_add_u64 v[130:131], s[62:63], 0, v[64:65]
	s_mov_b32 m0, s23
	s_nop 0
	global_load_lds_dwordx4 v[130:131], off
	v_lshl_add_u64 v[130:131], s[62:63], 0, v[66:67]
	s_mov_b32 m0, s28
	s_nop 0
	global_load_lds_dwordx4 v[130:131], off
	s_waitcnt vmcnt(8)
	s_waitcnt lgkmcnt(0)
	s_barrier
	v_mfma_f32_16x16x32_bf16 v[28:31], v[82:85], v[98:101], v[28:31]
	v_mfma_f32_16x16x32_bf16 v[24:27], v[90:93], v[98:101], v[24:27]
	v_mfma_f32_16x16x32_bf16 v[20:23], v[82:85], v[106:109], v[20:23]
	v_mfma_f32_16x16x32_bf16 v[16:19], v[90:93], v[106:109], v[16:19]
	v_mfma_f32_16x16x32_bf16 v[12:15], v[82:85], v[114:117], v[12:15]
	v_mfma_f32_16x16x32_bf16 v[8:11], v[90:93], v[114:117], v[8:11]
	v_mfma_f32_16x16x32_bf16 v[4:7], v[82:85], v[122:125], v[4:7]
	v_mfma_f32_16x16x32_bf16 v[0:3], v[90:93], v[122:125], v[0:3]
	v_mfma_f32_16x16x32_bf16 v[28:31], v[86:89], v[102:105], v[28:31]
	v_mfma_f32_16x16x32_bf16 v[24:27], v[94:97], v[102:105], v[24:27]
	v_mfma_f32_16x16x32_bf16 v[20:23], v[86:89], v[110:113], v[20:23]
	v_mfma_f32_16x16x32_bf16 v[16:19], v[94:97], v[110:113], v[16:19]
	v_mfma_f32_16x16x32_bf16 v[12:15], v[86:89], v[118:121], v[12:15]
	v_mfma_f32_16x16x32_bf16 v[8:11], v[94:97], v[118:121], v[8:11]
	v_mfma_f32_16x16x32_bf16 v[4:7], v[86:89], v[126:129], v[4:7]
	v_mfma_f32_16x16x32_bf16 v[0:3], v[94:97], v[126:129], v[0:3]
	s_barrier
; #define PG_BAR __builtin_amdgcn_s_barrier()
; template <class Epi, class Sched, class Hook = NoHook>
; __device__ __forceinline__ void gemm_phase_w(LAS unsigned char* lds, const Sched& S, const Epi& E, int wave_id, const Hook& HK = Hook()) {
;     ...
;         if constexpr (!SEG2) {
;             for (int tt = 0; tt < nt; tt += 2) {
;                 if constexpr (GATHER) { if (tt == nt - 2) {
;                     if (has_next) { gnxt_00 = S.grow_l(nxt, lds, nbuf, R0) + (unsigned)(C0 * 2); gnxt_01 = S.grow_l(nxt, lds, nbuf, R1) + (unsigned)(C1 * 2); gnxt_10 = S.grow_l(nxt, lds, nbuf, 128 + R0) + (unsigned)(C0 * 2); gnxt_11 = S.grow_l(nxt, lds, nbuf, 128 + R1) + (unsigned)(C1 * 2); }
;                     else { gnxt_00 = gcur_00; gnxt_01 = gcur_01; gnxt_10 = gcur_10; gnxt_11 = gcur_11; } } }
;                 PG_TRIP(tt, false, false, false);
;             }
;         } else {
;             for (int tt = 0; tt < nt - 4; tt += 2) PG_TRIP(tt, false, false, false);
;             PG_TRIP(nt - 4, false, true, false);
;             PG_TRIP(nt - 2, true, false, true);
;         }
;     ...
;         if (wr == 0) PG_BAR;
	ds_read_b128 v[82:85], v81
	ds_read_b128 v[86:89], v81 offset:1024
	ds_read_b128 v[90:93], v81 offset:2048
	ds_read_b128 v[94:97], v81 offset:3072
	s_add_i32 s69, s69, 0x20000
	s_add_u32 s62, s8, s69
	s_addc_u32 s63, s9, 0
	s_mov_b32 m0, s29
	v_lshl_add_u64 v[130:131], s[62:63], 0, v[64:65]
	ds_read_b128 v[98:101], v76 offset:32768
	ds_read_b128 v[102:105], v76 offset:33792
	ds_read_b128 v[106:109], v76 offset:34816
	ds_read_b128 v[110:113], v76 offset:35840
	ds_read_b128 v[114:117], v76 offset:36864
	ds_read_b128 v[118:121], v76 offset:37888
	ds_read_b128 v[122:125], v76 offset:38912
	ds_read_b128 v[126:129], v76 offset:39936
	global_load_lds_dwordx4 v[130:131], off
	v_lshl_add_u64 v[130:131], s[62:63], 0, v[66:67]
	s_mov_b32 m0, s30
	s_nop 0
	global_load_lds_dwordx4 v[130:131], off
	s_waitcnt vmcnt(8)
	s_waitcnt lgkmcnt(0)
	s_barrier
	v_mfma_f32_16x16x32_bf16 v[60:63], v[82:85], v[98:101], v[60:63]
	v_mfma_f32_16x16x32_bf16 v[56:59], v[90:93], v[98:101], v[56:59]
	v_mfma_f32_16x16x32_bf16 v[52:55], v[82:85], v[106:109], v[52:55]
	v_mfma_f32_16x16x32_bf16 v[48:51], v[90:93], v[106:109], v[48:51]
	v_mfma_f32_16x16x32_bf16 v[44:47], v[82:85], v[114:117], v[44:47]
	v_mfma_f32_16x16x32_bf16 v[40:43], v[90:93], v[114:117], v[40:43]
	v_mfma_f32_16x16x32_bf16 v[36:39], v[82:85], v[122:125], v[36:39]
	v_mfma_f32_16x16x32_bf16 v[32:35], v[90:93], v[122:125], v[32:35]
	v_mfma_f32_16x16x32_bf16 v[60:63], v[86:89], v[102:105], v[60:63]
	v_mfma_f32_16x16x32_bf16 v[56:59], v[94:97], v[102:105], v[56:59]
	v_mfma_f32_16x16x32_bf16 v[52:55], v[86:89], v[110:113], v[52:55]
	v_mfma_f32_16x16x32_bf16 v[48:51], v[94:97], v[110:113], v[48:51]
	v_mfma_f32_16x16x32_bf16 v[44:47], v[86:89], v[118:121], v[44:47]
	v_mfma_f32_16x16x32_bf16 v[40:43], v[94:97], v[118:121], v[40:43]
	v_mfma_f32_16x16x32_bf16 v[36:39], v[86:89], v[126:129], v[36:39]
	v_mfma_f32_16x16x32_bf16 v[32:35], v[94:97], v[126:129], v[32:35]
	s_barrier
	s_bitset1_b32 s61, 7
	s_add_i32 s62, s61, s68
	s_ashr_i32 s63, s62, 31
	s_add_u32 s62, s3, s62
	s_addc_u32 s63, s22, s63
	s_mov_b32 m0, s44
	v_lshl_add_u64 v[130:131], s[62:63], 0, v[64:65]
	ds_read_b128 v[98:101], v76 offset:49152
	ds_read_b128 v[102:105], v76 offset:50176
	ds_read_b128 v[106:109], v76 offset:51200
	ds_read_b128 v[110:113], v76 offset:52224
	ds_read_b128 v[114:117], v76 offset:53248
	ds_read_b128 v[118:121], v76 offset:54272
	ds_read_b128 v[122:125], v76 offset:55296
	ds_read_b128 v[126:129], v76 offset:56320
	global_load_lds_dwordx4 v[130:131], off
	v_lshl_add_u64 v[130:131], s[62:63], 0, v[66:67]
	s_add_i32 s62, s61, s67
	s_ashr_i32 s63, s62, 31
	s_add_u32 s62, s3, s62
	s_mov_b32 m0, s45
	s_addc_u32 s63, s22, s63
	global_load_lds_dwordx4 v[130:131], off
	v_lshl_add_u64 v[130:131], s[62:63], 0, v[64:65]
	s_mov_b32 m0, s36
	s_add_i32 s61, s61, s66
	global_load_lds_dwordx4 v[130:131], off
	v_lshl_add_u64 v[130:131], s[62:63], 0, v[66:67]
	s_add_u32 s62, s8, s61
	s_mov_b32 m0, s37
	s_addc_u32 s63, s9, 0
	global_load_lds_dwordx4 v[130:131], off
	v_lshl_add_u64 v[130:131], s[62:63], 0, v[64:65]
	s_mov_b32 m0, s34
	s_nop 0
	global_load_lds_dwordx4 v[130:131], off
	v_lshl_add_u64 v[130:131], s[62:63], 0, v[66:67]
	s_mov_b32 m0, s35
	s_nop 0
	global_load_lds_dwordx4 v[130:131], off
	s_waitcnt vmcnt(8)
	s_waitcnt lgkmcnt(0)
	s_barrier
	v_mfma_f32_16x16x32_bf16 v[28:31], v[82:85], v[98:101], v[28:31]
	v_mfma_f32_16x16x32_bf16 v[24:27], v[90:93], v[98:101], v[24:27]
	v_mfma_f32_16x16x32_bf16 v[20:23], v[82:85], v[106:109], v[20:23]
	v_mfma_f32_16x16x32_bf16 v[16:19], v[90:93], v[106:109], v[16:19]
	v_mfma_f32_16x16x32_bf16 v[12:15], v[82:85], v[114:117], v[12:15]
	v_mfma_f32_16x16x32_bf16 v[8:11], v[90:93], v[114:117], v[8:11]
	v_mfma_f32_16x16x32_bf16 v[4:7], v[82:85], v[122:125], v[4:7]
	v_mfma_f32_16x16x32_bf16 v[0:3], v[90:93], v[122:125], v[0:3]
	v_mfma_f32_16x16x32_bf16 v[28:31], v[86:89], v[102:105], v[28:31]
	v_mfma_f32_16x16x32_bf16 v[24:27], v[94:97], v[102:105], v[24:27]
	v_mfma_f32_16x16x32_bf16 v[20:23], v[86:89], v[110:113], v[20:23]
	v_mfma_f32_16x16x32_bf16 v[16:19], v[94:97], v[110:113], v[16:19]
	v_mfma_f32_16x16x32_bf16 v[12:15], v[86:89], v[118:121], v[12:15]
	v_mfma_f32_16x16x32_bf16 v[8:11], v[94:97], v[118:121], v[8:11]
	v_mfma_f32_16x16x32_bf16 v[4:7], v[86:89], v[126:129], v[4:7]
	v_mfma_f32_16x16x32_bf16 v[0:3], v[94:97], v[126:129], v[0:3]
	s_barrier
	s_addk_i32 s20, 0x100
	s_add_i32 s21, s21, 2
	s_cmp_gt_u32 s21, 5
	s_cbranch_scc0 .LBB0_1585
	s_and_b64 vcc, exec, s[16:17]
	s_cbranch_vccz .LBB0_1590
	s_barrier
	s_andn2_b64 vcc, exec, s[6:7]
	s_mov_b64 s[20:21], -1
	s_cbranch_vccz .LBB0_1591

.LBB0_1776:
	s_add_i32 s27, 0, 0x10000
	s_add_i32 s59, 0, 0x14000
	v_add_u32_e32 v128, s27, v171
	v_add_u32_e32 v129, s59, v171
	ds_read_b128 v[130:133], v128
	ds_read_b128 v[162:165], v128 offset:1024
	ds_read_b128 v[178:181], v128 offset:2048
	ds_read_b128 v[182:185], v128 offset:3072
	ds_read_b128 v[186:189], v129
	ds_read_b128 v[190:193], v129 offset:1024
	ds_read_b128 v[194:197], v129 offset:2048
	ds_read_b128 v[198:201], v129 offset:3072
	s_add_i32 s26, s84, s5
	s_add_u32 s60, s3, s26
	s_addc_u32 s61, s36, 0
	s_add_i32 vcc_lo, s63, 0xc000
	s_add_i32 s35, s63, 0xe000
	s_add_i32 s42, s5, 0xfffe0080
	s_cmp_eq_u32 s70, s34
	s_cselect_b32 s50, s4, s84
	s_cselect_b32 s58, s85, s97
	s_mov_b32 m0, vcc_lo
	v_lshl_add_u64 v[134:135], s[60:61], 0, v[148:149]
	ds_read_b128 v[202:205], v172
	ds_read_b128 v[206:209], v172 offset:1024
	ds_read_b128 v[210:213], v172 offset:2048
	ds_read_b128 v[214:217], v172 offset:3072
	ds_read_b128 v[218:221], v172 offset:4096
	ds_read_b128 v[222:225], v172 offset:5120
	ds_read_b128 v[226:229], v172 offset:6144
	ds_read_b128 v[230:233], v172 offset:7168
	global_load_lds_dwordx4 v[134:135], off
	v_lshl_add_u64 v[134:135], s[60:61], 0, v[146:147]
	s_mov_b32 m0, s35
	s_nop 0
	global_load_lds_dwordx4 v[134:135], off
	s_waitcnt vmcnt(8)
	s_waitcnt lgkmcnt(0)
	s_barrier
	v_mfma_f32_16x16x32_bf16 v[124:127], v[130:133], v[202:205], v[124:127]
	v_mfma_f32_16x16x32_bf16 v[120:123], v[178:181], v[202:205], v[120:123]
	v_mfma_f32_16x16x32_bf16 v[116:119], v[130:133], v[210:213], v[116:119]
	v_mfma_f32_16x16x32_bf16 v[112:115], v[178:181], v[210:213], v[112:115]
	v_mfma_f32_16x16x32_bf16 v[108:111], v[130:133], v[218:221], v[108:111]
	v_mfma_f32_16x16x32_bf16 v[104:107], v[178:181], v[218:221], v[104:107]
	v_mfma_f32_16x16x32_bf16 v[100:103], v[130:133], v[226:229], v[100:103]
	v_mfma_f32_16x16x32_bf16 v[96:99], v[178:181], v[226:229], v[96:99]
	v_mfma_f32_16x16x32_bf16 v[124:127], v[162:165], v[206:209], v[124:127]
	v_mfma_f32_16x16x32_bf16 v[120:123], v[182:185], v[206:209], v[120:123]
	v_mfma_f32_16x16x32_bf16 v[116:119], v[162:165], v[214:217], v[116:119]
	v_mfma_f32_16x16x32_bf16 v[112:115], v[182:185], v[214:217], v[112:115]
	v_mfma_f32_16x16x32_bf16 v[108:111], v[162:165], v[222:225], v[108:111]
	v_mfma_f32_16x16x32_bf16 v[104:107], v[182:185], v[222:225], v[104:107]
	v_mfma_f32_16x16x32_bf16 v[100:103], v[162:165], v[230:233], v[100:103]
	v_mfma_f32_16x16x32_bf16 v[96:99], v[182:185], v[230:233], v[96:99]
	v_mfma_f32_16x16x32_bf16 v[92:95], v[186:189], v[202:205], v[92:95]
	v_mfma_f32_16x16x32_bf16 v[88:91], v[194:197], v[202:205], v[88:91]
	v_mfma_f32_16x16x32_bf16 v[84:87], v[186:189], v[210:213], v[84:87]
	v_mfma_f32_16x16x32_bf16 v[80:83], v[194:197], v[210:213], v[80:83]
	v_mfma_f32_16x16x32_bf16 v[76:79], v[186:189], v[218:221], v[76:79]
	v_mfma_f32_16x16x32_bf16 v[72:75], v[194:197], v[218:221], v[72:75]
	v_mfma_f32_16x16x32_bf16 v[68:71], v[186:189], v[226:229], v[68:71]
	v_mfma_f32_16x16x32_bf16 v[64:67], v[194:197], v[226:229], v[64:67]
	v_mfma_f32_16x16x32_bf16 v[92:95], v[190:193], v[206:209], v[92:95]
	v_mfma_f32_16x16x32_bf16 v[88:91], v[198:201], v[206:209], v[88:91]
	v_mfma_f32_16x16x32_bf16 v[84:87], v[190:193], v[214:217], v[84:87]
	v_mfma_f32_16x16x32_bf16 v[80:83], v[198:201], v[214:217], v[80:83]
	v_mfma_f32_16x16x32_bf16 v[76:79], v[190:193], v[222:225], v[76:79]
	v_mfma_f32_16x16x32_bf16 v[72:75], v[198:201], v[222:225], v[72:75]
	v_mfma_f32_16x16x32_bf16 v[68:71], v[190:193], v[230:233], v[68:71]
	v_mfma_f32_16x16x32_bf16 v[64:67], v[198:201], v[230:233], v[64:67]
	s_barrier
	s_cselect_b32 s44, 0, s42
	s_add_i32 s42, s44, s58
	s_ashr_i32 s43, s42, 31
	s_add_u32 s60, s6, s42
	s_addc_u32 s61, s7, s43
	s_add_i32 s51, s58, 0xffffff00
	s_add_i32 s27, s27, s48
	s_add_i32 s42, s51, s44
	v_lshl_add_u64 v[134:135], s[60:61], 0, v[144:145]
	s_mov_b32 m0, s27
	s_add_i32 vcc_hi, s27, 0x2000
	s_ashr_i32 s43, s42, 31
	ds_read_b128 v[202:205], v172 offset:16384
	ds_read_b128 v[206:209], v172 offset:17408
	ds_read_b128 v[210:213], v172 offset:18432
	ds_read_b128 v[214:217], v172 offset:19456
	ds_read_b128 v[218:221], v172 offset:20480
	ds_read_b128 v[222:225], v172 offset:21504
	ds_read_b128 v[226:229], v172 offset:22528
	ds_read_b128 v[230:233], v172 offset:23552
	global_load_lds_dwordx4 v[134:135], off
	v_lshl_add_u64 v[134:135], s[60:61], 0, v[142:143]
	s_add_u32 s60, s6, s42
	s_mov_b32 m0, vcc_hi
	s_addc_u32 s61, s7, s43
	s_add_i32 s59, s59, s48
	global_load_lds_dwordx4 v[134:135], off
	v_lshl_add_u64 v[134:135], s[60:61], 0, v[144:145]
	s_mov_b32 m0, s59
	s_add_i32 s49, s44, s50
	global_load_lds_dwordx4 v[134:135], off
	v_lshl_add_u64 v[134:135], s[60:61], 0, v[142:143]
	s_add_i32 s60, s59, 0x2000
	s_add_u32 s42, s3, s49
	s_mov_b32 m0, s60
	s_addc_u32 s43, s36, 0
	global_load_lds_dwordx4 v[134:135], off
	v_lshl_add_u64 v[134:135], s[42:43], 0, v[148:149]
	s_mov_b32 m0, s63
	s_nop 0
	global_load_lds_dwordx4 v[134:135], off
	v_lshl_add_u64 v[134:135], s[42:43], 0, v[146:147]
	s_mov_b32 m0, s66
	s_nop 0
	global_load_lds_dwordx4 v[134:135], off
	s_waitcnt vmcnt(8)
	s_waitcnt lgkmcnt(0)
	s_barrier
	v_mfma_f32_16x16x32_bf16 v[60:63], v[130:133], v[202:205], v[60:63]
	v_mfma_f32_16x16x32_bf16 v[56:59], v[178:181], v[202:205], v[56:59]
	v_mfma_f32_16x16x32_bf16 v[52:55], v[130:133], v[210:213], v[52:55]
	v_mfma_f32_16x16x32_bf16 v[48:51], v[178:181], v[210:213], v[48:51]
	v_mfma_f32_16x16x32_bf16 v[44:47], v[130:133], v[218:221], v[44:47]
	v_mfma_f32_16x16x32_bf16 v[40:43], v[178:181], v[218:221], v[40:43]
	v_mfma_f32_16x16x32_bf16 v[36:39], v[130:133], v[226:229], v[36:39]
	v_mfma_f32_16x16x32_bf16 v[32:35], v[178:181], v[226:229], v[32:35]
	v_mfma_f32_16x16x32_bf16 v[60:63], v[162:165], v[206:209], v[60:63]
	v_mfma_f32_16x16x32_bf16 v[56:59], v[182:185], v[206:209], v[56:59]
	v_mfma_f32_16x16x32_bf16 v[52:55], v[162:165], v[214:217], v[52:55]
	v_mfma_f32_16x16x32_bf16 v[48:51], v[182:185], v[214:217], v[48:51]
	v_mfma_f32_16x16x32_bf16 v[44:47], v[162:165], v[222:225], v[44:47]
	v_mfma_f32_16x16x32_bf16 v[40:43], v[182:185], v[222:225], v[40:43]
	v_mfma_f32_16x16x32_bf16 v[36:39], v[162:165], v[230:233], v[36:39]
	v_mfma_f32_16x16x32_bf16 v[32:35], v[182:185], v[230:233], v[32:35]
	v_mfma_f32_16x16x32_bf16 v[28:31], v[186:189], v[202:205], v[28:31]
	v_mfma_f32_16x16x32_bf16 v[24:27], v[194:197], v[202:205], v[24:27]
	v_mfma_f32_16x16x32_bf16 v[20:23], v[186:189], v[210:213], v[20:23]
	v_mfma_f32_16x16x32_bf16 v[16:19], v[194:197], v[210:213], v[16:19]
	v_mfma_f32_16x16x32_bf16 v[12:15], v[186:189], v[218:221], v[12:15]
	v_mfma_f32_16x16x32_bf16 v[8:11], v[194:197], v[218:221], v[8:11]
	v_mfma_f32_16x16x32_bf16 v[4:7], v[186:189], v[226:229], v[4:7]
	v_mfma_f32_16x16x32_bf16 v[0:3], v[194:197], v[226:229], v[0:3]
	v_mfma_f32_16x16x32_bf16 v[28:31], v[190:193], v[206:209], v[28:31]
	v_mfma_f32_16x16x32_bf16 v[24:27], v[198:201], v[206:209], v[24:27]
	v_mfma_f32_16x16x32_bf16 v[20:23], v[190:193], v[214:217], v[20:23]
	v_mfma_f32_16x16x32_bf16 v[16:19], v[198:201], v[214:217], v[16:19]
	v_mfma_f32_16x16x32_bf16 v[12:15], v[190:193], v[222:225], v[12:15]
	v_mfma_f32_16x16x32_bf16 v[8:11], v[198:201], v[222:225], v[8:11]
	v_mfma_f32_16x16x32_bf16 v[4:7], v[190:193], v[230:233], v[4:7]
	v_mfma_f32_16x16x32_bf16 v[0:3], v[198:201], v[230:233], v[0:3]
	s_barrier
	s_add_i32 s61, 0, 0x18000
	s_add_i32 s26, 0, 0x1c000
	v_add_u32_e32 v130, s61, v171
	v_add_u32_e32 v131, s26, v171
	ds_read_b128 v[132:135], v130
	ds_read_b128 v[162:165], v130 offset:1024
	ds_read_b128 v[178:181], v130 offset:2048
	ds_read_b128 v[182:185], v130 offset:3072
	ds_read_b128 v[186:189], v131
	ds_read_b128 v[190:193], v131 offset:1024
	ds_read_b128 v[194:197], v131 offset:2048
	ds_read_b128 v[198:201], v131 offset:3072
	s_add_i32 s49, s49, 0x20000
	s_add_u32 s42, s3, s49
	s_addc_u32 s43, s36, 0
	s_mov_b32 m0, s67
	v_lshl_add_u64 v[166:167], s[42:43], 0, v[148:149]
	ds_read_b128 v[202:205], v172 offset:32768
	ds_read_b128 v[206:209], v172 offset:33792
	ds_read_b128 v[210:213], v172 offset:34816
	ds_read_b128 v[214:217], v172 offset:35840
	ds_read_b128 v[218:221], v172 offset:36864
	ds_read_b128 v[222:225], v172 offset:37888
	ds_read_b128 v[226:229], v172 offset:38912
	ds_read_b128 v[230:233], v172 offset:39936
	global_load_lds_dwordx4 v[166:167], off
	v_lshl_add_u64 v[166:167], s[42:43], 0, v[146:147]
	s_mov_b32 m0, s68
	s_nop 0
	global_load_lds_dwordx4 v[166:167], off
	s_waitcnt vmcnt(8)
	s_waitcnt lgkmcnt(0)
	s_barrier
	v_mfma_f32_16x16x32_bf16 v[124:127], v[132:135], v[202:205], v[124:127]
	v_mfma_f32_16x16x32_bf16 v[120:123], v[178:181], v[202:205], v[120:123]
	v_mfma_f32_16x16x32_bf16 v[116:119], v[132:135], v[210:213], v[116:119]
	v_mfma_f32_16x16x32_bf16 v[112:115], v[178:181], v[210:213], v[112:115]
	v_mfma_f32_16x16x32_bf16 v[108:111], v[132:135], v[218:221], v[108:111]
	v_mfma_f32_16x16x32_bf16 v[104:107], v[178:181], v[218:221], v[104:107]
	v_mfma_f32_16x16x32_bf16 v[100:103], v[132:135], v[226:229], v[100:103]
	v_mfma_f32_16x16x32_bf16 v[96:99], v[178:181], v[226:229], v[96:99]
	v_mfma_f32_16x16x32_bf16 v[124:127], v[162:165], v[206:209], v[124:127]
	v_mfma_f32_16x16x32_bf16 v[120:123], v[182:185], v[206:209], v[120:123]
	v_mfma_f32_16x16x32_bf16 v[116:119], v[162:165], v[214:217], v[116:119]
	v_mfma_f32_16x16x32_bf16 v[112:115], v[182:185], v[214:217], v[112:115]
	v_mfma_f32_16x16x32_bf16 v[108:111], v[162:165], v[222:225], v[108:111]
	v_mfma_f32_16x16x32_bf16 v[104:107], v[182:185], v[222:225], v[104:107]
	v_mfma_f32_16x16x32_bf16 v[100:103], v[162:165], v[230:233], v[100:103]
	v_mfma_f32_16x16x32_bf16 v[96:99], v[182:185], v[230:233], v[96:99]
	v_mfma_f32_16x16x32_bf16 v[92:95], v[186:189], v[202:205], v[92:95]
	v_mfma_f32_16x16x32_bf16 v[88:91], v[194:197], v[202:205], v[88:91]
	v_mfma_f32_16x16x32_bf16 v[84:87], v[186:189], v[210:213], v[84:87]
	v_mfma_f32_16x16x32_bf16 v[80:83], v[194:197], v[210:213], v[80:83]
	v_mfma_f32_16x16x32_bf16 v[76:79], v[186:189], v[218:221], v[76:79]
	v_mfma_f32_16x16x32_bf16 v[72:75], v[194:197], v[218:221], v[72:75]
	v_mfma_f32_16x16x32_bf16 v[68:71], v[186:189], v[226:229], v[68:71]
	v_mfma_f32_16x16x32_bf16 v[64:67], v[194:197], v[226:229], v[64:67]
	v_mfma_f32_16x16x32_bf16 v[92:95], v[190:193], v[206:209], v[92:95]
	v_mfma_f32_16x16x32_bf16 v[88:91], v[198:201], v[206:209], v[88:91]
	v_mfma_f32_16x16x32_bf16 v[84:87], v[190:193], v[214:217], v[84:87]
	v_mfma_f32_16x16x32_bf16 v[80:83], v[198:201], v[214:217], v[80:83]
	v_mfma_f32_16x16x32_bf16 v[76:79], v[190:193], v[222:225], v[76:79]
	v_mfma_f32_16x16x32_bf16 v[72:75], v[198:201], v[222:225], v[72:75]
	v_mfma_f32_16x16x32_bf16 v[68:71], v[190:193], v[230:233], v[68:71]
	v_mfma_f32_16x16x32_bf16 v[64:67], v[198:201], v[230:233], v[64:67]
	s_barrier
; template <class Epi, class Sched, class Hook = NoHook>
; __device__ __forceinline__ void gemm_phase_w(LAS unsigned char* lds, const Sched& S, const Epi& E, int wave_id, const Hook& HK = Hook()) {
;     ...
;         if constexpr (!SEG2) {
;             for (int tt = 0; tt < nt; tt += 2) {
;                 if constexpr (GATHER) { if (tt == nt - 2) {
;                     if (has_next) { gnxt_00 = S.grow_l(nxt, lds, nbuf, R0) + (unsigned)(C0 * 2); gnxt_01 = S.grow_l(nxt, lds, nbuf, R1) + (unsigned)(C1 * 2); gnxt_10 = S.grow_l(nxt, lds, nbuf, 128 + R0) + (unsigned)(C0 * 2); gnxt_11 = S.grow_l(nxt, lds, nbuf, 128 + R1) + (unsigned)(C1 * 2); }
;                     else { gnxt_00 = gcur_00; gnxt_01 = gcur_01; gnxt_10 = gcur_10; gnxt_11 = gcur_11; } } }
;                 PG_TRIP(tt, false, false, false);
;             }
;         } else {
;             for (int tt = 0; tt < nt - 4; tt += 2) PG_TRIP(tt, false, false, false);
;             PG_TRIP(nt - 4, false, true, false);
;             PG_TRIP(nt - 2, true, false, true);
	s_or_b32 s18, s44, 0x80
	s_add_i32 s19, s18, s58
	s_ashr_i32 s43, s19, 31
	s_add_u32 s42, s6, s19
	s_addc_u32 s43, s7, s43
	s_add_i32 s61, s61, s48
	v_lshl_add_u64 v[166:167], s[42:43], 0, v[144:145]
	s_mov_b32 m0, s61
	s_add_i32 s19, s18, s51
	ds_read_b128 v[202:205], v172 offset:49152
	ds_read_b128 v[206:209], v172 offset:50176
	ds_read_b128 v[210:213], v172 offset:51200
	ds_read_b128 v[214:217], v172 offset:52224
	ds_read_b128 v[218:221], v172 offset:53248
	ds_read_b128 v[222:225], v172 offset:54272
	ds_read_b128 v[226:229], v172 offset:55296
	ds_read_b128 v[230:233], v172 offset:56320
	global_load_lds_dwordx4 v[166:167], off
	v_lshl_add_u64 v[166:167], s[42:43], 0, v[142:143]
	s_add_i32 s49, s61, 0x2000
	s_ashr_i32 s43, s19, 31
	s_add_u32 s42, s6, s19
	s_mov_b32 m0, s49
	s_addc_u32 s43, s7, s43
	s_add_i32 s26, s26, s48
	global_load_lds_dwordx4 v[166:167], off
	v_lshl_add_u64 v[166:167], s[42:43], 0, v[144:145]
	s_mov_b32 m0, s26
	s_add_i32 s44, s26, 0x2000
	s_add_i32 s18, s18, s50
	global_load_lds_dwordx4 v[166:167], off
	v_lshl_add_u64 v[166:167], s[42:43], 0, v[142:143]
	s_add_u32 s42, s3, s18
	s_mov_b32 m0, s44
	s_addc_u32 s43, s36, 0
	global_load_lds_dwordx4 v[166:167], off
	v_lshl_add_u64 v[166:167], s[42:43], 0, v[148:149]
	s_mov_b32 m0, s71
	s_nop 0
	global_load_lds_dwordx4 v[166:167], off
	v_lshl_add_u64 v[166:167], s[42:43], 0, v[146:147]
	s_mov_b32 m0, s72
	s_nop 0
	global_load_lds_dwordx4 v[166:167], off
	s_waitcnt vmcnt(8)
	s_waitcnt lgkmcnt(0)
	s_barrier
	v_mfma_f32_16x16x32_bf16 v[60:63], v[132:135], v[202:205], v[60:63]
	v_mfma_f32_16x16x32_bf16 v[56:59], v[178:181], v[202:205], v[56:59]
	v_mfma_f32_16x16x32_bf16 v[52:55], v[132:135], v[210:213], v[52:55]
	v_mfma_f32_16x16x32_bf16 v[48:51], v[178:181], v[210:213], v[48:51]
	v_mfma_f32_16x16x32_bf16 v[44:47], v[132:135], v[218:221], v[44:47]
	v_mfma_f32_16x16x32_bf16 v[40:43], v[178:181], v[218:221], v[40:43]
	v_mfma_f32_16x16x32_bf16 v[36:39], v[132:135], v[226:229], v[36:39]
	v_mfma_f32_16x16x32_bf16 v[32:35], v[178:181], v[226:229], v[32:35]
	v_mfma_f32_16x16x32_bf16 v[60:63], v[162:165], v[206:209], v[60:63]
	v_mfma_f32_16x16x32_bf16 v[56:59], v[182:185], v[206:209], v[56:59]
	v_mfma_f32_16x16x32_bf16 v[52:55], v[162:165], v[214:217], v[52:55]
	v_mfma_f32_16x16x32_bf16 v[48:51], v[182:185], v[214:217], v[48:51]
	v_mfma_f32_16x16x32_bf16 v[44:47], v[162:165], v[222:225], v[44:47]
	v_mfma_f32_16x16x32_bf16 v[40:43], v[182:185], v[222:225], v[40:43]
	v_mfma_f32_16x16x32_bf16 v[36:39], v[162:165], v[230:233], v[36:39]
	v_mfma_f32_16x16x32_bf16 v[32:35], v[182:185], v[230:233], v[32:35]
	v_mfma_f32_16x16x32_bf16 v[28:31], v[186:189], v[202:205], v[28:31]
	v_mfma_f32_16x16x32_bf16 v[24:27], v[194:197], v[202:205], v[24:27]
	v_mfma_f32_16x16x32_bf16 v[20:23], v[186:189], v[210:213], v[20:23]
	v_mfma_f32_16x16x32_bf16 v[16:19], v[194:197], v[210:213], v[16:19]
	v_mfma_f32_16x16x32_bf16 v[12:15], v[186:189], v[218:221], v[12:15]
	v_mfma_f32_16x16x32_bf16 v[8:11], v[194:197], v[218:221], v[8:11]
	v_mfma_f32_16x16x32_bf16 v[4:7], v[186:189], v[226:229], v[4:7]
	v_mfma_f32_16x16x32_bf16 v[0:3], v[194:197], v[226:229], v[0:3]
	v_mfma_f32_16x16x32_bf16 v[28:31], v[190:193], v[206:209], v[28:31]
	v_mfma_f32_16x16x32_bf16 v[24:27], v[198:201], v[206:209], v[24:27]
	v_mfma_f32_16x16x32_bf16 v[20:23], v[190:193], v[214:217], v[20:23]
	v_mfma_f32_16x16x32_bf16 v[16:19], v[198:201], v[214:217], v[16:19]
	v_mfma_f32_16x16x32_bf16 v[12:15], v[190:193], v[222:225], v[12:15]
	v_mfma_f32_16x16x32_bf16 v[8:11], v[198:201], v[222:225], v[8:11]
	v_mfma_f32_16x16x32_bf16 v[4:7], v[190:193], v[230:233], v[4:7]
	v_mfma_f32_16x16x32_bf16 v[0:3], v[198:201], v[230:233], v[0:3]
	s_barrier
	s_addk_i32 s5, 0x100
	s_add_i32 s18, s34, 2
	s_add_i32 s19, s34, 4
	s_cmp_ge_u32 s19, s70
	s_mov_b32 s34, s18
	s_cbranch_scc0 .LBB0_1776
	ds_read_b128 v[132:135], v128
	ds_read_b128 v[162:165], v128 offset:1024
	ds_read_b128 v[178:181], v128 offset:2048
	ds_read_b128 v[182:185], v128 offset:3072
	ds_read_b128 v[186:189], v129
	ds_read_b128 v[190:193], v129 offset:1024
	ds_read_b128 v[194:197], v129 offset:2048
	ds_read_b128 v[198:201], v129 offset:3072
	s_add_i32 s5, s73, s84
	s_add_u32 s50, s3, s5
	s_addc_u32 s51, s36, 0
	s_mov_b32 m0, vcc_lo
	v_lshl_add_u64 v[166:167], s[50:51], 0, v[148:149]
	ds_read_b128 v[202:205], v172
	ds_read_b128 v[206:209], v172 offset:1024
	ds_read_b128 v[210:213], v172 offset:2048
	ds_read_b128 v[214:217], v172 offset:3072
	ds_read_b128 v[218:221], v172 offset:4096
	ds_read_b128 v[222:225], v172 offset:5120
	ds_read_b128 v[226:229], v172 offset:6144
	ds_read_b128 v[230:233], v172 offset:7168
	global_load_lds_dwordx4 v[166:167], off
	v_lshl_add_u64 v[166:167], s[50:51], 0, v[146:147]
	s_mov_b32 m0, s35
	s_nop 0
	global_load_lds_dwordx4 v[166:167], off
	s_waitcnt vmcnt(8)
	s_waitcnt lgkmcnt(0)
	s_barrier
; template <class Epi, class Sched, class Hook = NoHook>
; __device__ __forceinline__ void gemm_phase_w(LAS unsigned char* lds, const Sched& S, const Epi& E, int wave_id, const Hook& HK = Hook()) {
;     ...
;             PG_TRIP(nt - 4, false, true, false);
;             PG_TRIP(nt - 2, true, false, true);
	v_mfma_f32_16x16x32_bf16 v[124:127], v[132:135], v[202:205], v[124:127]
	v_mfma_f32_16x16x32_bf16 v[120:123], v[178:181], v[202:205], v[120:123]
	v_mfma_f32_16x16x32_bf16 v[116:119], v[132:135], v[210:213], v[116:119]
	v_mfma_f32_16x16x32_bf16 v[112:115], v[178:181], v[210:213], v[112:115]
	v_mfma_f32_16x16x32_bf16 v[108:111], v[132:135], v[218:221], v[108:111]
	v_mfma_f32_16x16x32_bf16 v[104:107], v[178:181], v[218:221], v[104:107]
	v_mfma_f32_16x16x32_bf16 v[100:103], v[132:135], v[226:229], v[100:103]
	v_mfma_f32_16x16x32_bf16 v[96:99], v[178:181], v[226:229], v[96:99]
	v_mfma_f32_16x16x32_bf16 v[124:127], v[162:165], v[206:209], v[124:127]
	v_mfma_f32_16x16x32_bf16 v[120:123], v[182:185], v[206:209], v[120:123]
	v_mfma_f32_16x16x32_bf16 v[116:119], v[162:165], v[214:217], v[116:119]
	v_mfma_f32_16x16x32_bf16 v[112:115], v[182:185], v[214:217], v[112:115]
	v_mfma_f32_16x16x32_bf16 v[108:111], v[162:165], v[222:225], v[108:111]
	v_mfma_f32_16x16x32_bf16 v[104:107], v[182:185], v[222:225], v[104:107]
	v_mfma_f32_16x16x32_bf16 v[100:103], v[162:165], v[230:233], v[100:103]
	v_mfma_f32_16x16x32_bf16 v[96:99], v[182:185], v[230:233], v[96:99]
	v_mfma_f32_16x16x32_bf16 v[92:95], v[186:189], v[202:205], v[92:95]
	v_mfma_f32_16x16x32_bf16 v[88:91], v[194:197], v[202:205], v[88:91]
	v_mfma_f32_16x16x32_bf16 v[84:87], v[186:189], v[210:213], v[84:87]
	v_mfma_f32_16x16x32_bf16 v[80:83], v[194:197], v[210:213], v[80:83]
	v_mfma_f32_16x16x32_bf16 v[76:79], v[186:189], v[218:221], v[76:79]
	v_mfma_f32_16x16x32_bf16 v[72:75], v[194:197], v[218:221], v[72:75]
	v_mfma_f32_16x16x32_bf16 v[68:71], v[186:189], v[226:229], v[68:71]
	v_mfma_f32_16x16x32_bf16 v[64:67], v[194:197], v[226:229], v[64:67]
	v_mfma_f32_16x16x32_bf16 v[92:95], v[190:193], v[206:209], v[92:95]
	v_mfma_f32_16x16x32_bf16 v[88:91], v[198:201], v[206:209], v[88:91]
	v_mfma_f32_16x16x32_bf16 v[84:87], v[190:193], v[214:217], v[84:87]
	v_mfma_f32_16x16x32_bf16 v[80:83], v[198:201], v[214:217], v[80:83]
	v_mfma_f32_16x16x32_bf16 v[76:79], v[190:193], v[222:225], v[76:79]
	v_mfma_f32_16x16x32_bf16 v[72:75], v[198:201], v[222:225], v[72:75]
	v_mfma_f32_16x16x32_bf16 v[68:71], v[190:193], v[230:233], v[68:71]
	v_mfma_f32_16x16x32_bf16 v[64:67], v[198:201], v[230:233], v[64:67]
	s_barrier
	s_ashr_i32 s5, s31, 31
	s_add_u32 s50, s8, s31
	s_addc_u32 s51, s9, s5
	s_add_i32 s5, s31, 0x8000
	s_mov_b32 m0, s27
	v_lshl_add_u64 v[166:167], s[50:51], 0, v[138:139]
	s_ashr_i32 s34, s5, 31
	ds_read_b128 v[202:205], v172 offset:16384
	ds_read_b128 v[206:209], v172 offset:17408
	ds_read_b128 v[210:213], v172 offset:18432
	ds_read_b128 v[214:217], v172 offset:19456
	ds_read_b128 v[218:221], v172 offset:20480
	ds_read_b128 v[222:225], v172 offset:21504
	ds_read_b128 v[226:229], v172 offset:22528
	ds_read_b128 v[230:233], v172 offset:23552
	global_load_lds_dwordx4 v[166:167], off
	v_lshl_add_u64 v[166:167], s[50:51], 0, v[140:141]
	s_add_u32 s50, s8, s5
	s_mov_b32 m0, vcc_hi
	s_addc_u32 s51, s9, s34
	global_load_lds_dwordx4 v[166:167], off
	v_lshl_add_u64 v[166:167], s[50:51], 0, v[138:139]
	s_mov_b32 m0, s59
	s_nop 0
	global_load_lds_dwordx4 v[166:167], off
	v_lshl_add_u64 v[166:167], s[50:51], 0, v[140:141]
	s_add_u32 s50, s37, s89
	s_mov_b32 m0, s60
	s_addc_u32 s51, s38, 0
	global_load_lds_dwordx4 v[166:167], off
	v_lshl_add_u64 v[166:167], s[50:51], 0, v[138:139]
	s_mov_b32 m0, s63
	s_nop 0
	global_load_lds_dwordx4 v[166:167], off
	v_lshl_add_u64 v[166:167], s[50:51], 0, v[140:141]
	s_mov_b32 m0, s66
	s_nop 0
	global_load_lds_dwordx4 v[166:167], off
	s_waitcnt vmcnt(8)
	s_waitcnt lgkmcnt(0)
	s_barrier
	v_mfma_f32_16x16x32_bf16 v[60:63], v[132:135], v[202:205], v[60:63]
	v_mfma_f32_16x16x32_bf16 v[56:59], v[178:181], v[202:205], v[56:59]
	v_mfma_f32_16x16x32_bf16 v[52:55], v[132:135], v[210:213], v[52:55]
	v_mfma_f32_16x16x32_bf16 v[48:51], v[178:181], v[210:213], v[48:51]
	v_mfma_f32_16x16x32_bf16 v[44:47], v[132:135], v[218:221], v[44:47]
	v_mfma_f32_16x16x32_bf16 v[40:43], v[178:181], v[218:221], v[40:43]
	v_mfma_f32_16x16x32_bf16 v[36:39], v[132:135], v[226:229], v[36:39]
	v_mfma_f32_16x16x32_bf16 v[32:35], v[178:181], v[226:229], v[32:35]
	v_mfma_f32_16x16x32_bf16 v[60:63], v[162:165], v[206:209], v[60:63]
	v_mfma_f32_16x16x32_bf16 v[56:59], v[182:185], v[206:209], v[56:59]
	v_mfma_f32_16x16x32_bf16 v[52:55], v[162:165], v[214:217], v[52:55]
	v_mfma_f32_16x16x32_bf16 v[48:51], v[182:185], v[214:217], v[48:51]
	v_mfma_f32_16x16x32_bf16 v[44:47], v[162:165], v[222:225], v[44:47]
	v_mfma_f32_16x16x32_bf16 v[40:43], v[182:185], v[222:225], v[40:43]
	v_mfma_f32_16x16x32_bf16 v[36:39], v[162:165], v[230:233], v[36:39]
	v_mfma_f32_16x16x32_bf16 v[32:35], v[182:185], v[230:233], v[32:35]
	v_mfma_f32_16x16x32_bf16 v[28:31], v[186:189], v[202:205], v[28:31]
	v_mfma_f32_16x16x32_bf16 v[24:27], v[194:197], v[202:205], v[24:27]
	v_mfma_f32_16x16x32_bf16 v[20:23], v[186:189], v[210:213], v[20:23]
	v_mfma_f32_16x16x32_bf16 v[16:19], v[194:197], v[210:213], v[16:19]
	v_mfma_f32_16x16x32_bf16 v[4:7], v[186:189], v[226:229], v[4:7]
	v_mfma_f32_16x16x32_bf16 v[0:3], v[194:197], v[226:229], v[0:3]
	v_mfma_f32_16x16x32_bf16 v[28:31], v[190:193], v[206:209], v[28:31]
	v_mfma_f32_16x16x32_bf16 v[24:27], v[198:201], v[206:209], v[24:27]
	v_mfma_f32_16x16x32_bf16 v[20:23], v[190:193], v[214:217], v[20:23]
	v_mfma_f32_16x16x32_bf16 v[16:19], v[198:201], v[214:217], v[16:19]
	v_mfma_f32_16x16x32_bf16 v[12:15], v[186:189], v[218:221], v[12:15]
	v_mfma_f32_16x16x32_bf16 v[8:11], v[194:197], v[218:221], v[8:11]
	v_mfma_f32_16x16x32_bf16 v[4:7], v[190:193], v[230:233], v[4:7]
	v_mfma_f32_16x16x32_bf16 v[0:3], v[198:201], v[230:233], v[0:3]
	v_mfma_f32_16x16x32_bf16 v[12:15], v[190:193], v[222:225], v[12:15]
	v_mfma_f32_16x16x32_bf16 v[8:11], v[198:201], v[222:225], v[8:11]
	s_barrier
	ds_read_b128 v[132:135], v130
	ds_read_b128 v[162:165], v130 offset:1024
	ds_read_b128 v[178:181], v130 offset:2048
	ds_read_b128 v[182:185], v130 offset:3072
	ds_read_b128 v[186:189], v131
	ds_read_b128 v[190:193], v131 offset:1024
	ds_read_b128 v[194:197], v131 offset:2048
	ds_read_b128 v[198:201], v131 offset:3072
	s_add_i32 s5, s89, 0x8000
	s_add_u32 s50, s37, s5
	s_addc_u32 s51, s38, 0
	s_mov_b32 m0, s67
	v_lshl_add_u64 v[166:167], s[50:51], 0, v[138:139]
	ds_read_b128 v[202:205], v172 offset:32768
	ds_read_b128 v[206:209], v172 offset:33792
	ds_read_b128 v[210:213], v172 offset:34816
	ds_read_b128 v[214:217], v172 offset:35840
	ds_read_b128 v[218:221], v172 offset:36864
	ds_read_b128 v[222:225], v172 offset:37888
	ds_read_b128 v[226:229], v172 offset:38912
	ds_read_b128 v[230:233], v172 offset:39936
	global_load_lds_dwordx4 v[166:167], off
	v_lshl_add_u64 v[166:167], s[50:51], 0, v[140:141]
	s_mov_b32 m0, s68
	s_nop 0
	global_load_lds_dwordx4 v[166:167], off
	s_waitcnt vmcnt(8)
	s_waitcnt lgkmcnt(0)
	s_barrier
	v_mfma_f32_16x16x32_bf16 v[124:127], v[132:135], v[202:205], v[124:127]
	v_mfma_f32_16x16x32_bf16 v[120:123], v[178:181], v[202:205], v[120:123]
	v_mfma_f32_16x16x32_bf16 v[116:119], v[132:135], v[210:213], v[116:119]
	v_mfma_f32_16x16x32_bf16 v[112:115], v[178:181], v[210:213], v[112:115]
	v_mfma_f32_16x16x32_bf16 v[108:111], v[132:135], v[218:221], v[108:111]
	v_mfma_f32_16x16x32_bf16 v[104:107], v[178:181], v[218:221], v[104:107]
	v_mfma_f32_16x16x32_bf16 v[100:103], v[132:135], v[226:229], v[100:103]
	v_mfma_f32_16x16x32_bf16 v[96:99], v[178:181], v[226:229], v[96:99]
	v_mfma_f32_16x16x32_bf16 v[124:127], v[162:165], v[206:209], v[124:127]
	v_mfma_f32_16x16x32_bf16 v[120:123], v[182:185], v[206:209], v[120:123]
	v_mfma_f32_16x16x32_bf16 v[116:119], v[162:165], v[214:217], v[116:119]
	v_mfma_f32_16x16x32_bf16 v[112:115], v[182:185], v[214:217], v[112:115]
	v_mfma_f32_16x16x32_bf16 v[108:111], v[162:165], v[222:225], v[108:111]
	v_mfma_f32_16x16x32_bf16 v[104:107], v[182:185], v[222:225], v[104:107]
	v_mfma_f32_16x16x32_bf16 v[100:103], v[162:165], v[230:233], v[100:103]
	v_mfma_f32_16x16x32_bf16 v[96:99], v[182:185], v[230:233], v[96:99]
	v_mfma_f32_16x16x32_bf16 v[92:95], v[186:189], v[202:205], v[92:95]
	v_mfma_f32_16x16x32_bf16 v[88:91], v[194:197], v[202:205], v[88:91]
	v_mfma_f32_16x16x32_bf16 v[84:87], v[186:189], v[210:213], v[84:87]
	v_mfma_f32_16x16x32_bf16 v[80:83], v[194:197], v[210:213], v[80:83]
	v_mfma_f32_16x16x32_bf16 v[76:79], v[186:189], v[218:221], v[76:79]
	v_mfma_f32_16x16x32_bf16 v[72:75], v[194:197], v[218:221], v[72:75]
	v_mfma_f32_16x16x32_bf16 v[68:71], v[186:189], v[226:229], v[68:71]
	v_mfma_f32_16x16x32_bf16 v[64:67], v[194:197], v[226:229], v[64:67]
	v_mfma_f32_16x16x32_bf16 v[92:95], v[190:193], v[206:209], v[92:95]
	v_mfma_f32_16x16x32_bf16 v[88:91], v[198:201], v[206:209], v[88:91]
	v_mfma_f32_16x16x32_bf16 v[84:87], v[190:193], v[214:217], v[84:87]
	v_mfma_f32_16x16x32_bf16 v[80:83], v[198:201], v[214:217], v[80:83]
	v_mfma_f32_16x16x32_bf16 v[76:79], v[190:193], v[222:225], v[76:79]
	v_mfma_f32_16x16x32_bf16 v[72:75], v[198:201], v[222:225], v[72:75]
	v_mfma_f32_16x16x32_bf16 v[68:71], v[190:193], v[230:233], v[68:71]
	v_mfma_f32_16x16x32_bf16 v[64:67], v[198:201], v[230:233], v[64:67]
	s_barrier
	s_add_i32 s50, s31, 0x80
	s_ashr_i32 s51, s50, 31
	s_add_i32 s5, s31, 0x8080
	s_mov_b32 m0, s61
	v_lshl_add_u64 v[166:167], v[154:155], 0, s[50:51]
	s_ashr_i32 s31, s5, 31
	ds_read_b128 v[202:205], v172 offset:49152
	ds_read_b128 v[206:209], v172 offset:50176
	ds_read_b128 v[210:213], v172 offset:51200
	ds_read_b128 v[214:217], v172 offset:52224
	ds_read_b128 v[218:221], v172 offset:53248
	ds_read_b128 v[222:225], v172 offset:54272
	ds_read_b128 v[226:229], v172 offset:55296
	ds_read_b128 v[230:233], v172 offset:56320
	global_load_lds_dwordx4 v[166:167], off
	v_lshl_add_u64 v[166:167], v[156:157], 0, s[50:51]
	s_add_u32 s50, s8, s5
	s_mov_b32 m0, s49
	s_addc_u32 s51, s9, s31
	global_load_lds_dwordx4 v[166:167], off
	v_lshl_add_u64 v[166:167], s[50:51], 0, v[138:139]
	s_mov_b32 m0, s26
	s_add_i32 s5, s89, 0x80
	global_load_lds_dwordx4 v[166:167], off
	v_lshl_add_u64 v[166:167], s[50:51], 0, v[140:141]
	s_add_u32 s50, s37, s5
	s_mov_b32 m0, s44
	s_addc_u32 s51, s38, 0
	global_load_lds_dwordx4 v[166:167], off
	v_lshl_add_u64 v[166:167], s[50:51], 0, v[138:139]
	s_mov_b32 m0, s71
	s_nop 0
	global_load_lds_dwordx4 v[166:167], off
	v_lshl_add_u64 v[166:167], s[50:51], 0, v[140:141]
	s_mov_b32 m0, s72
	s_nop 0
	global_load_lds_dwordx4 v[166:167], off
	s_waitcnt vmcnt(8)
	s_waitcnt lgkmcnt(0)
	s_barrier
	v_mfma_f32_16x16x32_bf16 v[60:63], v[132:135], v[202:205], v[60:63]
	v_mfma_f32_16x16x32_bf16 v[56:59], v[178:181], v[202:205], v[56:59]
	v_mfma_f32_16x16x32_bf16 v[52:55], v[132:135], v[210:213], v[52:55]
	v_mfma_f32_16x16x32_bf16 v[48:51], v[178:181], v[210:213], v[48:51]
	v_mfma_f32_16x16x32_bf16 v[44:47], v[132:135], v[218:221], v[44:47]
	v_mfma_f32_16x16x32_bf16 v[40:43], v[178:181], v[218:221], v[40:43]
	v_mfma_f32_16x16x32_bf16 v[36:39], v[132:135], v[226:229], v[36:39]
	v_mfma_f32_16x16x32_bf16 v[32:35], v[178:181], v[226:229], v[32:35]
	v_mfma_f32_16x16x32_bf16 v[60:63], v[162:165], v[206:209], v[60:63]
	v_mfma_f32_16x16x32_bf16 v[56:59], v[182:185], v[206:209], v[56:59]
	v_mfma_f32_16x16x32_bf16 v[52:55], v[162:165], v[214:217], v[52:55]
	v_mfma_f32_16x16x32_bf16 v[48:51], v[182:185], v[214:217], v[48:51]
	v_mfma_f32_16x16x32_bf16 v[44:47], v[162:165], v[222:225], v[44:47]
	v_mfma_f32_16x16x32_bf16 v[40:43], v[182:185], v[222:225], v[40:43]
	v_mfma_f32_16x16x32_bf16 v[36:39], v[162:165], v[230:233], v[36:39]
	v_mfma_f32_16x16x32_bf16 v[32:35], v[182:185], v[230:233], v[32:35]
	v_mfma_f32_16x16x32_bf16 v[28:31], v[186:189], v[202:205], v[28:31]
	v_mfma_f32_16x16x32_bf16 v[24:27], v[194:197], v[202:205], v[24:27]
	v_mfma_f32_16x16x32_bf16 v[20:23], v[186:189], v[210:213], v[20:23]
	v_mfma_f32_16x16x32_bf16 v[16:19], v[194:197], v[210:213], v[16:19]
	v_mfma_f32_16x16x32_bf16 v[4:7], v[186:189], v[226:229], v[4:7]
	v_mfma_f32_16x16x32_bf16 v[0:3], v[194:197], v[226:229], v[0:3]
	v_mfma_f32_16x16x32_bf16 v[28:31], v[190:193], v[206:209], v[28:31]
	v_mfma_f32_16x16x32_bf16 v[24:27], v[198:201], v[206:209], v[24:27]
	v_mfma_f32_16x16x32_bf16 v[20:23], v[190:193], v[214:217], v[20:23]
	v_mfma_f32_16x16x32_bf16 v[16:19], v[198:201], v[214:217], v[16:19]
	v_mfma_f32_16x16x32_bf16 v[12:15], v[186:189], v[218:221], v[12:15]
	v_mfma_f32_16x16x32_bf16 v[8:11], v[194:197], v[218:221], v[8:11]
	v_mfma_f32_16x16x32_bf16 v[4:7], v[190:193], v[230:233], v[4:7]
	v_mfma_f32_16x16x32_bf16 v[0:3], v[198:201], v[230:233], v[0:3]
	v_mfma_f32_16x16x32_bf16 v[12:15], v[190:193], v[222:225], v[12:15]
	v_mfma_f32_16x16x32_bf16 v[8:11], v[198:201], v[222:225], v[8:11]
	s_barrier
	ds_read_b128 v[132:135], v128
	ds_read_b128 v[162:165], v128 offset:1024
	ds_read_b128 v[178:181], v128 offset:2048
	ds_read_b128 v[182:185], v128 offset:3072
	ds_read_b128 v[186:189], v129
	ds_read_b128 v[190:193], v129 offset:1024
	ds_read_b128 v[194:197], v129 offset:2048
	ds_read_b128 v[198:201], v129 offset:3072
	s_add_i32 s5, s89, 0x8080
	s_add_u32 s50, s37, s5
	s_addc_u32 s51, s38, 0
	s_mov_b32 m0, vcc_lo
	v_lshl_add_u64 v[128:129], s[50:51], 0, v[138:139]
	ds_read_b128 v[202:205], v172
	ds_read_b128 v[206:209], v172 offset:1024
	ds_read_b128 v[210:213], v172 offset:2048
	ds_read_b128 v[214:217], v172 offset:3072
	ds_read_b128 v[218:221], v172 offset:4096
	ds_read_b128 v[222:225], v172 offset:5120
	ds_read_b128 v[226:229], v172 offset:6144
	ds_read_b128 v[230:233], v172 offset:7168
	global_load_lds_dwordx4 v[128:129], off
	v_lshl_add_u64 v[128:129], s[50:51], 0, v[140:141]
	s_mov_b32 m0, s35
	s_nop 0
	global_load_lds_dwordx4 v[128:129], off
	s_waitcnt vmcnt(8)
	s_waitcnt lgkmcnt(0)
	s_barrier
	v_mfma_f32_16x16x32_bf16 v[124:127], v[132:135], v[202:205], v[124:127]
	v_mfma_f32_16x16x32_bf16 v[120:123], v[178:181], v[202:205], v[120:123]
	v_mfma_f32_16x16x32_bf16 v[116:119], v[132:135], v[210:213], v[116:119]
	v_mfma_f32_16x16x32_bf16 v[112:115], v[178:181], v[210:213], v[112:115]
	v_mfma_f32_16x16x32_bf16 v[108:111], v[132:135], v[218:221], v[108:111]
	v_mfma_f32_16x16x32_bf16 v[104:107], v[178:181], v[218:221], v[104:107]
	v_mfma_f32_16x16x32_bf16 v[124:127], v[162:165], v[206:209], v[124:127]
	v_mfma_f32_16x16x32_bf16 v[120:123], v[182:185], v[206:209], v[120:123]
	v_mfma_f32_16x16x32_bf16 v[116:119], v[162:165], v[214:217], v[116:119]
	v_mfma_f32_16x16x32_bf16 v[112:115], v[182:185], v[214:217], v[112:115]
	v_mfma_f32_16x16x32_bf16 v[108:111], v[162:165], v[222:225], v[108:111]
	v_mfma_f32_16x16x32_bf16 v[104:107], v[182:185], v[222:225], v[104:107]
	v_mfma_f32_16x16x32_bf16 v[100:103], v[132:135], v[226:229], v[100:103]
	v_mfma_f32_16x16x32_bf16 v[96:99], v[178:181], v[226:229], v[96:99]
	v_mfma_f32_16x16x32_bf16 v[234:237], v[162:165], v[230:233], v[100:103]
	v_mfma_f32_16x16x32_bf16 v[238:241], v[182:185], v[230:233], v[96:99]
	v_mfma_f32_16x16x32_bf16 v[92:95], v[186:189], v[202:205], v[92:95]
	v_mfma_f32_16x16x32_bf16 v[88:91], v[194:197], v[202:205], v[88:91]
	v_mfma_f32_16x16x32_bf16 v[76:79], v[186:189], v[218:221], v[76:79]
	v_mfma_f32_16x16x32_bf16 v[72:75], v[194:197], v[218:221], v[72:75]
	v_mfma_f32_16x16x32_bf16 v[68:71], v[186:189], v[226:229], v[68:71]
	v_mfma_f32_16x16x32_bf16 v[64:67], v[194:197], v[226:229], v[64:67]
	v_mfma_f32_16x16x32_bf16 v[92:95], v[190:193], v[206:209], v[92:95]
	v_mfma_f32_16x16x32_bf16 v[88:91], v[198:201], v[206:209], v[88:91]
	v_mfma_f32_16x16x32_bf16 v[84:87], v[186:189], v[210:213], v[84:87]
	v_mfma_f32_16x16x32_bf16 v[80:83], v[194:197], v[210:213], v[80:83]
	v_mfma_f32_16x16x32_bf16 v[76:79], v[190:193], v[222:225], v[76:79]
	v_mfma_f32_16x16x32_bf16 v[72:75], v[198:201], v[222:225], v[72:75]
	v_mfma_f32_16x16x32_bf16 v[68:71], v[190:193], v[230:233], v[68:71]
	v_mfma_f32_16x16x32_bf16 v[64:67], v[198:201], v[230:233], v[64:67]
	v_mfma_f32_16x16x32_bf16 v[202:205], v[190:193], v[214:217], v[84:87]
	v_mfma_f32_16x16x32_bf16 v[206:209], v[198:201], v[214:217], v[80:83]
	s_barrier
	s_ashr_i32 s5, s85, 31
	s_add_u32 s34, s6, s85
	s_addc_u32 s35, s7, s5
	s_add_i32 s5, s85, 0xffffff00
	s_mov_b32 m0, s27
	v_lshl_add_u64 v[128:129], s[34:35], 0, v[144:145]
	s_ashr_i32 s27, s5, 31
	ds_read_b128 v[80:83], v172 offset:16384
	ds_read_b128 v[84:87], v172 offset:17408
	ds_read_b128 v[96:99], v172 offset:18432
	ds_read_b128 v[100:103], v172 offset:19456
	ds_read_b128 v[210:213], v172 offset:20480
	ds_read_b128 v[214:217], v172 offset:21504
	ds_read_b128 v[218:221], v172 offset:22528
	ds_read_b128 v[222:225], v172 offset:23552
	global_load_lds_dwordx4 v[128:129], off
	v_lshl_add_u64 v[128:129], s[34:35], 0, v[142:143]
	s_add_u32 s34, s6, s5
	s_mov_b32 m0, vcc_hi
	s_addc_u32 s35, s7, s27
	global_load_lds_dwordx4 v[128:129], off
	v_lshl_add_u64 v[128:129], s[34:35], 0, v[144:145]
	s_mov_b32 m0, s59
	s_nop 0
	global_load_lds_dwordx4 v[128:129], off
	v_lshl_add_u64 v[128:129], s[34:35], 0, v[142:143]
	s_add_u32 s34, s3, s4
	s_mov_b32 m0, s60
	s_addc_u32 s35, s36, 0
	global_load_lds_dwordx4 v[128:129], off
	v_lshl_add_u64 v[128:129], s[34:35], 0, v[148:149]
	s_mov_b32 m0, s63
	s_nop 0
	global_load_lds_dwordx4 v[128:129], off
	v_lshl_add_u64 v[128:129], s[34:35], 0, v[146:147]
	s_mov_b32 m0, s66
	s_nop 0
	global_load_lds_dwordx4 v[128:129], off
	s_waitcnt vmcnt(8)
	s_waitcnt lgkmcnt(0)
	s_barrier
	v_mfma_f32_16x16x32_bf16 v[60:63], v[132:135], v[80:83], v[60:63]
	v_mfma_f32_16x16x32_bf16 v[56:59], v[178:181], v[80:83], v[56:59]
	v_mfma_f32_16x16x32_bf16 v[52:55], v[132:135], v[96:99], v[52:55]
	v_mfma_f32_16x16x32_bf16 v[48:51], v[178:181], v[96:99], v[48:51]
	v_mfma_f32_16x16x32_bf16 v[44:47], v[132:135], v[210:213], v[44:47]
	v_mfma_f32_16x16x32_bf16 v[40:43], v[178:181], v[210:213], v[40:43]
	v_mfma_f32_16x16x32_bf16 v[60:63], v[162:165], v[84:87], v[60:63]
	v_mfma_f32_16x16x32_bf16 v[56:59], v[182:185], v[84:87], v[56:59]
	v_mfma_f32_16x16x32_bf16 v[52:55], v[162:165], v[100:103], v[52:55]
	v_mfma_f32_16x16x32_bf16 v[48:51], v[182:185], v[100:103], v[48:51]
	v_mfma_f32_16x16x32_bf16 v[44:47], v[162:165], v[214:217], v[44:47]
	v_mfma_f32_16x16x32_bf16 v[40:43], v[182:185], v[214:217], v[40:43]
	v_mfma_f32_16x16x32_bf16 v[36:39], v[132:135], v[218:221], v[36:39]
	v_mfma_f32_16x16x32_bf16 v[32:35], v[178:181], v[218:221], v[32:35]
	v_mfma_f32_16x16x32_bf16 v[162:165], v[162:165], v[222:225], v[36:39]
	v_mfma_f32_16x16x32_bf16 v[178:181], v[182:185], v[222:225], v[32:35]
	v_mfma_f32_16x16x32_bf16 v[28:31], v[186:189], v[80:83], v[28:31]
	v_mfma_f32_16x16x32_bf16 v[24:27], v[194:197], v[80:83], v[24:27]
	v_mfma_f32_16x16x32_bf16 v[4:7], v[186:189], v[218:221], v[4:7]
	v_mfma_f32_16x16x32_bf16 v[0:3], v[194:197], v[218:221], v[0:3]
	v_mfma_f32_16x16x32_bf16 v[28:31], v[190:193], v[84:87], v[28:31]
	v_mfma_f32_16x16x32_bf16 v[24:27], v[198:201], v[84:87], v[24:27]
	v_mfma_f32_16x16x32_bf16 v[20:23], v[186:189], v[96:99], v[20:23]
	v_mfma_f32_16x16x32_bf16 v[16:19], v[194:197], v[96:99], v[16:19]
	v_mfma_f32_16x16x32_bf16 v[12:15], v[186:189], v[210:213], v[12:15]
	v_mfma_f32_16x16x32_bf16 v[8:11], v[194:197], v[210:213], v[8:11]
	v_mfma_f32_16x16x32_bf16 v[4:7], v[190:193], v[222:225], v[4:7]
	v_mfma_f32_16x16x32_bf16 v[0:3], v[198:201], v[222:225], v[0:3]
	v_mfma_f32_16x16x32_bf16 v[182:185], v[190:193], v[100:103], v[20:23]
	v_mfma_f32_16x16x32_bf16 v[226:229], v[198:201], v[100:103], v[16:19]
	v_mfma_f32_16x16x32_bf16 v[12:15], v[190:193], v[214:217], v[12:15]
	v_mfma_f32_16x16x32_bf16 v[8:11], v[198:201], v[214:217], v[8:11]
	s_barrier
	ds_read_b128 v[16:19], v130
	ds_read_b128 v[20:23], v130 offset:1024
	ds_read_b128 v[186:189], v130 offset:2048
	ds_read_b128 v[190:193], v130 offset:3072
	ds_read_b128 v[194:197], v131
	ds_read_b128 v[198:201], v131 offset:1024
	ds_read_b128 v[210:213], v131 offset:2048
	ds_read_b128 v[214:217], v131 offset:3072
	s_add_i32 s5, s4, 0x20000
	s_add_u32 s34, s3, s5
	s_addc_u32 s35, s36, 0
	s_mov_b32 m0, s67
	v_lshl_add_u64 v[80:81], s[34:35], 0, v[148:149]
	ds_read_b128 v[32:35], v172 offset:32768
	ds_read_b128 v[36:39], v172 offset:33792
	ds_read_b128 v[218:221], v172 offset:34816
	ds_read_b128 v[222:225], v172 offset:35840
	ds_read_b128 v[230:233], v172 offset:36864
	ds_read_b128 v[242:245], v172 offset:37888
	ds_read_b128 v[246:249], v172 offset:38912
	ds_read_b128 v[250:253], v172 offset:39936
	global_load_lds_dwordx4 v[80:81], off
	v_lshl_add_u64 v[80:81], s[34:35], 0, v[146:147]
	s_mov_b32 m0, s68
	s_nop 0
	global_load_lds_dwordx4 v[80:81], off
	s_waitcnt vmcnt(8)
	s_waitcnt lgkmcnt(0)
	s_barrier
; #define PG_BAR __builtin_amdgcn_s_barrier()
; template <class Epi, class Sched, class Hook = NoHook>
; __device__ __forceinline__ void gemm_phase_w(LAS unsigned char* lds, const Sched& S, const Epi& E, int wave_id, const Hook& HK = Hook()) {
;     ...
;         if constexpr (!SEG2) {
;             for (int tt = 0; tt < nt; tt += 2) {
;                 if constexpr (GATHER) { if (tt == nt - 2) {
;                     if (has_next) { gnxt_00 = S.grow_l(nxt, lds, nbuf, R0) + (unsigned)(C0 * 2); gnxt_01 = S.grow_l(nxt, lds, nbuf, R1) + (unsigned)(C1 * 2); gnxt_10 = S.grow_l(nxt, lds, nbuf, 128 + R0) + (unsigned)(C0 * 2); gnxt_11 = S.grow_l(nxt, lds, nbuf, 128 + R1) + (unsigned)(C1 * 2); }
;                     else { gnxt_00 = gcur_00; gnxt_01 = gcur_01; gnxt_10 = gcur_10; gnxt_11 = gcur_11; } } }
;                 PG_TRIP(tt, false, false, false);
;             }
;         } else {
;             for (int tt = 0; tt < nt - 4; tt += 2) PG_TRIP(tt, false, false, false);
;             PG_TRIP(nt - 4, false, true, false);
;             PG_TRIP(nt - 2, true, false, true);
;         }
;     ...
;         if (wr == 0) PG_BAR;
	v_mfma_f32_16x16x32_bf16 v[80:83], v[16:19], v[32:35], v[124:127]
	v_mfma_f32_16x16x32_bf16 v[132:135], v[20:23], v[36:39], v[80:83]
	v_mfma_f32_16x16x32_bf16 v[80:83], v[186:189], v[32:35], v[120:123]
	v_mfma_f32_16x16x32_bf16 v[128:131], v[190:193], v[36:39], v[80:83]
	v_mfma_f32_16x16x32_bf16 v[80:83], v[16:19], v[218:221], v[116:119]
	v_mfma_f32_16x16x32_bf16 v[116:119], v[20:23], v[222:225], v[80:83]
	v_mfma_f32_16x16x32_bf16 v[80:83], v[186:189], v[218:221], v[112:115]
	v_mfma_f32_16x16x32_bf16 v[112:115], v[190:193], v[222:225], v[80:83]
	v_mfma_f32_16x16x32_bf16 v[80:83], v[16:19], v[230:233], v[108:111]
	v_mfma_f32_16x16x32_bf16 v[100:103], v[20:23], v[242:245], v[80:83]
	v_mfma_f32_16x16x32_bf16 v[80:83], v[186:189], v[230:233], v[104:107]
	v_mfma_f32_16x16x32_bf16 v[96:99], v[190:193], v[242:245], v[80:83]
	v_mfma_f32_16x16x32_bf16 v[80:83], v[16:19], v[246:249], v[234:237]
	v_mfma_f32_16x16x32_bf16 v[84:87], v[20:23], v[250:253], v[80:83]
	v_mfma_f32_16x16x32_bf16 v[80:83], v[186:189], v[246:249], v[238:241]
	v_mfma_f32_16x16x32_bf16 v[80:83], v[190:193], v[250:253], v[80:83]
	v_mfma_f32_16x16x32_bf16 v[92:95], v[194:197], v[32:35], v[92:95]
	v_mfma_f32_16x16x32_bf16 v[32:35], v[210:213], v[32:35], v[88:91]
	v_mfma_f32_16x16x32_bf16 v[120:123], v[214:217], v[36:39], v[32:35]
	v_mfma_f32_16x16x32_bf16 v[32:35], v[194:197], v[218:221], v[202:205]
	v_mfma_f32_16x16x32_bf16 v[108:111], v[198:201], v[222:225], v[32:35]
	v_mfma_f32_16x16x32_bf16 v[32:35], v[210:213], v[218:221], v[206:209]
	v_mfma_f32_16x16x32_bf16 v[104:107], v[214:217], v[222:225], v[32:35]
	v_mfma_f32_16x16x32_bf16 v[32:35], v[194:197], v[230:233], v[76:79]
	v_mfma_f32_16x16x32_bf16 v[124:127], v[198:201], v[36:39], v[92:95]
	v_mfma_f32_16x16x32_bf16 v[92:95], v[198:201], v[242:245], v[32:35]
	v_mfma_f32_16x16x32_bf16 v[32:35], v[210:213], v[230:233], v[72:75]
	v_mfma_f32_16x16x32_bf16 v[88:91], v[214:217], v[242:245], v[32:35]
	v_mfma_f32_16x16x32_bf16 v[32:35], v[194:197], v[246:249], v[68:71]
	v_mfma_f32_16x16x32_bf16 v[76:79], v[198:201], v[250:253], v[32:35]
	v_mfma_f32_16x16x32_bf16 v[32:35], v[210:213], v[246:249], v[64:67]
	v_mfma_f32_16x16x32_bf16 v[72:75], v[214:217], v[250:253], v[32:35]
	s_barrier
	s_add_i32 s34, s85, 0x80
	s_ashr_i32 s35, s34, 31
	s_add_i32 s5, s85, 0xffffff80
	s_mov_b32 m0, s61
	s_nop 0
	v_lshl_add_u64 v[32:33], v[158:159], 0, s[34:35]
	s_ashr_i32 s27, s5, 31
	ds_read_b128 v[202:205], v172 offset:49152
	ds_read_b128 v[206:209], v172 offset:50176
	ds_read_b128 v[218:221], v172 offset:51200
	ds_read_b128 v[222:225], v172 offset:52224
	ds_read_b128 v[230:233], v172 offset:53248
	ds_read_b128 v[234:237], v172 offset:54272
	ds_read_b128 v[238:241], v172 offset:55296
	ds_read_b128 v[242:245], v172 offset:56320
	global_load_lds_dwordx4 v[32:33], off
	v_lshl_add_u64 v[32:33], v[160:161], 0, s[34:35]
	s_add_u32 s34, s6, s5
	s_mov_b32 m0, s49
	s_addc_u32 s35, s7, s27
	s_add_i32 s5, s4, 0x80
	global_load_lds_dwordx4 v[32:33], off
	v_lshl_add_u64 v[32:33], s[34:35], 0, v[144:145]
	s_mov_b32 m0, s26
	s_add_u32 s26, s3, s5
	global_load_lds_dwordx4 v[32:33], off
	v_lshl_add_u64 v[32:33], s[34:35], 0, v[142:143]
	s_mov_b32 m0, s44
	s_addc_u32 s27, s36, 0
	global_load_lds_dwordx4 v[32:33], off
	v_lshl_add_u64 v[32:33], s[26:27], 0, v[148:149]
	s_mov_b32 m0, s71
	s_nop 0
	global_load_lds_dwordx4 v[32:33], off
	v_lshl_add_u64 v[32:33], s[26:27], 0, v[146:147]
	s_mov_b32 m0, s72
	s_nop 0
	global_load_lds_dwordx4 v[32:33], off
	s_waitcnt vmcnt(8)
	s_waitcnt lgkmcnt(0)
	s_barrier
	v_mfma_f32_16x16x32_bf16 v[32:35], v[16:19], v[202:205], v[60:63]
	v_mfma_f32_16x16x32_bf16 v[68:71], v[20:23], v[206:209], v[32:35]
	v_mfma_f32_16x16x32_bf16 v[32:35], v[186:189], v[202:205], v[56:59]
	v_mfma_f32_16x16x32_bf16 v[64:67], v[190:193], v[206:209], v[32:35]
	v_mfma_f32_16x16x32_bf16 v[32:35], v[16:19], v[218:221], v[52:55]
	v_mfma_f32_16x16x32_bf16 v[52:55], v[20:23], v[222:225], v[32:35]
	v_mfma_f32_16x16x32_bf16 v[32:35], v[186:189], v[218:221], v[48:51]
	v_mfma_f32_16x16x32_bf16 v[48:51], v[190:193], v[222:225], v[32:35]
	v_mfma_f32_16x16x32_bf16 v[32:35], v[16:19], v[230:233], v[44:47]
	v_mfma_f32_16x16x32_bf16 v[16:19], v[16:19], v[238:241], v[162:165]
	v_mfma_f32_16x16x32_bf16 v[36:39], v[20:23], v[234:237], v[32:35]
	v_mfma_f32_16x16x32_bf16 v[32:35], v[186:189], v[230:233], v[40:43]
	v_mfma_f32_16x16x32_bf16 v[20:23], v[20:23], v[242:245], v[16:19]
	v_mfma_f32_16x16x32_bf16 v[16:19], v[186:189], v[238:241], v[178:181]
	v_mfma_f32_16x16x32_bf16 v[32:35], v[190:193], v[234:237], v[32:35]
	v_mfma_f32_16x16x32_bf16 v[16:19], v[190:193], v[242:245], v[16:19]
	v_mfma_f32_16x16x32_bf16 v[24:27], v[210:213], v[202:205], v[24:27]
	v_mfma_f32_16x16x32_bf16 v[56:59], v[214:217], v[206:209], v[24:27]
	v_mfma_f32_16x16x32_bf16 v[24:27], v[194:197], v[218:221], v[182:185]
	v_mfma_f32_16x16x32_bf16 v[28:31], v[194:197], v[202:205], v[28:31]
	v_mfma_f32_16x16x32_bf16 v[44:47], v[198:201], v[222:225], v[24:27]
	v_mfma_f32_16x16x32_bf16 v[24:27], v[210:213], v[218:221], v[226:229]
	v_mfma_f32_16x16x32_bf16 v[12:15], v[194:197], v[230:233], v[12:15]
	v_mfma_f32_16x16x32_bf16 v[8:11], v[210:213], v[230:233], v[8:11]
	v_mfma_f32_16x16x32_bf16 v[4:7], v[194:197], v[238:241], v[4:7]
	v_mfma_f32_16x16x32_bf16 v[0:3], v[210:213], v[238:241], v[0:3]
	v_mfma_f32_16x16x32_bf16 v[60:63], v[198:201], v[206:209], v[28:31]
	v_mfma_f32_16x16x32_bf16 v[40:43], v[214:217], v[222:225], v[24:27]
	v_mfma_f32_16x16x32_bf16 v[28:31], v[198:201], v[234:237], v[12:15]
	v_mfma_f32_16x16x32_bf16 v[24:27], v[214:217], v[234:237], v[8:11]
	v_mfma_f32_16x16x32_bf16 v[4:7], v[198:201], v[242:245], v[4:7]
	v_mfma_f32_16x16x32_bf16 v[0:3], v[214:217], v[242:245], v[0:3]
	s_barrier
	s_and_b64 vcc, exec, s[64:65]
	s_cbranch_vccz .LBB0_1779
	s_barrier

.LBB0_1854:
	ds_read_b128 v[100:103], v197
	ds_read_b128 v[132:135], v197 offset:1024
	ds_read_b128 v[136:139], v197 offset:2048
	ds_read_b128 v[140:143], v197 offset:3072
	ds_read_b128 v[144:147], v198
	ds_read_b128 v[148:151], v198 offset:1024
	ds_read_b128 v[152:155], v198 offset:2048
	ds_read_b128 v[156:159], v198 offset:3072
	s_add_i32 s53, s21, 2
	s_cmp_eq_u32 s20, 0x9f000
	s_cselect_b32 s59, s48, s51
	s_cselect_b32 s60, 0, s53
	s_cselect_b32 s58, s49, s52
	s_add_i32 s61, s52, s20
	s_add_u32 s62, s3, s61
	s_addc_u32 s63, s30, 0
	v_lshl_add_u64 v[190:191], s[62:63], 0, v[164:165]
	s_add_i32 m0, s23, 0xc000
	ds_read_b128 v[160:163], v199
	ds_read_b128 v[174:177], v199 offset:1024
	ds_read_b128 v[178:181], v199 offset:2048
	ds_read_b128 v[182:185], v199 offset:3072
	ds_read_b128 v[186:189], v199 offset:4096
	ds_read_b128 v[200:203], v199 offset:5120
	ds_read_b128 v[204:207], v199 offset:6144
	ds_read_b128 v[208:211], v199 offset:7168
	global_load_lds_dwordx4 v[190:191], off
	v_lshl_add_u64 v[190:191], s[62:63], 0, v[166:167]
	s_add_i32 m0, s23, 0xe000
	s_nop 0
	global_load_lds_dwordx4 v[190:191], off
	s_waitcnt vmcnt(8)
	s_waitcnt lgkmcnt(0)
	s_barrier
	v_mfma_f32_16x16x32_bf16 v[128:131], v[100:103], v[160:163], v[128:131]
	v_mfma_f32_16x16x32_bf16 v[124:127], v[136:139], v[160:163], v[124:127]
	v_mfma_f32_16x16x32_bf16 v[116:119], v[100:103], v[178:181], v[116:119]
	v_mfma_f32_16x16x32_bf16 v[108:111], v[136:139], v[178:181], v[108:111]
	v_mfma_f32_16x16x32_bf16 v[92:95], v[100:103], v[186:189], v[92:95]
	v_mfma_f32_16x16x32_bf16 v[84:87], v[136:139], v[186:189], v[84:87]
	v_mfma_f32_16x16x32_bf16 v[76:79], v[100:103], v[204:207], v[76:79]
	v_mfma_f32_16x16x32_bf16 v[68:71], v[136:139], v[204:207], v[68:71]
	v_mfma_f32_16x16x32_bf16 v[128:131], v[132:135], v[174:177], v[128:131]
	v_mfma_f32_16x16x32_bf16 v[124:127], v[140:143], v[174:177], v[124:127]
	v_mfma_f32_16x16x32_bf16 v[116:119], v[132:135], v[182:185], v[116:119]
	v_mfma_f32_16x16x32_bf16 v[108:111], v[140:143], v[182:185], v[108:111]
	v_mfma_f32_16x16x32_bf16 v[92:95], v[132:135], v[200:203], v[92:95]
	v_mfma_f32_16x16x32_bf16 v[84:87], v[140:143], v[200:203], v[84:87]
	v_mfma_f32_16x16x32_bf16 v[76:79], v[132:135], v[208:211], v[76:79]
	v_mfma_f32_16x16x32_bf16 v[68:71], v[140:143], v[208:211], v[68:71]
	v_mfma_f32_16x16x32_bf16 v[96:99], v[144:147], v[160:163], v[96:99]
	v_mfma_f32_16x16x32_bf16 v[120:123], v[152:155], v[160:163], v[120:123]
	v_mfma_f32_16x16x32_bf16 v[112:115], v[144:147], v[178:181], v[112:115]
	v_mfma_f32_16x16x32_bf16 v[104:107], v[152:155], v[178:181], v[104:107]
	v_mfma_f32_16x16x32_bf16 v[88:91], v[144:147], v[186:189], v[88:91]
	v_mfma_f32_16x16x32_bf16 v[80:83], v[152:155], v[186:189], v[80:83]
	v_mfma_f32_16x16x32_bf16 v[72:75], v[144:147], v[204:207], v[72:75]
	v_mfma_f32_16x16x32_bf16 v[64:67], v[152:155], v[204:207], v[64:67]
	v_mfma_f32_16x16x32_bf16 v[96:99], v[148:151], v[174:177], v[96:99]
	v_mfma_f32_16x16x32_bf16 v[120:123], v[156:159], v[174:177], v[120:123]
	v_mfma_f32_16x16x32_bf16 v[112:115], v[148:151], v[182:185], v[112:115]
	v_mfma_f32_16x16x32_bf16 v[104:107], v[156:159], v[182:185], v[104:107]
	v_mfma_f32_16x16x32_bf16 v[88:91], v[148:151], v[200:203], v[88:91]
	v_mfma_f32_16x16x32_bf16 v[80:83], v[156:159], v[200:203], v[80:83]
	v_mfma_f32_16x16x32_bf16 v[72:75], v[148:151], v[208:211], v[72:75]
	v_mfma_f32_16x16x32_bf16 v[64:67], v[156:159], v[208:211], v[64:67]
	s_barrier
	s_lshl_b32 s61, s60, 7
	s_add_i32 s62, s61, s59
	s_ashr_i32 s63, s62, 31
	s_add_u32 s62, s4, s62
	s_addc_u32 s63, s5, s63
	s_add_i32 s66, s42, s31
	v_lshl_add_u64 v[190:191], s[62:63], 0, v[168:169]
	s_mov_b32 m0, s66
	ds_read_b128 v[160:163], v199 offset:16384
	ds_read_b128 v[174:177], v199 offset:17408
	ds_read_b128 v[178:181], v199 offset:18432
	ds_read_b128 v[182:185], v199 offset:19456
	ds_read_b128 v[186:189], v199 offset:20480
	ds_read_b128 v[200:203], v199 offset:21504
	ds_read_b128 v[204:207], v199 offset:22528
	ds_read_b128 v[208:211], v199 offset:23552
	global_load_lds_dwordx4 v[190:191], off
	s_add_i32 m0, s66, 0x2000
	s_add_i32 s66, s59, 0x80000
	s_add_i32 s61, s66, s61
	v_lshl_add_u64 v[190:191], s[62:63], 0, v[170:171]
	s_ashr_i32 s63, s61, 31
	s_add_u32 s62, s4, s61
	s_addc_u32 s63, s5, s63
	s_add_i32 s61, s43, s31
	global_load_lds_dwordx4 v[190:191], off
	v_lshl_add_u64 v[190:191], s[62:63], 0, v[168:169]
	s_mov_b32 m0, s61
	s_nop 0
	global_load_lds_dwordx4 v[190:191], off
	s_add_i32 m0, s61, 0x2000
	s_lshl_b32 s61, s60, 12
	s_add_i32 s61, s61, s58
	v_lshl_add_u64 v[190:191], s[62:63], 0, v[170:171]
	s_add_u32 s62, s3, s61
	s_addc_u32 s63, s30, 0
	global_load_lds_dwordx4 v[190:191], off
	v_lshl_add_u64 v[190:191], s[62:63], 0, v[164:165]
	s_mov_b32 m0, s23
	s_nop 0
	global_load_lds_dwordx4 v[190:191], off
	v_lshl_add_u64 v[190:191], s[62:63], 0, v[166:167]
	s_mov_b32 m0, s24
	s_nop 0
	global_load_lds_dwordx4 v[190:191], off
	s_waitcnt vmcnt(8)
	s_waitcnt lgkmcnt(0)
	s_barrier
	v_mfma_f32_16x16x32_bf16 v[60:63], v[100:103], v[160:163], v[60:63]
	v_mfma_f32_16x16x32_bf16 v[52:55], v[136:139], v[160:163], v[52:55]
	v_mfma_f32_16x16x32_bf16 v[44:47], v[100:103], v[178:181], v[44:47]
	v_mfma_f32_16x16x32_bf16 v[36:39], v[136:139], v[178:181], v[36:39]
	v_mfma_f32_16x16x32_bf16 v[28:31], v[100:103], v[186:189], v[28:31]
	v_mfma_f32_16x16x32_bf16 v[20:23], v[136:139], v[186:189], v[20:23]
	v_mfma_f32_16x16x32_bf16 v[12:15], v[100:103], v[204:207], v[12:15]
	v_mfma_f32_16x16x32_bf16 v[4:7], v[136:139], v[204:207], v[4:7]
	v_mfma_f32_16x16x32_bf16 v[60:63], v[132:135], v[174:177], v[60:63]
	v_mfma_f32_16x16x32_bf16 v[52:55], v[140:143], v[174:177], v[52:55]
	v_mfma_f32_16x16x32_bf16 v[44:47], v[132:135], v[182:185], v[44:47]
	v_mfma_f32_16x16x32_bf16 v[36:39], v[140:143], v[182:185], v[36:39]
	v_mfma_f32_16x16x32_bf16 v[28:31], v[132:135], v[200:203], v[28:31]
	v_mfma_f32_16x16x32_bf16 v[20:23], v[140:143], v[200:203], v[20:23]
	v_mfma_f32_16x16x32_bf16 v[12:15], v[132:135], v[208:211], v[12:15]
	v_mfma_f32_16x16x32_bf16 v[4:7], v[140:143], v[208:211], v[4:7]
	v_mfma_f32_16x16x32_bf16 v[56:59], v[144:147], v[160:163], v[56:59]
	v_mfma_f32_16x16x32_bf16 v[48:51], v[152:155], v[160:163], v[48:51]
	v_mfma_f32_16x16x32_bf16 v[40:43], v[144:147], v[178:181], v[40:43]
	v_mfma_f32_16x16x32_bf16 v[32:35], v[152:155], v[178:181], v[32:35]
	v_mfma_f32_16x16x32_bf16 v[24:27], v[144:147], v[186:189], v[24:27]
	v_mfma_f32_16x16x32_bf16 v[16:19], v[152:155], v[186:189], v[16:19]
	v_mfma_f32_16x16x32_bf16 v[8:11], v[144:147], v[204:207], v[8:11]
	v_mfma_f32_16x16x32_bf16 v[0:3], v[152:155], v[204:207], v[0:3]
	v_mfma_f32_16x16x32_bf16 v[56:59], v[148:151], v[174:177], v[56:59]
	v_mfma_f32_16x16x32_bf16 v[48:51], v[156:159], v[174:177], v[48:51]
	v_mfma_f32_16x16x32_bf16 v[40:43], v[148:151], v[182:185], v[40:43]
	v_mfma_f32_16x16x32_bf16 v[32:35], v[156:159], v[182:185], v[32:35]
	v_mfma_f32_16x16x32_bf16 v[24:27], v[148:151], v[200:203], v[24:27]
	v_mfma_f32_16x16x32_bf16 v[16:19], v[156:159], v[200:203], v[16:19]
	v_mfma_f32_16x16x32_bf16 v[8:11], v[148:151], v[208:211], v[8:11]
	v_mfma_f32_16x16x32_bf16 v[0:3], v[156:159], v[208:211], v[0:3]
	s_barrier
	s_add_i32 s67, 0, 0x18000
	s_add_i32 s68, 0, 0x1c000
	v_add_u32_e32 v140, s67, v195
	v_add_u32_e32 v156, s68, v195
	ds_read_b128 v[100:103], v140
	ds_read_b128 v[132:135], v140 offset:1024
	ds_read_b128 v[136:139], v140 offset:2048
	ds_read_b128 v[140:143], v140 offset:3072
	ds_read_b128 v[144:147], v156
	ds_read_b128 v[148:151], v156 offset:1024
	ds_read_b128 v[152:155], v156 offset:2048
	ds_read_b128 v[156:159], v156 offset:3072
	s_add_i32 s61, s61, 0x80000
	s_add_u32 s62, s3, s61
	s_addc_u32 s63, s30, 0
	s_mov_b32 m0, s25
	v_lshl_add_u64 v[190:191], s[62:63], 0, v[164:165]
	ds_read_b128 v[160:163], v199 offset:32768
	ds_read_b128 v[174:177], v199 offset:33792
	ds_read_b128 v[178:181], v199 offset:34816
	ds_read_b128 v[182:185], v199 offset:35840
	ds_read_b128 v[186:189], v199 offset:36864
	ds_read_b128 v[200:203], v199 offset:37888
	ds_read_b128 v[204:207], v199 offset:38912
	ds_read_b128 v[208:211], v199 offset:39936
	global_load_lds_dwordx4 v[190:191], off
	v_lshl_add_u64 v[190:191], s[62:63], 0, v[166:167]
	s_mov_b32 m0, s26
	s_nop 0
	global_load_lds_dwordx4 v[190:191], off
	s_waitcnt vmcnt(8)
	s_waitcnt lgkmcnt(0)
	s_barrier
	v_mfma_f32_16x16x32_bf16 v[128:131], v[100:103], v[160:163], v[128:131]
	v_mfma_f32_16x16x32_bf16 v[124:127], v[136:139], v[160:163], v[124:127]
	v_mfma_f32_16x16x32_bf16 v[116:119], v[100:103], v[178:181], v[116:119]
	v_mfma_f32_16x16x32_bf16 v[108:111], v[136:139], v[178:181], v[108:111]
	v_mfma_f32_16x16x32_bf16 v[92:95], v[100:103], v[186:189], v[92:95]
	v_mfma_f32_16x16x32_bf16 v[84:87], v[136:139], v[186:189], v[84:87]
	v_mfma_f32_16x16x32_bf16 v[76:79], v[100:103], v[204:207], v[76:79]
	v_mfma_f32_16x16x32_bf16 v[68:71], v[136:139], v[204:207], v[68:71]
	v_mfma_f32_16x16x32_bf16 v[128:131], v[132:135], v[174:177], v[128:131]
	v_mfma_f32_16x16x32_bf16 v[124:127], v[140:143], v[174:177], v[124:127]
	v_mfma_f32_16x16x32_bf16 v[116:119], v[132:135], v[182:185], v[116:119]
	v_mfma_f32_16x16x32_bf16 v[108:111], v[140:143], v[182:185], v[108:111]
	v_mfma_f32_16x16x32_bf16 v[92:95], v[132:135], v[200:203], v[92:95]
	v_mfma_f32_16x16x32_bf16 v[84:87], v[140:143], v[200:203], v[84:87]
	v_mfma_f32_16x16x32_bf16 v[76:79], v[132:135], v[208:211], v[76:79]
	v_mfma_f32_16x16x32_bf16 v[68:71], v[140:143], v[208:211], v[68:71]
	v_mfma_f32_16x16x32_bf16 v[96:99], v[144:147], v[160:163], v[96:99]
	v_mfma_f32_16x16x32_bf16 v[120:123], v[152:155], v[160:163], v[120:123]
	v_mfma_f32_16x16x32_bf16 v[112:115], v[144:147], v[178:181], v[112:115]
	v_mfma_f32_16x16x32_bf16 v[104:107], v[152:155], v[178:181], v[104:107]
	v_mfma_f32_16x16x32_bf16 v[88:91], v[144:147], v[186:189], v[88:91]
	v_mfma_f32_16x16x32_bf16 v[80:83], v[152:155], v[186:189], v[80:83]
	v_mfma_f32_16x16x32_bf16 v[72:75], v[144:147], v[204:207], v[72:75]
	v_mfma_f32_16x16x32_bf16 v[64:67], v[152:155], v[204:207], v[64:67]
	v_mfma_f32_16x16x32_bf16 v[96:99], v[148:151], v[174:177], v[96:99]
	v_mfma_f32_16x16x32_bf16 v[120:123], v[156:159], v[174:177], v[120:123]
	v_mfma_f32_16x16x32_bf16 v[112:115], v[148:151], v[182:185], v[112:115]
	v_mfma_f32_16x16x32_bf16 v[104:107], v[156:159], v[182:185], v[104:107]
	v_mfma_f32_16x16x32_bf16 v[88:91], v[148:151], v[200:203], v[88:91]
	v_mfma_f32_16x16x32_bf16 v[80:83], v[156:159], v[200:203], v[80:83]
	v_mfma_f32_16x16x32_bf16 v[72:75], v[148:151], v[208:211], v[72:75]
	v_mfma_f32_16x16x32_bf16 v[64:67], v[156:159], v[208:211], v[64:67]
	s_barrier
; template <class Epi, class Sched, class Hook = NoHook>
; __device__ __forceinline__ void gemm_phase_w(LAS unsigned char* lds, const Sched& S, const Epi& E, int wave_id, const Hook& HK = Hook()) {
;     ...
;         if constexpr (!SEG2) {
;             for (int tt = 0; tt < nt; tt += 2) {
;                 if constexpr (GATHER) { if (tt == nt - 2) {
;                     if (has_next) { gnxt_00 = S.grow_l(nxt, lds, nbuf, R0) + (unsigned)(C0 * 2); gnxt_01 = S.grow_l(nxt, lds, nbuf, R1) + (unsigned)(C1 * 2); gnxt_10 = S.grow_l(nxt, lds, nbuf, 128 + R0) + (unsigned)(C0 * 2); gnxt_11 = S.grow_l(nxt, lds, nbuf, 128 + R1) + (unsigned)(C1 * 2); }
;                     else { gnxt_00 = gcur_00; gnxt_01 = gcur_01; gnxt_10 = gcur_10; gnxt_11 = gcur_11; } } }
;                 PG_TRIP(tt, false, false, false);
;             }
	s_or_b32 s62, s60, 1
	s_lshl_b32 s63, s62, 7
	s_add_i32 s59, s63, s59
	s_ashr_i32 s61, s59, 31
	s_add_u32 s60, s4, s59
	s_addc_u32 s61, s5, s61
	s_add_i32 s59, s67, s31
	v_lshl_add_u64 v[190:191], s[60:61], 0, v[168:169]
	s_mov_b32 m0, s59
	s_add_i32 s63, s63, s66
	ds_read_b128 v[160:163], v199 offset:49152
	ds_read_b128 v[174:177], v199 offset:50176
	ds_read_b128 v[178:181], v199 offset:51200
	ds_read_b128 v[182:185], v199 offset:52224
	ds_read_b128 v[186:189], v199 offset:53248
	ds_read_b128 v[200:203], v199 offset:54272
	ds_read_b128 v[204:207], v199 offset:55296
	ds_read_b128 v[208:211], v199 offset:56320
	global_load_lds_dwordx4 v[190:191], off
	s_add_i32 m0, s59, 0x2000
	s_ashr_i32 s59, s63, 31
	v_lshl_add_u64 v[190:191], s[60:61], 0, v[170:171]
	s_add_u32 s60, s4, s63
	s_addc_u32 s61, s5, s59
	s_add_i32 s59, s68, s31
	global_load_lds_dwordx4 v[190:191], off
	v_lshl_add_u64 v[190:191], s[60:61], 0, v[168:169]
	s_mov_b32 m0, s59
	s_nop 0
	global_load_lds_dwordx4 v[190:191], off
	s_add_i32 m0, s59, 0x2000
	s_lshl_b32 s59, s62, 12
	s_add_i32 s59, s59, s58
	s_add_u32 s58, s3, s59
	v_lshl_add_u64 v[190:191], s[60:61], 0, v[170:171]
	s_addc_u32 s59, s30, 0
	global_load_lds_dwordx4 v[190:191], off
	v_lshl_add_u64 v[190:191], s[58:59], 0, v[164:165]
	s_mov_b32 m0, s28
	s_nop 0
	global_load_lds_dwordx4 v[190:191], off
	v_lshl_add_u64 v[190:191], s[58:59], 0, v[166:167]
	s_mov_b32 m0, s29
	s_nop 0
	global_load_lds_dwordx4 v[190:191], off
	s_waitcnt vmcnt(8)
	s_waitcnt lgkmcnt(0)
	s_barrier
	v_mfma_f32_16x16x32_bf16 v[60:63], v[100:103], v[160:163], v[60:63]
	v_mfma_f32_16x16x32_bf16 v[52:55], v[136:139], v[160:163], v[52:55]
	v_mfma_f32_16x16x32_bf16 v[44:47], v[100:103], v[178:181], v[44:47]
	v_mfma_f32_16x16x32_bf16 v[36:39], v[136:139], v[178:181], v[36:39]
	v_mfma_f32_16x16x32_bf16 v[28:31], v[100:103], v[186:189], v[28:31]
	v_mfma_f32_16x16x32_bf16 v[20:23], v[136:139], v[186:189], v[20:23]
	v_mfma_f32_16x16x32_bf16 v[12:15], v[100:103], v[204:207], v[12:15]
	v_mfma_f32_16x16x32_bf16 v[4:7], v[136:139], v[204:207], v[4:7]
	v_mfma_f32_16x16x32_bf16 v[60:63], v[132:135], v[174:177], v[60:63]
	v_mfma_f32_16x16x32_bf16 v[52:55], v[140:143], v[174:177], v[52:55]
	v_mfma_f32_16x16x32_bf16 v[44:47], v[132:135], v[182:185], v[44:47]
	v_mfma_f32_16x16x32_bf16 v[36:39], v[140:143], v[182:185], v[36:39]
	v_mfma_f32_16x16x32_bf16 v[28:31], v[132:135], v[200:203], v[28:31]
	v_mfma_f32_16x16x32_bf16 v[20:23], v[140:143], v[200:203], v[20:23]
	v_mfma_f32_16x16x32_bf16 v[12:15], v[132:135], v[208:211], v[12:15]
	v_mfma_f32_16x16x32_bf16 v[4:7], v[140:143], v[208:211], v[4:7]
	v_mfma_f32_16x16x32_bf16 v[56:59], v[144:147], v[160:163], v[56:59]
	v_mfma_f32_16x16x32_bf16 v[48:51], v[152:155], v[160:163], v[48:51]
	v_mfma_f32_16x16x32_bf16 v[40:43], v[144:147], v[178:181], v[40:43]
	v_mfma_f32_16x16x32_bf16 v[32:35], v[152:155], v[178:181], v[32:35]
	v_mfma_f32_16x16x32_bf16 v[24:27], v[144:147], v[186:189], v[24:27]
	v_mfma_f32_16x16x32_bf16 v[16:19], v[152:155], v[186:189], v[16:19]
	v_mfma_f32_16x16x32_bf16 v[8:11], v[144:147], v[204:207], v[8:11]
	v_mfma_f32_16x16x32_bf16 v[0:3], v[152:155], v[204:207], v[0:3]
	v_mfma_f32_16x16x32_bf16 v[56:59], v[148:151], v[174:177], v[56:59]
	v_mfma_f32_16x16x32_bf16 v[48:51], v[156:159], v[174:177], v[48:51]
	v_mfma_f32_16x16x32_bf16 v[40:43], v[148:151], v[182:185], v[40:43]
	v_mfma_f32_16x16x32_bf16 v[32:35], v[156:159], v[182:185], v[32:35]
	v_mfma_f32_16x16x32_bf16 v[24:27], v[148:151], v[200:203], v[24:27]
	v_mfma_f32_16x16x32_bf16 v[16:19], v[156:159], v[200:203], v[16:19]
	v_mfma_f32_16x16x32_bf16 v[8:11], v[148:151], v[208:211], v[8:11]
	v_mfma_f32_16x16x32_bf16 v[0:3], v[156:159], v[208:211], v[0:3]
	s_barrier
	s_addk_i32 s20, 0x2000
	s_cmp_gt_u32 s21, 29
	s_mov_b32 s21, s53
	s_cbranch_scc0 .LBB0_1854
	s_and_b64 vcc, exec, s[16:17]
	s_cbranch_vccz .LBB0_1857
	s_barrier

.LBB0_1983:
	ds_read_b128 v[100:103], v195
	ds_read_b128 v[132:135], v195 offset:1024
	ds_read_b128 v[136:139], v195 offset:2048
	ds_read_b128 v[140:143], v195 offset:3072
	ds_read_b128 v[144:147], v196
	ds_read_b128 v[148:151], v196 offset:1024
	ds_read_b128 v[152:155], v196 offset:2048
	ds_read_b128 v[156:159], v196 offset:3072
	s_add_i32 s45, s21, 2
	s_cmp_eq_u32 s20, 0x9f000
	s_cselect_b32 s49, s40, s43
	s_cselect_b32 s50, 0, s45
	s_cselect_b32 s48, s41, s44
	s_add_i32 s51, s44, s20
	s_add_u32 s52, s3, s51
	s_addc_u32 s53, s30, 0
	v_lshl_add_u64 v[190:191], s[52:53], 0, v[164:165]
	s_add_i32 m0, s24, 0xc000
	ds_read_b128 v[160:163], v197
	ds_read_b128 v[174:177], v197 offset:1024
	ds_read_b128 v[178:181], v197 offset:2048
	ds_read_b128 v[182:185], v197 offset:3072
	ds_read_b128 v[186:189], v197 offset:4096
	ds_read_b128 v[198:201], v197 offset:5120
	ds_read_b128 v[202:205], v197 offset:6144
	ds_read_b128 v[206:209], v197 offset:7168
	global_load_lds_dwordx4 v[190:191], off
	v_lshl_add_u64 v[190:191], s[52:53], 0, v[166:167]
	s_add_i32 m0, s24, 0xe000
	s_nop 0
	global_load_lds_dwordx4 v[190:191], off
	s_waitcnt vmcnt(8)
	s_waitcnt lgkmcnt(0)
	s_barrier
	v_mfma_f32_16x16x32_bf16 v[128:131], v[100:103], v[160:163], v[128:131]
	v_mfma_f32_16x16x32_bf16 v[124:127], v[136:139], v[160:163], v[124:127]
	v_mfma_f32_16x16x32_bf16 v[116:119], v[100:103], v[178:181], v[116:119]
	v_mfma_f32_16x16x32_bf16 v[108:111], v[136:139], v[178:181], v[108:111]
	v_mfma_f32_16x16x32_bf16 v[92:95], v[100:103], v[186:189], v[92:95]
	v_mfma_f32_16x16x32_bf16 v[84:87], v[136:139], v[186:189], v[84:87]
	v_mfma_f32_16x16x32_bf16 v[76:79], v[100:103], v[202:205], v[76:79]
	v_mfma_f32_16x16x32_bf16 v[68:71], v[136:139], v[202:205], v[68:71]
	v_mfma_f32_16x16x32_bf16 v[128:131], v[132:135], v[174:177], v[128:131]
	v_mfma_f32_16x16x32_bf16 v[124:127], v[140:143], v[174:177], v[124:127]
	v_mfma_f32_16x16x32_bf16 v[116:119], v[132:135], v[182:185], v[116:119]
	v_mfma_f32_16x16x32_bf16 v[108:111], v[140:143], v[182:185], v[108:111]
	v_mfma_f32_16x16x32_bf16 v[92:95], v[132:135], v[198:201], v[92:95]
	v_mfma_f32_16x16x32_bf16 v[84:87], v[140:143], v[198:201], v[84:87]
	v_mfma_f32_16x16x32_bf16 v[76:79], v[132:135], v[206:209], v[76:79]
	v_mfma_f32_16x16x32_bf16 v[68:71], v[140:143], v[206:209], v[68:71]
	v_mfma_f32_16x16x32_bf16 v[96:99], v[144:147], v[160:163], v[96:99]
	v_mfma_f32_16x16x32_bf16 v[120:123], v[152:155], v[160:163], v[120:123]
	v_mfma_f32_16x16x32_bf16 v[112:115], v[144:147], v[178:181], v[112:115]
	v_mfma_f32_16x16x32_bf16 v[104:107], v[152:155], v[178:181], v[104:107]
	v_mfma_f32_16x16x32_bf16 v[88:91], v[144:147], v[186:189], v[88:91]
	v_mfma_f32_16x16x32_bf16 v[80:83], v[152:155], v[186:189], v[80:83]
	v_mfma_f32_16x16x32_bf16 v[72:75], v[144:147], v[202:205], v[72:75]
	v_mfma_f32_16x16x32_bf16 v[64:67], v[152:155], v[202:205], v[64:67]
	v_mfma_f32_16x16x32_bf16 v[96:99], v[148:151], v[174:177], v[96:99]
	v_mfma_f32_16x16x32_bf16 v[120:123], v[156:159], v[174:177], v[120:123]
	v_mfma_f32_16x16x32_bf16 v[112:115], v[148:151], v[182:185], v[112:115]
	v_mfma_f32_16x16x32_bf16 v[104:107], v[156:159], v[182:185], v[104:107]
	v_mfma_f32_16x16x32_bf16 v[88:91], v[148:151], v[198:201], v[88:91]
	v_mfma_f32_16x16x32_bf16 v[80:83], v[156:159], v[198:201], v[80:83]
	v_mfma_f32_16x16x32_bf16 v[72:75], v[148:151], v[206:209], v[72:75]
	v_mfma_f32_16x16x32_bf16 v[64:67], v[156:159], v[206:209], v[64:67]
	s_barrier
	s_lshl_b32 s51, s50, 7
	s_add_i32 s52, s51, s49
	s_ashr_i32 s53, s52, 31
	s_add_u32 s52, s4, s52
	s_addc_u32 s53, s5, s53
	s_add_i32 s58, s34, s31
	v_lshl_add_u64 v[190:191], s[52:53], 0, v[168:169]
	s_mov_b32 m0, s58
	ds_read_b128 v[160:163], v197 offset:16384
	ds_read_b128 v[174:177], v197 offset:17408
	ds_read_b128 v[178:181], v197 offset:18432
	ds_read_b128 v[182:185], v197 offset:19456
	ds_read_b128 v[186:189], v197 offset:20480
	ds_read_b128 v[198:201], v197 offset:21504
	ds_read_b128 v[202:205], v197 offset:22528
	ds_read_b128 v[206:209], v197 offset:23552
	global_load_lds_dwordx4 v[190:191], off
	s_add_i32 m0, s58, 0x2000
	s_add_i32 s58, s49, 0x80000
	s_add_i32 s51, s58, s51
	v_lshl_add_u64 v[190:191], s[52:53], 0, v[170:171]
	s_ashr_i32 s53, s51, 31
	s_add_u32 s52, s4, s51
	s_addc_u32 s53, s5, s53
	s_add_i32 s51, s36, s31
	global_load_lds_dwordx4 v[190:191], off
	v_lshl_add_u64 v[190:191], s[52:53], 0, v[168:169]
	s_mov_b32 m0, s51
	s_nop 0
	global_load_lds_dwordx4 v[190:191], off
	s_add_i32 m0, s51, 0x2000
	s_lshl_b32 s51, s50, 12
	s_add_i32 s51, s51, s48
	v_lshl_add_u64 v[190:191], s[52:53], 0, v[170:171]
	s_add_u32 s52, s3, s51
	s_addc_u32 s53, s30, 0
	global_load_lds_dwordx4 v[190:191], off
	v_lshl_add_u64 v[190:191], s[52:53], 0, v[164:165]
	s_mov_b32 m0, s24
	s_nop 0
	global_load_lds_dwordx4 v[190:191], off
	v_lshl_add_u64 v[190:191], s[52:53], 0, v[166:167]
	s_mov_b32 m0, s25
	s_nop 0
	global_load_lds_dwordx4 v[190:191], off
	s_waitcnt vmcnt(8)
	s_waitcnt lgkmcnt(0)
	s_barrier
	v_mfma_f32_16x16x32_bf16 v[60:63], v[100:103], v[160:163], v[60:63]
	v_mfma_f32_16x16x32_bf16 v[52:55], v[136:139], v[160:163], v[52:55]
	v_mfma_f32_16x16x32_bf16 v[44:47], v[100:103], v[178:181], v[44:47]
	v_mfma_f32_16x16x32_bf16 v[36:39], v[136:139], v[178:181], v[36:39]
	v_mfma_f32_16x16x32_bf16 v[28:31], v[100:103], v[186:189], v[28:31]
	v_mfma_f32_16x16x32_bf16 v[20:23], v[136:139], v[186:189], v[20:23]
	v_mfma_f32_16x16x32_bf16 v[12:15], v[100:103], v[202:205], v[12:15]
	v_mfma_f32_16x16x32_bf16 v[4:7], v[136:139], v[202:205], v[4:7]
	v_mfma_f32_16x16x32_bf16 v[60:63], v[132:135], v[174:177], v[60:63]
	v_mfma_f32_16x16x32_bf16 v[52:55], v[140:143], v[174:177], v[52:55]
	v_mfma_f32_16x16x32_bf16 v[44:47], v[132:135], v[182:185], v[44:47]
	v_mfma_f32_16x16x32_bf16 v[36:39], v[140:143], v[182:185], v[36:39]
	v_mfma_f32_16x16x32_bf16 v[28:31], v[132:135], v[198:201], v[28:31]
	v_mfma_f32_16x16x32_bf16 v[20:23], v[140:143], v[198:201], v[20:23]
	v_mfma_f32_16x16x32_bf16 v[12:15], v[132:135], v[206:209], v[12:15]
	v_mfma_f32_16x16x32_bf16 v[4:7], v[140:143], v[206:209], v[4:7]
	v_mfma_f32_16x16x32_bf16 v[56:59], v[144:147], v[160:163], v[56:59]
	v_mfma_f32_16x16x32_bf16 v[48:51], v[152:155], v[160:163], v[48:51]
	v_mfma_f32_16x16x32_bf16 v[40:43], v[144:147], v[178:181], v[40:43]
	v_mfma_f32_16x16x32_bf16 v[32:35], v[152:155], v[178:181], v[32:35]
	v_mfma_f32_16x16x32_bf16 v[24:27], v[144:147], v[186:189], v[24:27]
	v_mfma_f32_16x16x32_bf16 v[16:19], v[152:155], v[186:189], v[16:19]
	v_mfma_f32_16x16x32_bf16 v[8:11], v[144:147], v[202:205], v[8:11]
	v_mfma_f32_16x16x32_bf16 v[0:3], v[152:155], v[202:205], v[0:3]
	v_mfma_f32_16x16x32_bf16 v[56:59], v[148:151], v[174:177], v[56:59]
	v_mfma_f32_16x16x32_bf16 v[48:51], v[156:159], v[174:177], v[48:51]
	v_mfma_f32_16x16x32_bf16 v[40:43], v[148:151], v[182:185], v[40:43]
	v_mfma_f32_16x16x32_bf16 v[32:35], v[156:159], v[182:185], v[32:35]
	v_mfma_f32_16x16x32_bf16 v[24:27], v[148:151], v[198:201], v[24:27]
	v_mfma_f32_16x16x32_bf16 v[16:19], v[156:159], v[198:201], v[16:19]
	v_mfma_f32_16x16x32_bf16 v[8:11], v[148:151], v[206:209], v[8:11]
	v_mfma_f32_16x16x32_bf16 v[0:3], v[156:159], v[206:209], v[0:3]
	s_barrier
	s_add_i32 s59, 0, 0x18000
	s_add_i32 s60, 0, 0x1c000
	v_add_u32_e32 v140, s59, v193
	v_add_u32_e32 v156, s60, v193
	ds_read_b128 v[100:103], v140
	ds_read_b128 v[132:135], v140 offset:1024
	ds_read_b128 v[136:139], v140 offset:2048
	ds_read_b128 v[140:143], v140 offset:3072
	ds_read_b128 v[144:147], v156
	ds_read_b128 v[148:151], v156 offset:1024
	ds_read_b128 v[152:155], v156 offset:2048
	ds_read_b128 v[156:159], v156 offset:3072
	s_add_i32 s51, s51, 0x80000
	s_add_u32 s52, s3, s51
	s_addc_u32 s53, s30, 0
	s_mov_b32 m0, s26
	v_lshl_add_u64 v[190:191], s[52:53], 0, v[164:165]
	ds_read_b128 v[160:163], v197 offset:32768
	ds_read_b128 v[174:177], v197 offset:33792
	ds_read_b128 v[178:181], v197 offset:34816
	ds_read_b128 v[182:185], v197 offset:35840
	ds_read_b128 v[186:189], v197 offset:36864
	ds_read_b128 v[198:201], v197 offset:37888
	ds_read_b128 v[202:205], v197 offset:38912
	ds_read_b128 v[206:209], v197 offset:39936
	global_load_lds_dwordx4 v[190:191], off
	v_lshl_add_u64 v[190:191], s[52:53], 0, v[166:167]
	s_mov_b32 m0, s27
	s_nop 0
	global_load_lds_dwordx4 v[190:191], off
	s_waitcnt vmcnt(8)
	s_waitcnt lgkmcnt(0)
	s_barrier
	v_mfma_f32_16x16x32_bf16 v[128:131], v[100:103], v[160:163], v[128:131]
	v_mfma_f32_16x16x32_bf16 v[124:127], v[136:139], v[160:163], v[124:127]
	v_mfma_f32_16x16x32_bf16 v[116:119], v[100:103], v[178:181], v[116:119]
	v_mfma_f32_16x16x32_bf16 v[108:111], v[136:139], v[178:181], v[108:111]
	v_mfma_f32_16x16x32_bf16 v[92:95], v[100:103], v[186:189], v[92:95]
	v_mfma_f32_16x16x32_bf16 v[84:87], v[136:139], v[186:189], v[84:87]
	v_mfma_f32_16x16x32_bf16 v[76:79], v[100:103], v[202:205], v[76:79]
	v_mfma_f32_16x16x32_bf16 v[68:71], v[136:139], v[202:205], v[68:71]
	v_mfma_f32_16x16x32_bf16 v[128:131], v[132:135], v[174:177], v[128:131]
	v_mfma_f32_16x16x32_bf16 v[124:127], v[140:143], v[174:177], v[124:127]
	v_mfma_f32_16x16x32_bf16 v[116:119], v[132:135], v[182:185], v[116:119]
	v_mfma_f32_16x16x32_bf16 v[108:111], v[140:143], v[182:185], v[108:111]
	v_mfma_f32_16x16x32_bf16 v[92:95], v[132:135], v[198:201], v[92:95]
	v_mfma_f32_16x16x32_bf16 v[84:87], v[140:143], v[198:201], v[84:87]
	v_mfma_f32_16x16x32_bf16 v[76:79], v[132:135], v[206:209], v[76:79]
	v_mfma_f32_16x16x32_bf16 v[68:71], v[140:143], v[206:209], v[68:71]
	v_mfma_f32_16x16x32_bf16 v[96:99], v[144:147], v[160:163], v[96:99]
	v_mfma_f32_16x16x32_bf16 v[120:123], v[152:155], v[160:163], v[120:123]
	v_mfma_f32_16x16x32_bf16 v[112:115], v[144:147], v[178:181], v[112:115]
	v_mfma_f32_16x16x32_bf16 v[104:107], v[152:155], v[178:181], v[104:107]
	v_mfma_f32_16x16x32_bf16 v[88:91], v[144:147], v[186:189], v[88:91]
	v_mfma_f32_16x16x32_bf16 v[80:83], v[152:155], v[186:189], v[80:83]
	v_mfma_f32_16x16x32_bf16 v[72:75], v[144:147], v[202:205], v[72:75]
	v_mfma_f32_16x16x32_bf16 v[64:67], v[152:155], v[202:205], v[64:67]
	v_mfma_f32_16x16x32_bf16 v[96:99], v[148:151], v[174:177], v[96:99]
	v_mfma_f32_16x16x32_bf16 v[120:123], v[156:159], v[174:177], v[120:123]
	v_mfma_f32_16x16x32_bf16 v[112:115], v[148:151], v[182:185], v[112:115]
	v_mfma_f32_16x16x32_bf16 v[104:107], v[156:159], v[182:185], v[104:107]
	v_mfma_f32_16x16x32_bf16 v[88:91], v[148:151], v[198:201], v[88:91]
	v_mfma_f32_16x16x32_bf16 v[80:83], v[156:159], v[198:201], v[80:83]
	v_mfma_f32_16x16x32_bf16 v[72:75], v[148:151], v[206:209], v[72:75]
	v_mfma_f32_16x16x32_bf16 v[64:67], v[156:159], v[206:209], v[64:67]
	s_barrier
; template <class Epi, class Sched, class Hook = NoHook>
; __device__ __forceinline__ void gemm_phase_w(LAS unsigned char* lds, const Sched& S, const Epi& E, int wave_id, const Hook& HK = Hook()) {
;     ...
;         if constexpr (!SEG2) {
;             for (int tt = 0; tt < nt; tt += 2) {
;                 if constexpr (GATHER) { if (tt == nt - 2) {
;                     if (has_next) { gnxt_00 = S.grow_l(nxt, lds, nbuf, R0) + (unsigned)(C0 * 2); gnxt_01 = S.grow_l(nxt, lds, nbuf, R1) + (unsigned)(C1 * 2); gnxt_10 = S.grow_l(nxt, lds, nbuf, 128 + R0) + (unsigned)(C0 * 2); gnxt_11 = S.grow_l(nxt, lds, nbuf, 128 + R1) + (unsigned)(C1 * 2); }
;                     else { gnxt_00 = gcur_00; gnxt_01 = gcur_01; gnxt_10 = gcur_10; gnxt_11 = gcur_11; } } }
;                 PG_TRIP(tt, false, false, false);
;             }
	s_or_b32 s52, s50, 1
	s_lshl_b32 s53, s52, 7
	s_add_i32 s49, s53, s49
	s_ashr_i32 s51, s49, 31
	s_add_u32 s50, s4, s49
	s_addc_u32 s51, s5, s51
	s_add_i32 s49, s59, s31
	v_lshl_add_u64 v[190:191], s[50:51], 0, v[168:169]
	s_mov_b32 m0, s49
	s_add_i32 s53, s53, s58
	ds_read_b128 v[160:163], v197 offset:49152
	ds_read_b128 v[174:177], v197 offset:50176
	ds_read_b128 v[178:181], v197 offset:51200
	ds_read_b128 v[182:185], v197 offset:52224
	ds_read_b128 v[186:189], v197 offset:53248
	ds_read_b128 v[198:201], v197 offset:54272
	ds_read_b128 v[202:205], v197 offset:55296
	ds_read_b128 v[206:209], v197 offset:56320
	global_load_lds_dwordx4 v[190:191], off
	s_add_i32 m0, s49, 0x2000
	s_ashr_i32 s49, s53, 31
	v_lshl_add_u64 v[190:191], s[50:51], 0, v[170:171]
	s_add_u32 s50, s4, s53
	s_addc_u32 s51, s5, s49
	s_add_i32 s49, s60, s31
	global_load_lds_dwordx4 v[190:191], off
	v_lshl_add_u64 v[190:191], s[50:51], 0, v[168:169]
	s_mov_b32 m0, s49
	s_nop 0
	global_load_lds_dwordx4 v[190:191], off
	s_add_i32 m0, s49, 0x2000
	s_lshl_b32 s49, s52, 12
	s_add_i32 s49, s49, s48
	s_add_u32 s48, s3, s49
	v_lshl_add_u64 v[190:191], s[50:51], 0, v[170:171]
	s_addc_u32 s49, s30, 0
	global_load_lds_dwordx4 v[190:191], off
	v_lshl_add_u64 v[190:191], s[48:49], 0, v[164:165]
	s_mov_b32 m0, s29
	s_nop 0
	global_load_lds_dwordx4 v[190:191], off
	v_lshl_add_u64 v[190:191], s[48:49], 0, v[166:167]
	s_mov_b32 m0, s38
	s_nop 0
	global_load_lds_dwordx4 v[190:191], off
	s_waitcnt vmcnt(8)
	s_waitcnt lgkmcnt(0)
	s_barrier
	v_mfma_f32_16x16x32_bf16 v[60:63], v[100:103], v[160:163], v[60:63]
	v_mfma_f32_16x16x32_bf16 v[52:55], v[136:139], v[160:163], v[52:55]
	v_mfma_f32_16x16x32_bf16 v[44:47], v[100:103], v[178:181], v[44:47]
	v_mfma_f32_16x16x32_bf16 v[36:39], v[136:139], v[178:181], v[36:39]
	v_mfma_f32_16x16x32_bf16 v[28:31], v[100:103], v[186:189], v[28:31]
	v_mfma_f32_16x16x32_bf16 v[20:23], v[136:139], v[186:189], v[20:23]
	v_mfma_f32_16x16x32_bf16 v[12:15], v[100:103], v[202:205], v[12:15]
	v_mfma_f32_16x16x32_bf16 v[4:7], v[136:139], v[202:205], v[4:7]
	v_mfma_f32_16x16x32_bf16 v[60:63], v[132:135], v[174:177], v[60:63]
	v_mfma_f32_16x16x32_bf16 v[52:55], v[140:143], v[174:177], v[52:55]
	v_mfma_f32_16x16x32_bf16 v[44:47], v[132:135], v[182:185], v[44:47]
	v_mfma_f32_16x16x32_bf16 v[36:39], v[140:143], v[182:185], v[36:39]
	v_mfma_f32_16x16x32_bf16 v[28:31], v[132:135], v[198:201], v[28:31]
	v_mfma_f32_16x16x32_bf16 v[20:23], v[140:143], v[198:201], v[20:23]
	v_mfma_f32_16x16x32_bf16 v[12:15], v[132:135], v[206:209], v[12:15]
	v_mfma_f32_16x16x32_bf16 v[4:7], v[140:143], v[206:209], v[4:7]
	v_mfma_f32_16x16x32_bf16 v[56:59], v[144:147], v[160:163], v[56:59]
	v_mfma_f32_16x16x32_bf16 v[48:51], v[152:155], v[160:163], v[48:51]
	v_mfma_f32_16x16x32_bf16 v[40:43], v[144:147], v[178:181], v[40:43]
	v_mfma_f32_16x16x32_bf16 v[32:35], v[152:155], v[178:181], v[32:35]
	v_mfma_f32_16x16x32_bf16 v[24:27], v[144:147], v[186:189], v[24:27]
	v_mfma_f32_16x16x32_bf16 v[16:19], v[152:155], v[186:189], v[16:19]
	v_mfma_f32_16x16x32_bf16 v[8:11], v[144:147], v[202:205], v[8:11]
	v_mfma_f32_16x16x32_bf16 v[0:3], v[152:155], v[202:205], v[0:3]
	v_mfma_f32_16x16x32_bf16 v[56:59], v[148:151], v[174:177], v[56:59]
	v_mfma_f32_16x16x32_bf16 v[48:51], v[156:159], v[174:177], v[48:51]
	v_mfma_f32_16x16x32_bf16 v[40:43], v[148:151], v[182:185], v[40:43]
	v_mfma_f32_16x16x32_bf16 v[32:35], v[156:159], v[182:185], v[32:35]
	v_mfma_f32_16x16x32_bf16 v[24:27], v[148:151], v[198:201], v[24:27]
	v_mfma_f32_16x16x32_bf16 v[16:19], v[156:159], v[198:201], v[16:19]
	v_mfma_f32_16x16x32_bf16 v[8:11], v[148:151], v[206:209], v[8:11]
	v_mfma_f32_16x16x32_bf16 v[0:3], v[156:159], v[206:209], v[0:3]
	s_barrier
	s_addk_i32 s20, 0x2000
	s_cmp_gt_u32 s21, 29
	s_mov_b32 s21, s45
	s_cbranch_scc0 .LBB0_1983
	s_and_b64 vcc, exec, s[16:17]
	s_cbranch_vccz .LBB0_1986
	s_barrier

.LBB0_2156:
	v_add_u32_e32 v147, s69, v166
	ds_read_b128 v[186:189], v147
	ds_read_b128 v[190:193], v147 offset:1024
	ds_read_b128 v[194:197], v147 offset:2048
	ds_read_b128 v[198:201], v147 offset:3072
	v_add_u32_e32 v147, s70, v166
	ds_read_b128 v[202:205], v147
	ds_read_b128 v[206:209], v147 offset:1024
	ds_read_b128 v[210:213], v147 offset:2048
	ds_read_b128 v[214:217], v147 offset:3072
	v_lshl_add_u64 v[250:251], s[38:39], 0, v[130:131]
	s_add_i32 m0, s58, 0xc000
	ds_read_b128 v[218:221], v182
	ds_read_b128 v[222:225], v182 offset:1024
	ds_read_b128 v[226:229], v182 offset:2048
	ds_read_b128 v[230:233], v182 offset:3072
	ds_read_b128 v[234:237], v182 offset:4096
	ds_read_b128 v[238:241], v182 offset:5120
	ds_read_b128 v[242:245], v182 offset:6144
	ds_read_b128 v[246:249], v182 offset:7168
	global_load_lds_dwordx4 v[250:251], off
	v_lshl_add_u64 v[250:251], s[38:39], 0, v[132:133]
	s_add_i32 m0, s58, 0xe000
	s_nop 0
	global_load_lds_dwordx4 v[250:251], off
	s_waitcnt vmcnt(8)
	s_waitcnt lgkmcnt(0)
	s_barrier
	v_mfma_f32_16x16x32_bf16 v[124:127], v[186:189], v[218:221], v[124:127]
	v_mfma_f32_16x16x32_bf16 v[120:123], v[194:197], v[218:221], v[120:123]
	v_mfma_f32_16x16x32_bf16 v[108:111], v[186:189], v[226:229], v[108:111]
	v_mfma_f32_16x16x32_bf16 v[104:107], v[194:197], v[226:229], v[104:107]
	v_mfma_f32_16x16x32_bf16 v[92:95], v[186:189], v[234:237], v[92:95]
	v_mfma_f32_16x16x32_bf16 v[88:91], v[194:197], v[234:237], v[88:91]
	v_mfma_f32_16x16x32_bf16 v[76:79], v[186:189], v[242:245], v[76:79]
	v_mfma_f32_16x16x32_bf16 v[72:75], v[194:197], v[242:245], v[72:75]
	v_mfma_f32_16x16x32_bf16 v[124:127], v[190:193], v[222:225], v[124:127]
	v_mfma_f32_16x16x32_bf16 v[120:123], v[198:201], v[222:225], v[120:123]
	v_mfma_f32_16x16x32_bf16 v[108:111], v[190:193], v[230:233], v[108:111]
	v_mfma_f32_16x16x32_bf16 v[104:107], v[198:201], v[230:233], v[104:107]
	v_mfma_f32_16x16x32_bf16 v[92:95], v[190:193], v[238:241], v[92:95]
	v_mfma_f32_16x16x32_bf16 v[88:91], v[198:201], v[238:241], v[88:91]
	v_mfma_f32_16x16x32_bf16 v[76:79], v[190:193], v[246:249], v[76:79]
	v_mfma_f32_16x16x32_bf16 v[72:75], v[198:201], v[246:249], v[72:75]
	v_mfma_f32_16x16x32_bf16 v[116:119], v[202:205], v[218:221], v[116:119]
	v_mfma_f32_16x16x32_bf16 v[112:115], v[210:213], v[218:221], v[112:115]
	v_mfma_f32_16x16x32_bf16 v[100:103], v[202:205], v[226:229], v[100:103]
	v_mfma_f32_16x16x32_bf16 v[96:99], v[210:213], v[226:229], v[96:99]
	v_mfma_f32_16x16x32_bf16 v[84:87], v[202:205], v[234:237], v[84:87]
	v_mfma_f32_16x16x32_bf16 v[80:83], v[210:213], v[234:237], v[80:83]
	v_mfma_f32_16x16x32_bf16 v[68:71], v[202:205], v[242:245], v[68:71]
	v_mfma_f32_16x16x32_bf16 v[64:67], v[210:213], v[242:245], v[64:67]
	v_mfma_f32_16x16x32_bf16 v[116:119], v[206:209], v[222:225], v[116:119]
	v_mfma_f32_16x16x32_bf16 v[112:115], v[214:217], v[222:225], v[112:115]
	v_mfma_f32_16x16x32_bf16 v[100:103], v[206:209], v[230:233], v[100:103]
	v_mfma_f32_16x16x32_bf16 v[96:99], v[214:217], v[230:233], v[96:99]
	v_mfma_f32_16x16x32_bf16 v[84:87], v[206:209], v[238:241], v[84:87]
	v_mfma_f32_16x16x32_bf16 v[80:83], v[214:217], v[238:241], v[80:83]
	v_mfma_f32_16x16x32_bf16 v[68:71], v[206:209], v[246:249], v[68:71]
	v_mfma_f32_16x16x32_bf16 v[64:67], v[214:217], v[246:249], v[64:67]
	s_barrier
	s_and_b64 s[40:41], s[40:41], exec
	s_cselect_b32 s22, 0, s80
	s_add_i32 s84, s81, s22
	s_ashr_i32 s41, s84, 31
	s_add_u32 s40, s16, s84
	s_addc_u32 s41, s17, s41
	s_add_i32 s85, s69, s44
	v_lshl_add_u64 v[250:251], s[40:41], 0, v[136:137]
	s_mov_b32 m0, s85
	s_add_i32 s84, s84, 0x80000
	ds_read_b128 v[218:221], v182 offset:16384
	ds_read_b128 v[222:225], v182 offset:17408
	ds_read_b128 v[226:229], v182 offset:18432
	ds_read_b128 v[230:233], v182 offset:19456
	ds_read_b128 v[234:237], v182 offset:20480
	ds_read_b128 v[238:241], v182 offset:21504
	ds_read_b128 v[242:245], v182 offset:22528
	ds_read_b128 v[246:249], v182 offset:23552
	global_load_lds_dwordx4 v[250:251], off
	v_lshl_add_u64 v[250:251], s[40:41], 0, v[138:139]
	s_add_i32 m0, s85, 0x2000
	s_ashr_i32 s41, s84, 31
	s_add_u32 s40, s16, s84
	s_addc_u32 s41, s17, s41
	s_add_i32 s84, s70, s44
	global_load_lds_dwordx4 v[250:251], off
	v_lshl_add_u64 v[250:251], s[40:41], 0, v[136:137]
	s_mov_b32 m0, s84
	v_mov_b32_e32 v147, v141
	global_load_lds_dwordx4 v[250:251], off
	s_add_i32 m0, s84, 0x2000
	v_lshl_add_u64 v[250:251], s[40:41], 0, v[138:139]
	s_add_u32 s40, s14, s22
	global_load_lds_dwordx4 v[250:251], off
	s_addc_u32 s41, s15, 0
	s_mov_b32 m0, s58
	s_nop 0
	global_load_lds_dwordx4 v140, s[40:41]
	s_mov_b32 m0, s59
	s_nop 0
	global_load_lds_dwordx4 v146, s[40:41]
	s_waitcnt vmcnt(8)
	s_waitcnt lgkmcnt(0)
	s_barrier
	v_mfma_f32_16x16x32_bf16 v[60:63], v[186:189], v[218:221], v[60:63]
	v_mfma_f32_16x16x32_bf16 v[56:59], v[194:197], v[218:221], v[56:59]
	v_mfma_f32_16x16x32_bf16 v[44:47], v[186:189], v[226:229], v[44:47]
	v_mfma_f32_16x16x32_bf16 v[40:43], v[194:197], v[226:229], v[40:43]
	v_mfma_f32_16x16x32_bf16 v[28:31], v[186:189], v[234:237], v[28:31]
	v_mfma_f32_16x16x32_bf16 v[24:27], v[194:197], v[234:237], v[24:27]
	v_mfma_f32_16x16x32_bf16 v[12:15], v[186:189], v[242:245], v[12:15]
	v_mfma_f32_16x16x32_bf16 v[8:11], v[194:197], v[242:245], v[8:11]
	v_mfma_f32_16x16x32_bf16 v[60:63], v[190:193], v[222:225], v[60:63]
	v_mfma_f32_16x16x32_bf16 v[56:59], v[198:201], v[222:225], v[56:59]
	v_mfma_f32_16x16x32_bf16 v[44:47], v[190:193], v[230:233], v[44:47]
	v_mfma_f32_16x16x32_bf16 v[40:43], v[198:201], v[230:233], v[40:43]
	v_mfma_f32_16x16x32_bf16 v[28:31], v[190:193], v[238:241], v[28:31]
	v_mfma_f32_16x16x32_bf16 v[24:27], v[198:201], v[238:241], v[24:27]
	v_mfma_f32_16x16x32_bf16 v[12:15], v[190:193], v[246:249], v[12:15]
	v_mfma_f32_16x16x32_bf16 v[8:11], v[198:201], v[246:249], v[8:11]
	v_mfma_f32_16x16x32_bf16 v[52:55], v[202:205], v[218:221], v[52:55]
	v_mfma_f32_16x16x32_bf16 v[48:51], v[210:213], v[218:221], v[48:51]
	v_mfma_f32_16x16x32_bf16 v[36:39], v[202:205], v[226:229], v[36:39]
	v_mfma_f32_16x16x32_bf16 v[32:35], v[210:213], v[226:229], v[32:35]
	v_mfma_f32_16x16x32_bf16 v[20:23], v[202:205], v[234:237], v[20:23]
	v_mfma_f32_16x16x32_bf16 v[16:19], v[210:213], v[234:237], v[16:19]
	v_mfma_f32_16x16x32_bf16 v[4:7], v[202:205], v[242:245], v[4:7]
	v_mfma_f32_16x16x32_bf16 v[0:3], v[210:213], v[242:245], v[0:3]
	v_mfma_f32_16x16x32_bf16 v[52:55], v[206:209], v[222:225], v[52:55]
	v_mfma_f32_16x16x32_bf16 v[48:51], v[214:217], v[222:225], v[48:51]
	v_mfma_f32_16x16x32_bf16 v[36:39], v[206:209], v[230:233], v[36:39]
	v_mfma_f32_16x16x32_bf16 v[32:35], v[214:217], v[230:233], v[32:35]
	v_mfma_f32_16x16x32_bf16 v[20:23], v[206:209], v[238:241], v[20:23]
	v_mfma_f32_16x16x32_bf16 v[16:19], v[214:217], v[238:241], v[16:19]
	v_mfma_f32_16x16x32_bf16 v[4:7], v[206:209], v[246:249], v[4:7]
	v_mfma_f32_16x16x32_bf16 v[0:3], v[214:217], v[246:249], v[0:3]
	s_barrier
	s_add_i32 s84, 0, 0x18000
	v_add_u32_e32 v185, s84, v166
	s_add_i32 s85, 0, 0x1c000
	ds_read_b128 v[186:189], v185
	ds_read_b128 v[190:193], v185 offset:1024
	ds_read_b128 v[194:197], v185 offset:2048
	ds_read_b128 v[198:201], v185 offset:3072
	v_add_u32_e32 v185, s85, v166
	ds_read_b128 v[202:205], v185
	ds_read_b128 v[206:209], v185 offset:1024
	ds_read_b128 v[210:213], v185 offset:2048
	ds_read_b128 v[214:217], v185 offset:3072
	s_mov_b32 m0, s60
	v_lshl_add_u64 v[148:149], s[40:41], 0, v[148:149]
	ds_read_b128 v[218:221], v182 offset:32768
	ds_read_b128 v[222:225], v182 offset:33792
	ds_read_b128 v[226:229], v182 offset:34816
	ds_read_b128 v[230:233], v182 offset:35840
	ds_read_b128 v[234:237], v182 offset:36864
	ds_read_b128 v[238:241], v182 offset:37888
	ds_read_b128 v[242:245], v182 offset:38912
	ds_read_b128 v[246:249], v182 offset:39936
	global_load_lds_dwordx4 v[148:149], off
	v_lshl_add_u64 v[148:149], s[40:41], 0, v[150:151]
	s_mov_b32 m0, s61
	s_nop 0
	global_load_lds_dwordx4 v[148:149], off
	s_waitcnt vmcnt(8)
	s_waitcnt lgkmcnt(0)
	s_barrier
	v_mfma_f32_16x16x32_bf16 v[124:127], v[186:189], v[218:221], v[124:127]
	v_mfma_f32_16x16x32_bf16 v[120:123], v[194:197], v[218:221], v[120:123]
	v_mfma_f32_16x16x32_bf16 v[108:111], v[186:189], v[226:229], v[108:111]
	v_mfma_f32_16x16x32_bf16 v[104:107], v[194:197], v[226:229], v[104:107]
	v_mfma_f32_16x16x32_bf16 v[92:95], v[186:189], v[234:237], v[92:95]
	v_mfma_f32_16x16x32_bf16 v[88:91], v[194:197], v[234:237], v[88:91]
	v_mfma_f32_16x16x32_bf16 v[76:79], v[186:189], v[242:245], v[76:79]
	v_mfma_f32_16x16x32_bf16 v[72:75], v[194:197], v[242:245], v[72:75]
	v_mfma_f32_16x16x32_bf16 v[124:127], v[190:193], v[222:225], v[124:127]
	v_mfma_f32_16x16x32_bf16 v[120:123], v[198:201], v[222:225], v[120:123]
	v_mfma_f32_16x16x32_bf16 v[108:111], v[190:193], v[230:233], v[108:111]
	v_mfma_f32_16x16x32_bf16 v[104:107], v[198:201], v[230:233], v[104:107]
	v_mfma_f32_16x16x32_bf16 v[92:95], v[190:193], v[238:241], v[92:95]
	v_mfma_f32_16x16x32_bf16 v[88:91], v[198:201], v[238:241], v[88:91]
	v_mfma_f32_16x16x32_bf16 v[76:79], v[190:193], v[246:249], v[76:79]
	v_mfma_f32_16x16x32_bf16 v[72:75], v[198:201], v[246:249], v[72:75]
	v_mfma_f32_16x16x32_bf16 v[116:119], v[202:205], v[218:221], v[116:119]
	v_mfma_f32_16x16x32_bf16 v[112:115], v[210:213], v[218:221], v[112:115]
	v_mfma_f32_16x16x32_bf16 v[100:103], v[202:205], v[226:229], v[100:103]
	v_mfma_f32_16x16x32_bf16 v[96:99], v[210:213], v[226:229], v[96:99]
	v_mfma_f32_16x16x32_bf16 v[84:87], v[202:205], v[234:237], v[84:87]
	v_mfma_f32_16x16x32_bf16 v[80:83], v[210:213], v[234:237], v[80:83]
	v_mfma_f32_16x16x32_bf16 v[68:71], v[202:205], v[242:245], v[68:71]
	v_mfma_f32_16x16x32_bf16 v[64:67], v[210:213], v[242:245], v[64:67]
	v_mfma_f32_16x16x32_bf16 v[116:119], v[206:209], v[222:225], v[116:119]
	v_mfma_f32_16x16x32_bf16 v[112:115], v[214:217], v[222:225], v[112:115]
	v_mfma_f32_16x16x32_bf16 v[100:103], v[206:209], v[230:233], v[100:103]
	v_mfma_f32_16x16x32_bf16 v[96:99], v[214:217], v[230:233], v[96:99]
	v_mfma_f32_16x16x32_bf16 v[84:87], v[206:209], v[238:241], v[84:87]
	v_mfma_f32_16x16x32_bf16 v[80:83], v[214:217], v[238:241], v[80:83]
	v_mfma_f32_16x16x32_bf16 v[68:71], v[206:209], v[246:249], v[68:71]
	v_mfma_f32_16x16x32_bf16 v[64:67], v[214:217], v[246:249], v[64:67]
	s_barrier
; template <class Epi, class Sched, class Hook = NoHook>
; __device__ __forceinline__ void gemm_phase_w(LAS unsigned char* lds, const Sched& S, const Epi& E, int wave_id, const Hook& HK = Hook()) {
;     ...
;         if constexpr (!SEG2) {
;             for (int tt = 0; tt < nt; tt += 2) {
;                 if constexpr (GATHER) { if (tt == nt - 2) {
;                     if (has_next) { gnxt_00 = S.grow_l(nxt, lds, nbuf, R0) + (unsigned)(C0 * 2); gnxt_01 = S.grow_l(nxt, lds, nbuf, R1) + (unsigned)(C1 * 2); gnxt_10 = S.grow_l(nxt, lds, nbuf, 128 + R0) + (unsigned)(C0 * 2); gnxt_11 = S.grow_l(nxt, lds, nbuf, 128 + R1) + (unsigned)(C1 * 2); }
;                     else { gnxt_00 = gcur_00; gnxt_01 = gcur_01; gnxt_10 = gcur_10; gnxt_11 = gcur_11; } } }
;                 PG_TRIP(tt, false, false, false);
;             }
	s_bitset1_b32 s22, 7
	s_add_i32 s81, s81, s22
	s_ashr_i32 s41, s81, 31
	s_add_u32 s40, s16, s81
	s_addc_u32 s41, s17, s41
	s_add_i32 s84, s84, s44
	v_lshl_add_u64 v[246:247], s[40:41], 0, v[136:137]
	s_mov_b32 m0, s84
	s_add_i32 s81, s81, 0x80000
	ds_read_b128 v[148:151], v182 offset:49152
	ds_read_b128 v[218:221], v182 offset:50176
	ds_read_b128 v[222:225], v182 offset:51200
	ds_read_b128 v[226:229], v182 offset:52224
	ds_read_b128 v[230:233], v182 offset:53248
	ds_read_b128 v[234:237], v182 offset:54272
	ds_read_b128 v[238:241], v182 offset:55296
	ds_read_b128 v[242:245], v182 offset:56320
	global_load_lds_dwordx4 v[246:247], off
	v_lshl_add_u64 v[246:247], s[40:41], 0, v[138:139]
	s_add_i32 m0, s84, 0x2000
	s_ashr_i32 s41, s81, 31
	s_add_u32 s40, s16, s81
	s_addc_u32 s41, s17, s41
	s_add_i32 s81, s85, s44
	global_load_lds_dwordx4 v[246:247], off
	v_lshl_add_u64 v[246:247], s[40:41], 0, v[136:137]
	s_mov_b32 m0, s81
	v_lshl_add_u64 v[146:147], s[14:15], 0, v[146:147]
	global_load_lds_dwordx4 v[246:247], off
	v_lshl_add_u64 v[246:247], s[40:41], 0, v[138:139]
	s_add_i32 m0, s81, 0x2000
	v_lshl_add_u64 v[146:147], v[146:147], 0, s[22:23]
	global_load_lds_dwordx4 v[246:247], off
	v_lshl_add_u64 v[246:247], s[14:15], 0, v[140:141]
	v_lshl_add_u64 v[246:247], v[246:247], 0, s[22:23]
	s_mov_b32 m0, s62
	s_nop 0
	global_load_lds_dwordx4 v[246:247], off
	s_mov_b32 m0, s63
	s_nop 0
	global_load_lds_dwordx4 v[146:147], off
	s_waitcnt vmcnt(8)
	s_waitcnt lgkmcnt(0)
	s_barrier
	v_mfma_f32_16x16x32_bf16 v[60:63], v[186:189], v[148:151], v[60:63]
	v_mfma_f32_16x16x32_bf16 v[56:59], v[194:197], v[148:151], v[56:59]
	v_mfma_f32_16x16x32_bf16 v[44:47], v[186:189], v[222:225], v[44:47]
	v_mfma_f32_16x16x32_bf16 v[40:43], v[194:197], v[222:225], v[40:43]
	v_mfma_f32_16x16x32_bf16 v[28:31], v[186:189], v[230:233], v[28:31]
	v_mfma_f32_16x16x32_bf16 v[24:27], v[194:197], v[230:233], v[24:27]
	v_mfma_f32_16x16x32_bf16 v[12:15], v[186:189], v[238:241], v[12:15]
	v_mfma_f32_16x16x32_bf16 v[8:11], v[194:197], v[238:241], v[8:11]
	v_mfma_f32_16x16x32_bf16 v[60:63], v[190:193], v[218:221], v[60:63]
	v_mfma_f32_16x16x32_bf16 v[56:59], v[198:201], v[218:221], v[56:59]
	v_mfma_f32_16x16x32_bf16 v[44:47], v[190:193], v[226:229], v[44:47]
	v_mfma_f32_16x16x32_bf16 v[40:43], v[198:201], v[226:229], v[40:43]
	v_mfma_f32_16x16x32_bf16 v[28:31], v[190:193], v[234:237], v[28:31]
	v_mfma_f32_16x16x32_bf16 v[24:27], v[198:201], v[234:237], v[24:27]
	v_mfma_f32_16x16x32_bf16 v[12:15], v[190:193], v[242:245], v[12:15]
	v_mfma_f32_16x16x32_bf16 v[8:11], v[198:201], v[242:245], v[8:11]
	v_mfma_f32_16x16x32_bf16 v[52:55], v[202:205], v[148:151], v[52:55]
	v_mfma_f32_16x16x32_bf16 v[48:51], v[210:213], v[148:151], v[48:51]
	v_mfma_f32_16x16x32_bf16 v[36:39], v[202:205], v[222:225], v[36:39]
	v_mfma_f32_16x16x32_bf16 v[32:35], v[210:213], v[222:225], v[32:35]
	v_mfma_f32_16x16x32_bf16 v[20:23], v[202:205], v[230:233], v[20:23]
	v_mfma_f32_16x16x32_bf16 v[16:19], v[210:213], v[230:233], v[16:19]
	v_mfma_f32_16x16x32_bf16 v[4:7], v[202:205], v[238:241], v[4:7]
	v_mfma_f32_16x16x32_bf16 v[0:3], v[210:213], v[238:241], v[0:3]
	v_mfma_f32_16x16x32_bf16 v[52:55], v[206:209], v[218:221], v[52:55]
	v_mfma_f32_16x16x32_bf16 v[48:51], v[214:217], v[218:221], v[48:51]
	v_mfma_f32_16x16x32_bf16 v[36:39], v[206:209], v[226:229], v[36:39]
	v_mfma_f32_16x16x32_bf16 v[32:35], v[214:217], v[226:229], v[32:35]
	v_mfma_f32_16x16x32_bf16 v[20:23], v[206:209], v[234:237], v[20:23]
	v_mfma_f32_16x16x32_bf16 v[16:19], v[214:217], v[234:237], v[16:19]
	v_mfma_f32_16x16x32_bf16 v[4:7], v[206:209], v[242:245], v[4:7]
	v_mfma_f32_16x16x32_bf16 v[0:3], v[214:217], v[242:245], v[0:3]
	s_barrier
	s_add_i32 s79, s79, 2
	s_addk_i32 s80, 0x100
	s_add_u32 s38, s38, 0x100
	s_addc_u32 s39, s39, 0
	s_cmp_gt_u32 s79, 29
	s_cbranch_scc1 .LBB0_2160

.LBB0_2410:
	v_add_u32_e32 v147, s49, v163
	ds_read_b128 v[182:185], v147
	ds_read_b128 v[186:189], v147 offset:1024
	ds_read_b128 v[190:193], v147 offset:2048
	ds_read_b128 v[194:197], v147 offset:3072
	v_add_u32_e32 v147, s50, v163
	ds_read_b128 v[198:201], v147
	ds_read_b128 v[202:205], v147 offset:1024
	ds_read_b128 v[206:209], v147 offset:2048
	ds_read_b128 v[210:213], v147 offset:3072
	v_lshl_add_u64 v[246:247], s[38:39], 0, v[130:131]
	s_add_i32 m0, s57, 0xc000
	ds_read_b128 v[214:217], v179
	ds_read_b128 v[218:221], v179 offset:1024
	ds_read_b128 v[222:225], v179 offset:2048
	ds_read_b128 v[226:229], v179 offset:3072
	ds_read_b128 v[230:233], v179 offset:4096
	ds_read_b128 v[234:237], v179 offset:5120
	ds_read_b128 v[238:241], v179 offset:6144
	ds_read_b128 v[242:245], v179 offset:7168
	global_load_lds_dwordx4 v[246:247], off
	v_lshl_add_u64 v[246:247], s[38:39], 0, v[132:133]
	s_add_i32 m0, s57, 0xe000
	s_nop 0
	global_load_lds_dwordx4 v[246:247], off
	s_waitcnt vmcnt(8)
	s_waitcnt lgkmcnt(0)
	s_barrier
	v_mfma_f32_16x16x32_bf16 v[124:127], v[182:185], v[214:217], v[124:127]
	v_mfma_f32_16x16x32_bf16 v[120:123], v[190:193], v[214:217], v[120:123]
	v_mfma_f32_16x16x32_bf16 v[108:111], v[182:185], v[222:225], v[108:111]
	v_mfma_f32_16x16x32_bf16 v[104:107], v[190:193], v[222:225], v[104:107]
	v_mfma_f32_16x16x32_bf16 v[92:95], v[182:185], v[230:233], v[92:95]
	v_mfma_f32_16x16x32_bf16 v[88:91], v[190:193], v[230:233], v[88:91]
	v_mfma_f32_16x16x32_bf16 v[76:79], v[182:185], v[238:241], v[76:79]
	v_mfma_f32_16x16x32_bf16 v[72:75], v[190:193], v[238:241], v[72:75]
	v_mfma_f32_16x16x32_bf16 v[124:127], v[186:189], v[218:221], v[124:127]
	v_mfma_f32_16x16x32_bf16 v[120:123], v[194:197], v[218:221], v[120:123]
	v_mfma_f32_16x16x32_bf16 v[108:111], v[186:189], v[226:229], v[108:111]
	v_mfma_f32_16x16x32_bf16 v[104:107], v[194:197], v[226:229], v[104:107]
	v_mfma_f32_16x16x32_bf16 v[92:95], v[186:189], v[234:237], v[92:95]
	v_mfma_f32_16x16x32_bf16 v[88:91], v[194:197], v[234:237], v[88:91]
	v_mfma_f32_16x16x32_bf16 v[76:79], v[186:189], v[242:245], v[76:79]
	v_mfma_f32_16x16x32_bf16 v[72:75], v[194:197], v[242:245], v[72:75]
	v_mfma_f32_16x16x32_bf16 v[116:119], v[198:201], v[214:217], v[116:119]
	v_mfma_f32_16x16x32_bf16 v[112:115], v[206:209], v[214:217], v[112:115]
	v_mfma_f32_16x16x32_bf16 v[100:103], v[198:201], v[222:225], v[100:103]
	v_mfma_f32_16x16x32_bf16 v[96:99], v[206:209], v[222:225], v[96:99]
	v_mfma_f32_16x16x32_bf16 v[84:87], v[198:201], v[230:233], v[84:87]
	v_mfma_f32_16x16x32_bf16 v[80:83], v[206:209], v[230:233], v[80:83]
	v_mfma_f32_16x16x32_bf16 v[68:71], v[198:201], v[238:241], v[68:71]
	v_mfma_f32_16x16x32_bf16 v[64:67], v[206:209], v[238:241], v[64:67]
	v_mfma_f32_16x16x32_bf16 v[116:119], v[202:205], v[218:221], v[116:119]
	v_mfma_f32_16x16x32_bf16 v[112:115], v[210:213], v[218:221], v[112:115]
	v_mfma_f32_16x16x32_bf16 v[100:103], v[202:205], v[226:229], v[100:103]
	v_mfma_f32_16x16x32_bf16 v[96:99], v[210:213], v[226:229], v[96:99]
	v_mfma_f32_16x16x32_bf16 v[84:87], v[202:205], v[234:237], v[84:87]
	v_mfma_f32_16x16x32_bf16 v[80:83], v[210:213], v[234:237], v[80:83]
	v_mfma_f32_16x16x32_bf16 v[68:71], v[202:205], v[242:245], v[68:71]
	v_mfma_f32_16x16x32_bf16 v[64:67], v[210:213], v[242:245], v[64:67]
	s_barrier
	s_and_b64 s[40:41], s[40:41], exec
	s_cselect_b32 s22, 0, s70
	s_add_i32 s72, s71, s22
	s_ashr_i32 s41, s72, 31
	s_add_u32 s40, s16, s72
	s_addc_u32 s41, s17, s41
	s_add_i32 s73, s49, s44
	v_lshl_add_u64 v[246:247], s[40:41], 0, v[136:137]
	s_mov_b32 m0, s73
	s_add_i32 s72, s72, 0x80000
	ds_read_b128 v[214:217], v179 offset:16384
	ds_read_b128 v[218:221], v179 offset:17408
	ds_read_b128 v[222:225], v179 offset:18432
	ds_read_b128 v[226:229], v179 offset:19456
	ds_read_b128 v[230:233], v179 offset:20480
	ds_read_b128 v[234:237], v179 offset:21504
	ds_read_b128 v[238:241], v179 offset:22528
	ds_read_b128 v[242:245], v179 offset:23552
	global_load_lds_dwordx4 v[246:247], off
	v_lshl_add_u64 v[246:247], s[40:41], 0, v[138:139]
	s_add_i32 m0, s73, 0x2000
	s_ashr_i32 s41, s72, 31
	s_add_u32 s40, s16, s72
	s_addc_u32 s41, s17, s41
	s_add_i32 s72, s50, s44
	global_load_lds_dwordx4 v[246:247], off
	v_lshl_add_u64 v[246:247], s[40:41], 0, v[136:137]
	s_mov_b32 m0, s72
	v_mov_b32_e32 v147, v141
	global_load_lds_dwordx4 v[246:247], off
	s_add_i32 m0, s72, 0x2000
	v_lshl_add_u64 v[246:247], s[40:41], 0, v[138:139]
	s_add_u32 s40, s14, s22
	global_load_lds_dwordx4 v[246:247], off
	s_addc_u32 s41, s15, 0
	s_mov_b32 m0, s57
	s_nop 0
	global_load_lds_dwordx4 v140, s[40:41]
	s_mov_b32 m0, s58
	s_nop 0
	global_load_lds_dwordx4 v146, s[40:41]
	s_waitcnt vmcnt(8)
	s_waitcnt lgkmcnt(0)
	s_barrier
	v_mfma_f32_16x16x32_bf16 v[60:63], v[182:185], v[214:217], v[60:63]
	v_mfma_f32_16x16x32_bf16 v[56:59], v[190:193], v[214:217], v[56:59]
	v_mfma_f32_16x16x32_bf16 v[44:47], v[182:185], v[222:225], v[44:47]
	v_mfma_f32_16x16x32_bf16 v[40:43], v[190:193], v[222:225], v[40:43]
	v_mfma_f32_16x16x32_bf16 v[28:31], v[182:185], v[230:233], v[28:31]
	v_mfma_f32_16x16x32_bf16 v[24:27], v[190:193], v[230:233], v[24:27]
	v_mfma_f32_16x16x32_bf16 v[12:15], v[182:185], v[238:241], v[12:15]
	v_mfma_f32_16x16x32_bf16 v[8:11], v[190:193], v[238:241], v[8:11]
	v_mfma_f32_16x16x32_bf16 v[60:63], v[186:189], v[218:221], v[60:63]
	v_mfma_f32_16x16x32_bf16 v[56:59], v[194:197], v[218:221], v[56:59]
	v_mfma_f32_16x16x32_bf16 v[44:47], v[186:189], v[226:229], v[44:47]
	v_mfma_f32_16x16x32_bf16 v[40:43], v[194:197], v[226:229], v[40:43]
	v_mfma_f32_16x16x32_bf16 v[28:31], v[186:189], v[234:237], v[28:31]
	v_mfma_f32_16x16x32_bf16 v[24:27], v[194:197], v[234:237], v[24:27]
	v_mfma_f32_16x16x32_bf16 v[12:15], v[186:189], v[242:245], v[12:15]
	v_mfma_f32_16x16x32_bf16 v[8:11], v[194:197], v[242:245], v[8:11]
	v_mfma_f32_16x16x32_bf16 v[52:55], v[198:201], v[214:217], v[52:55]
	v_mfma_f32_16x16x32_bf16 v[48:51], v[206:209], v[214:217], v[48:51]
	v_mfma_f32_16x16x32_bf16 v[36:39], v[198:201], v[222:225], v[36:39]
	v_mfma_f32_16x16x32_bf16 v[32:35], v[206:209], v[222:225], v[32:35]
	v_mfma_f32_16x16x32_bf16 v[20:23], v[198:201], v[230:233], v[20:23]
	v_mfma_f32_16x16x32_bf16 v[16:19], v[206:209], v[230:233], v[16:19]
	v_mfma_f32_16x16x32_bf16 v[4:7], v[198:201], v[238:241], v[4:7]
	v_mfma_f32_16x16x32_bf16 v[0:3], v[206:209], v[238:241], v[0:3]
	v_mfma_f32_16x16x32_bf16 v[52:55], v[202:205], v[218:221], v[52:55]
	v_mfma_f32_16x16x32_bf16 v[48:51], v[210:213], v[218:221], v[48:51]
	v_mfma_f32_16x16x32_bf16 v[36:39], v[202:205], v[226:229], v[36:39]
	v_mfma_f32_16x16x32_bf16 v[32:35], v[210:213], v[226:229], v[32:35]
	v_mfma_f32_16x16x32_bf16 v[20:23], v[202:205], v[234:237], v[20:23]
	v_mfma_f32_16x16x32_bf16 v[16:19], v[210:213], v[234:237], v[16:19]
	v_mfma_f32_16x16x32_bf16 v[4:7], v[202:205], v[242:245], v[4:7]
	v_mfma_f32_16x16x32_bf16 v[0:3], v[210:213], v[242:245], v[0:3]
	s_barrier
	s_add_i32 s72, 0, 0x18000
	s_add_i32 s73, 0, 0x1c000
	v_add_u32_e32 v194, s72, v163
	v_add_u32_e32 v210, s73, v163
	ds_read_b128 v[182:185], v194
	ds_read_b128 v[186:189], v194 offset:1024
	ds_read_b128 v[190:193], v194 offset:2048
	ds_read_b128 v[194:197], v194 offset:3072
	ds_read_b128 v[198:201], v210
	ds_read_b128 v[202:205], v210 offset:1024
	ds_read_b128 v[206:209], v210 offset:2048
	ds_read_b128 v[210:213], v210 offset:3072
	s_mov_b32 m0, s59
	v_lshl_add_u64 v[148:149], s[40:41], 0, v[148:149]
	ds_read_b128 v[214:217], v179 offset:32768
	ds_read_b128 v[218:221], v179 offset:33792
	ds_read_b128 v[222:225], v179 offset:34816
	ds_read_b128 v[226:229], v179 offset:35840
	ds_read_b128 v[230:233], v179 offset:36864
	ds_read_b128 v[234:237], v179 offset:37888
	ds_read_b128 v[238:241], v179 offset:38912
	ds_read_b128 v[242:245], v179 offset:39936
	global_load_lds_dwordx4 v[148:149], off
	v_lshl_add_u64 v[148:149], s[40:41], 0, v[150:151]
	s_mov_b32 m0, s60
	s_nop 0
	global_load_lds_dwordx4 v[148:149], off
	s_waitcnt vmcnt(8)
	s_waitcnt lgkmcnt(0)
	s_barrier
	v_mfma_f32_16x16x32_bf16 v[124:127], v[182:185], v[214:217], v[124:127]
	v_mfma_f32_16x16x32_bf16 v[120:123], v[190:193], v[214:217], v[120:123]
	v_mfma_f32_16x16x32_bf16 v[108:111], v[182:185], v[222:225], v[108:111]
	v_mfma_f32_16x16x32_bf16 v[104:107], v[190:193], v[222:225], v[104:107]
	v_mfma_f32_16x16x32_bf16 v[92:95], v[182:185], v[230:233], v[92:95]
	v_mfma_f32_16x16x32_bf16 v[88:91], v[190:193], v[230:233], v[88:91]
	v_mfma_f32_16x16x32_bf16 v[76:79], v[182:185], v[238:241], v[76:79]
	v_mfma_f32_16x16x32_bf16 v[72:75], v[190:193], v[238:241], v[72:75]
	v_mfma_f32_16x16x32_bf16 v[124:127], v[186:189], v[218:221], v[124:127]
	v_mfma_f32_16x16x32_bf16 v[120:123], v[194:197], v[218:221], v[120:123]
	v_mfma_f32_16x16x32_bf16 v[108:111], v[186:189], v[226:229], v[108:111]
	v_mfma_f32_16x16x32_bf16 v[104:107], v[194:197], v[226:229], v[104:107]
	v_mfma_f32_16x16x32_bf16 v[92:95], v[186:189], v[234:237], v[92:95]
	v_mfma_f32_16x16x32_bf16 v[88:91], v[194:197], v[234:237], v[88:91]
	v_mfma_f32_16x16x32_bf16 v[76:79], v[186:189], v[242:245], v[76:79]
	v_mfma_f32_16x16x32_bf16 v[72:75], v[194:197], v[242:245], v[72:75]
	v_mfma_f32_16x16x32_bf16 v[116:119], v[198:201], v[214:217], v[116:119]
	v_mfma_f32_16x16x32_bf16 v[112:115], v[206:209], v[214:217], v[112:115]
	v_mfma_f32_16x16x32_bf16 v[100:103], v[198:201], v[222:225], v[100:103]
	v_mfma_f32_16x16x32_bf16 v[96:99], v[206:209], v[222:225], v[96:99]
	v_mfma_f32_16x16x32_bf16 v[84:87], v[198:201], v[230:233], v[84:87]
	v_mfma_f32_16x16x32_bf16 v[80:83], v[206:209], v[230:233], v[80:83]
	v_mfma_f32_16x16x32_bf16 v[68:71], v[198:201], v[238:241], v[68:71]
	v_mfma_f32_16x16x32_bf16 v[64:67], v[206:209], v[238:241], v[64:67]
	v_mfma_f32_16x16x32_bf16 v[116:119], v[202:205], v[218:221], v[116:119]
	v_mfma_f32_16x16x32_bf16 v[112:115], v[210:213], v[218:221], v[112:115]
	v_mfma_f32_16x16x32_bf16 v[100:103], v[202:205], v[226:229], v[100:103]
	v_mfma_f32_16x16x32_bf16 v[96:99], v[210:213], v[226:229], v[96:99]
	v_mfma_f32_16x16x32_bf16 v[84:87], v[202:205], v[234:237], v[84:87]
	v_mfma_f32_16x16x32_bf16 v[80:83], v[210:213], v[234:237], v[80:83]
	v_mfma_f32_16x16x32_bf16 v[68:71], v[202:205], v[242:245], v[68:71]
	v_mfma_f32_16x16x32_bf16 v[64:67], v[210:213], v[242:245], v[64:67]
	s_barrier
; template <class Epi, class Sched, class Hook = NoHook>
; __device__ __forceinline__ void gemm_phase_w(LAS unsigned char* lds, const Sched& S, const Epi& E, int wave_id, const Hook& HK = Hook()) {
;     ...
;         if constexpr (!SEG2) {
;             for (int tt = 0; tt < nt; tt += 2) {
;                 if constexpr (GATHER) { if (tt == nt - 2) {
;                     if (has_next) { gnxt_00 = S.grow_l(nxt, lds, nbuf, R0) + (unsigned)(C0 * 2); gnxt_01 = S.grow_l(nxt, lds, nbuf, R1) + (unsigned)(C1 * 2); gnxt_10 = S.grow_l(nxt, lds, nbuf, 128 + R0) + (unsigned)(C0 * 2); gnxt_11 = S.grow_l(nxt, lds, nbuf, 128 + R1) + (unsigned)(C1 * 2); }
;                     else { gnxt_00 = gcur_00; gnxt_01 = gcur_01; gnxt_10 = gcur_10; gnxt_11 = gcur_11; } } }
;                 PG_TRIP(tt, false, false, false);
;             }
	s_bitset1_b32 s22, 7
	s_add_i32 s71, s71, s22
	s_ashr_i32 s41, s71, 31
	s_add_u32 s40, s16, s71
	s_addc_u32 s41, s17, s41
	s_add_i32 s72, s72, s44
	v_lshl_add_u64 v[242:243], s[40:41], 0, v[136:137]
	s_mov_b32 m0, s72
	s_add_i32 s71, s71, 0x80000
	ds_read_b128 v[148:151], v179 offset:49152
	ds_read_b128 v[214:217], v179 offset:50176
	ds_read_b128 v[218:221], v179 offset:51200
	ds_read_b128 v[222:225], v179 offset:52224
	ds_read_b128 v[226:229], v179 offset:53248
	ds_read_b128 v[230:233], v179 offset:54272
	ds_read_b128 v[234:237], v179 offset:55296
	ds_read_b128 v[238:241], v179 offset:56320
	global_load_lds_dwordx4 v[242:243], off
	v_lshl_add_u64 v[242:243], s[40:41], 0, v[138:139]
	s_add_i32 m0, s72, 0x2000
	s_ashr_i32 s41, s71, 31
	s_add_u32 s40, s16, s71
	s_addc_u32 s41, s17, s41
	s_add_i32 s71, s73, s44
	global_load_lds_dwordx4 v[242:243], off
	v_lshl_add_u64 v[242:243], s[40:41], 0, v[136:137]
	s_mov_b32 m0, s71
	v_lshl_add_u64 v[146:147], s[14:15], 0, v[146:147]
	global_load_lds_dwordx4 v[242:243], off
	v_lshl_add_u64 v[242:243], s[40:41], 0, v[138:139]
	s_add_i32 m0, s71, 0x2000
	v_lshl_add_u64 v[146:147], v[146:147], 0, s[22:23]
	global_load_lds_dwordx4 v[242:243], off
	v_lshl_add_u64 v[242:243], s[14:15], 0, v[140:141]
	v_lshl_add_u64 v[242:243], v[242:243], 0, s[22:23]
	s_mov_b32 m0, s51
	s_nop 0
	global_load_lds_dwordx4 v[242:243], off
	s_mov_b32 m0, s61
	s_nop 0
	global_load_lds_dwordx4 v[146:147], off
	s_waitcnt vmcnt(8)
	s_waitcnt lgkmcnt(0)
	s_barrier
	v_mfma_f32_16x16x32_bf16 v[60:63], v[182:185], v[148:151], v[60:63]
	v_mfma_f32_16x16x32_bf16 v[56:59], v[190:193], v[148:151], v[56:59]
	v_mfma_f32_16x16x32_bf16 v[44:47], v[182:185], v[218:221], v[44:47]
	v_mfma_f32_16x16x32_bf16 v[40:43], v[190:193], v[218:221], v[40:43]
	v_mfma_f32_16x16x32_bf16 v[28:31], v[182:185], v[226:229], v[28:31]
	v_mfma_f32_16x16x32_bf16 v[24:27], v[190:193], v[226:229], v[24:27]
	v_mfma_f32_16x16x32_bf16 v[12:15], v[182:185], v[234:237], v[12:15]
	v_mfma_f32_16x16x32_bf16 v[8:11], v[190:193], v[234:237], v[8:11]
	v_mfma_f32_16x16x32_bf16 v[60:63], v[186:189], v[214:217], v[60:63]
	v_mfma_f32_16x16x32_bf16 v[56:59], v[194:197], v[214:217], v[56:59]
	v_mfma_f32_16x16x32_bf16 v[44:47], v[186:189], v[222:225], v[44:47]
	v_mfma_f32_16x16x32_bf16 v[40:43], v[194:197], v[222:225], v[40:43]
	v_mfma_f32_16x16x32_bf16 v[28:31], v[186:189], v[230:233], v[28:31]
	v_mfma_f32_16x16x32_bf16 v[24:27], v[194:197], v[230:233], v[24:27]
	v_mfma_f32_16x16x32_bf16 v[12:15], v[186:189], v[238:241], v[12:15]
	v_mfma_f32_16x16x32_bf16 v[8:11], v[194:197], v[238:241], v[8:11]
	v_mfma_f32_16x16x32_bf16 v[52:55], v[198:201], v[148:151], v[52:55]
	v_mfma_f32_16x16x32_bf16 v[48:51], v[206:209], v[148:151], v[48:51]
	v_mfma_f32_16x16x32_bf16 v[36:39], v[198:201], v[218:221], v[36:39]
	v_mfma_f32_16x16x32_bf16 v[32:35], v[206:209], v[218:221], v[32:35]
	v_mfma_f32_16x16x32_bf16 v[20:23], v[198:201], v[226:229], v[20:23]
	v_mfma_f32_16x16x32_bf16 v[16:19], v[206:209], v[226:229], v[16:19]
	v_mfma_f32_16x16x32_bf16 v[4:7], v[198:201], v[234:237], v[4:7]
	v_mfma_f32_16x16x32_bf16 v[0:3], v[206:209], v[234:237], v[0:3]
	v_mfma_f32_16x16x32_bf16 v[52:55], v[202:205], v[214:217], v[52:55]
	v_mfma_f32_16x16x32_bf16 v[48:51], v[210:213], v[214:217], v[48:51]
	v_mfma_f32_16x16x32_bf16 v[36:39], v[202:205], v[222:225], v[36:39]
	v_mfma_f32_16x16x32_bf16 v[32:35], v[210:213], v[222:225], v[32:35]
	v_mfma_f32_16x16x32_bf16 v[20:23], v[202:205], v[230:233], v[20:23]
	v_mfma_f32_16x16x32_bf16 v[16:19], v[210:213], v[230:233], v[16:19]
	v_mfma_f32_16x16x32_bf16 v[4:7], v[202:205], v[238:241], v[4:7]
	v_mfma_f32_16x16x32_bf16 v[0:3], v[210:213], v[238:241], v[0:3]
	s_barrier
	s_add_i32 s69, s69, 2
	s_addk_i32 s70, 0x100
	s_add_u32 s38, s38, 0x100
	s_addc_u32 s39, s39, 0
	s_cmp_gt_u32 s69, 29
	s_cbranch_scc1 .LBB0_2414

.LBB0_2522:
	ds_read_b128 v[156:159], v153
	ds_read_b128 v[160:163], v153 offset:1024
	ds_read_b128 v[164:167], v153 offset:2048
	ds_read_b128 v[168:171], v153 offset:3072
	ds_read_b128 v[172:175], v154
	ds_read_b128 v[176:179], v154 offset:1024
	ds_read_b128 v[180:183], v154 offset:2048
	ds_read_b128 v[184:187], v154 offset:3072
	s_add_i32 s22, s53, s10
	s_add_u32 s58, s28, s22
	s_addc_u32 s59, s29, 0
	s_add_i32 m0, s31, 0xc000
	s_add_i32 s60, s31, 0xe000
	s_add_i32 s61, s10, 0xfffc0080
	s_cmp_eq_u32 s19, 12
	s_cselect_b32 s22, s50, s53
	s_cselect_b32 s23, s51, s56
	v_lshl_add_u64 v[220:221], s[58:59], 0, v[130:131]
	ds_read_b128 v[188:191], v155
	ds_read_b128 v[192:195], v155 offset:1024
	ds_read_b128 v[196:199], v155 offset:2048
	ds_read_b128 v[200:203], v155 offset:3072
	ds_read_b128 v[204:207], v155 offset:4096
	ds_read_b128 v[208:211], v155 offset:5120
	ds_read_b128 v[212:215], v155 offset:6144
	ds_read_b128 v[216:219], v155 offset:7168
	global_load_lds_dwordx4 v[220:221], off
	v_lshl_add_u64 v[220:221], s[58:59], 0, v[132:133]
	s_mov_b32 m0, s60
	s_nop 0
	global_load_lds_dwordx4 v[220:221], off
	s_waitcnt vmcnt(8)
	s_waitcnt lgkmcnt(0)
	s_barrier
	v_mfma_f32_16x16x32_bf16 v[124:127], v[156:159], v[188:191], v[124:127]
	v_mfma_f32_16x16x32_bf16 v[120:123], v[164:167], v[188:191], v[120:123]
	v_mfma_f32_16x16x32_bf16 v[108:111], v[156:159], v[196:199], v[108:111]
	v_mfma_f32_16x16x32_bf16 v[104:107], v[164:167], v[196:199], v[104:107]
	v_mfma_f32_16x16x32_bf16 v[92:95], v[156:159], v[204:207], v[92:95]
	v_mfma_f32_16x16x32_bf16 v[88:91], v[164:167], v[204:207], v[88:91]
	v_mfma_f32_16x16x32_bf16 v[76:79], v[156:159], v[212:215], v[76:79]
	v_mfma_f32_16x16x32_bf16 v[72:75], v[164:167], v[212:215], v[72:75]
	v_mfma_f32_16x16x32_bf16 v[124:127], v[160:163], v[192:195], v[124:127]
	v_mfma_f32_16x16x32_bf16 v[120:123], v[168:171], v[192:195], v[120:123]
	v_mfma_f32_16x16x32_bf16 v[108:111], v[160:163], v[200:203], v[108:111]
	v_mfma_f32_16x16x32_bf16 v[104:107], v[168:171], v[200:203], v[104:107]
	v_mfma_f32_16x16x32_bf16 v[92:95], v[160:163], v[208:211], v[92:95]
	v_mfma_f32_16x16x32_bf16 v[88:91], v[168:171], v[208:211], v[88:91]
	v_mfma_f32_16x16x32_bf16 v[76:79], v[160:163], v[216:219], v[76:79]
	v_mfma_f32_16x16x32_bf16 v[72:75], v[168:171], v[216:219], v[72:75]
	v_mfma_f32_16x16x32_bf16 v[116:119], v[172:175], v[188:191], v[116:119]
	v_mfma_f32_16x16x32_bf16 v[112:115], v[180:183], v[188:191], v[112:115]
	v_mfma_f32_16x16x32_bf16 v[100:103], v[172:175], v[196:199], v[100:103]
	v_mfma_f32_16x16x32_bf16 v[96:99], v[180:183], v[196:199], v[96:99]
	v_mfma_f32_16x16x32_bf16 v[84:87], v[172:175], v[204:207], v[84:87]
	v_mfma_f32_16x16x32_bf16 v[80:83], v[180:183], v[204:207], v[80:83]
	v_mfma_f32_16x16x32_bf16 v[68:71], v[172:175], v[212:215], v[68:71]
	v_mfma_f32_16x16x32_bf16 v[64:67], v[180:183], v[212:215], v[64:67]
	v_mfma_f32_16x16x32_bf16 v[116:119], v[176:179], v[192:195], v[116:119]
	v_mfma_f32_16x16x32_bf16 v[112:115], v[184:187], v[192:195], v[112:115]
	v_mfma_f32_16x16x32_bf16 v[100:103], v[176:179], v[200:203], v[100:103]
	v_mfma_f32_16x16x32_bf16 v[96:99], v[184:187], v[200:203], v[96:99]
	v_mfma_f32_16x16x32_bf16 v[84:87], v[176:179], v[208:211], v[84:87]
	v_mfma_f32_16x16x32_bf16 v[80:83], v[184:187], v[208:211], v[80:83]
	v_mfma_f32_16x16x32_bf16 v[68:71], v[176:179], v[216:219], v[68:71]
	v_mfma_f32_16x16x32_bf16 v[64:67], v[184:187], v[216:219], v[64:67]
	s_barrier
	s_cselect_b32 s60, 0, s61
	s_add_i32 s58, s60, s23
	s_ashr_i32 s59, s58, 31
	s_add_u32 s58, s8, s58
	s_addc_u32 s59, s9, s59
	s_add_i32 s61, s42, s26
	v_lshl_add_u64 v[220:221], s[58:59], 0, v[130:131]
	s_mov_b32 m0, s61
	ds_read_b128 v[188:191], v155 offset:16384
	ds_read_b128 v[192:195], v155 offset:17408
	ds_read_b128 v[196:199], v155 offset:18432
	ds_read_b128 v[200:203], v155 offset:19456
	ds_read_b128 v[204:207], v155 offset:20480
	ds_read_b128 v[208:211], v155 offset:21504
	ds_read_b128 v[212:215], v155 offset:22528
	ds_read_b128 v[216:219], v155 offset:23552
	global_load_lds_dwordx4 v[220:221], off
	s_add_i32 m0, s61, 0x2000
	s_add_i32 s61, s23, 0x40000
	v_lshl_add_u64 v[220:221], s[58:59], 0, v[132:133]
	s_add_i32 s58, s61, s60
	s_ashr_i32 s59, s58, 31
	s_add_u32 s58, s8, s58
	s_addc_u32 s59, s9, s59
	s_add_i32 s62, s43, s26
	global_load_lds_dwordx4 v[220:221], off
	v_lshl_add_u64 v[220:221], s[58:59], 0, v[130:131]
	s_mov_b32 m0, s62
	s_nop 0
	global_load_lds_dwordx4 v[220:221], off
	s_add_i32 m0, s62, 0x2000
	s_add_i32 s62, s60, s22
	v_lshl_add_u64 v[220:221], s[58:59], 0, v[132:133]
	s_add_u32 s58, s28, s62
	s_addc_u32 s59, s29, 0
	global_load_lds_dwordx4 v[220:221], off
	v_lshl_add_u64 v[220:221], s[58:59], 0, v[130:131]
	s_mov_b32 m0, s31
	s_nop 0
	global_load_lds_dwordx4 v[220:221], off
	v_lshl_add_u64 v[220:221], s[58:59], 0, v[132:133]
	s_mov_b32 m0, s33
	s_nop 0
	global_load_lds_dwordx4 v[220:221], off
	s_waitcnt vmcnt(8)
	s_waitcnt lgkmcnt(0)
	s_barrier
	v_mfma_f32_16x16x32_bf16 v[60:63], v[156:159], v[188:191], v[60:63]
	v_mfma_f32_16x16x32_bf16 v[56:59], v[164:167], v[188:191], v[56:59]
	v_mfma_f32_16x16x32_bf16 v[44:47], v[156:159], v[196:199], v[44:47]
	v_mfma_f32_16x16x32_bf16 v[40:43], v[164:167], v[196:199], v[40:43]
	v_mfma_f32_16x16x32_bf16 v[28:31], v[156:159], v[204:207], v[28:31]
	v_mfma_f32_16x16x32_bf16 v[24:27], v[164:167], v[204:207], v[24:27]
	v_mfma_f32_16x16x32_bf16 v[12:15], v[156:159], v[212:215], v[12:15]
	v_mfma_f32_16x16x32_bf16 v[8:11], v[164:167], v[212:215], v[8:11]
	v_mfma_f32_16x16x32_bf16 v[60:63], v[160:163], v[192:195], v[60:63]
	v_mfma_f32_16x16x32_bf16 v[56:59], v[168:171], v[192:195], v[56:59]
	v_mfma_f32_16x16x32_bf16 v[44:47], v[160:163], v[200:203], v[44:47]
	v_mfma_f32_16x16x32_bf16 v[40:43], v[168:171], v[200:203], v[40:43]
	v_mfma_f32_16x16x32_bf16 v[28:31], v[160:163], v[208:211], v[28:31]
	v_mfma_f32_16x16x32_bf16 v[24:27], v[168:171], v[208:211], v[24:27]
	v_mfma_f32_16x16x32_bf16 v[12:15], v[160:163], v[216:219], v[12:15]
	v_mfma_f32_16x16x32_bf16 v[8:11], v[168:171], v[216:219], v[8:11]
	v_mfma_f32_16x16x32_bf16 v[52:55], v[172:175], v[188:191], v[52:55]
	v_mfma_f32_16x16x32_bf16 v[48:51], v[180:183], v[188:191], v[48:51]
	v_mfma_f32_16x16x32_bf16 v[36:39], v[172:175], v[196:199], v[36:39]
	v_mfma_f32_16x16x32_bf16 v[32:35], v[180:183], v[196:199], v[32:35]
	v_mfma_f32_16x16x32_bf16 v[20:23], v[172:175], v[204:207], v[20:23]
	v_mfma_f32_16x16x32_bf16 v[16:19], v[180:183], v[204:207], v[16:19]
	v_mfma_f32_16x16x32_bf16 v[4:7], v[172:175], v[212:215], v[4:7]
	v_mfma_f32_16x16x32_bf16 v[0:3], v[180:183], v[212:215], v[0:3]
	v_mfma_f32_16x16x32_bf16 v[52:55], v[176:179], v[192:195], v[52:55]
	v_mfma_f32_16x16x32_bf16 v[48:51], v[184:187], v[192:195], v[48:51]
	v_mfma_f32_16x16x32_bf16 v[36:39], v[176:179], v[200:203], v[36:39]
	v_mfma_f32_16x16x32_bf16 v[32:35], v[184:187], v[200:203], v[32:35]
	v_mfma_f32_16x16x32_bf16 v[20:23], v[176:179], v[208:211], v[20:23]
	v_mfma_f32_16x16x32_bf16 v[16:19], v[184:187], v[208:211], v[16:19]
	v_mfma_f32_16x16x32_bf16 v[4:7], v[176:179], v[216:219], v[4:7]
	v_mfma_f32_16x16x32_bf16 v[0:3], v[184:187], v[216:219], v[0:3]
	s_barrier
	s_add_i32 s63, 0, 0x18000
	s_add_i32 s64, 0, 0x1c000
	v_add_u32_e32 v168, s63, v137
	v_add_u32_e32 v184, s64, v137
	ds_read_b128 v[156:159], v168
	ds_read_b128 v[160:163], v168 offset:1024
	ds_read_b128 v[164:167], v168 offset:2048
	ds_read_b128 v[168:171], v168 offset:3072
	ds_read_b128 v[172:175], v184
	ds_read_b128 v[176:179], v184 offset:1024
	ds_read_b128 v[180:183], v184 offset:2048
	ds_read_b128 v[184:187], v184 offset:3072
	s_add_i32 s62, s62, 0x40000
	s_add_u32 s58, s28, s62
	s_addc_u32 s59, s29, 0
	s_mov_b32 m0, s34
	v_lshl_add_u64 v[220:221], s[58:59], 0, v[130:131]
	ds_read_b128 v[188:191], v155 offset:32768
	ds_read_b128 v[192:195], v155 offset:33792
	ds_read_b128 v[196:199], v155 offset:34816
	ds_read_b128 v[200:203], v155 offset:35840
	ds_read_b128 v[204:207], v155 offset:36864
	ds_read_b128 v[208:211], v155 offset:37888
	ds_read_b128 v[212:215], v155 offset:38912
	ds_read_b128 v[216:219], v155 offset:39936
	global_load_lds_dwordx4 v[220:221], off
	v_lshl_add_u64 v[220:221], s[58:59], 0, v[132:133]
	s_mov_b32 m0, s35
	s_nop 0
	global_load_lds_dwordx4 v[220:221], off
	s_waitcnt vmcnt(8)
	s_waitcnt lgkmcnt(0)
	s_barrier
	v_mfma_f32_16x16x32_bf16 v[124:127], v[156:159], v[188:191], v[124:127]
	v_mfma_f32_16x16x32_bf16 v[120:123], v[164:167], v[188:191], v[120:123]
	v_mfma_f32_16x16x32_bf16 v[108:111], v[156:159], v[196:199], v[108:111]
	v_mfma_f32_16x16x32_bf16 v[104:107], v[164:167], v[196:199], v[104:107]
	v_mfma_f32_16x16x32_bf16 v[92:95], v[156:159], v[204:207], v[92:95]
	v_mfma_f32_16x16x32_bf16 v[88:91], v[164:167], v[204:207], v[88:91]
	v_mfma_f32_16x16x32_bf16 v[76:79], v[156:159], v[212:215], v[76:79]
	v_mfma_f32_16x16x32_bf16 v[72:75], v[164:167], v[212:215], v[72:75]
	v_mfma_f32_16x16x32_bf16 v[124:127], v[160:163], v[192:195], v[124:127]
	v_mfma_f32_16x16x32_bf16 v[120:123], v[168:171], v[192:195], v[120:123]
	v_mfma_f32_16x16x32_bf16 v[108:111], v[160:163], v[200:203], v[108:111]
	v_mfma_f32_16x16x32_bf16 v[104:107], v[168:171], v[200:203], v[104:107]
	v_mfma_f32_16x16x32_bf16 v[92:95], v[160:163], v[208:211], v[92:95]
	v_mfma_f32_16x16x32_bf16 v[88:91], v[168:171], v[208:211], v[88:91]
	v_mfma_f32_16x16x32_bf16 v[76:79], v[160:163], v[216:219], v[76:79]
	v_mfma_f32_16x16x32_bf16 v[72:75], v[168:171], v[216:219], v[72:75]
	v_mfma_f32_16x16x32_bf16 v[116:119], v[172:175], v[188:191], v[116:119]
	v_mfma_f32_16x16x32_bf16 v[112:115], v[180:183], v[188:191], v[112:115]
	v_mfma_f32_16x16x32_bf16 v[100:103], v[172:175], v[196:199], v[100:103]
	v_mfma_f32_16x16x32_bf16 v[96:99], v[180:183], v[196:199], v[96:99]
	v_mfma_f32_16x16x32_bf16 v[84:87], v[172:175], v[204:207], v[84:87]
	v_mfma_f32_16x16x32_bf16 v[80:83], v[180:183], v[204:207], v[80:83]
	v_mfma_f32_16x16x32_bf16 v[68:71], v[172:175], v[212:215], v[68:71]
	v_mfma_f32_16x16x32_bf16 v[64:67], v[180:183], v[212:215], v[64:67]
	v_mfma_f32_16x16x32_bf16 v[116:119], v[176:179], v[192:195], v[116:119]
	v_mfma_f32_16x16x32_bf16 v[112:115], v[184:187], v[192:195], v[112:115]
	v_mfma_f32_16x16x32_bf16 v[100:103], v[176:179], v[200:203], v[100:103]
	v_mfma_f32_16x16x32_bf16 v[96:99], v[184:187], v[200:203], v[96:99]
	v_mfma_f32_16x16x32_bf16 v[84:87], v[176:179], v[208:211], v[84:87]
	v_mfma_f32_16x16x32_bf16 v[80:83], v[184:187], v[208:211], v[80:83]
	v_mfma_f32_16x16x32_bf16 v[68:71], v[176:179], v[216:219], v[68:71]
	v_mfma_f32_16x16x32_bf16 v[64:67], v[184:187], v[216:219], v[64:67]
	s_barrier
; #define PG_BAR __builtin_amdgcn_s_barrier()
; template <class Epi, class Sched, class Hook = NoHook>
; __device__ __forceinline__ void gemm_phase_w(LAS unsigned char* lds, const Sched& S, const Epi& E, int wave_id, const Hook& HK = Hook()) {
;     ...
;         if constexpr (!SEG2) {
;             for (int tt = 0; tt < nt; tt += 2) {
;                 if constexpr (GATHER) { if (tt == nt - 2) {
;                     if (has_next) { gnxt_00 = S.grow_l(nxt, lds, nbuf, R0) + (unsigned)(C0 * 2); gnxt_01 = S.grow_l(nxt, lds, nbuf, R1) + (unsigned)(C1 * 2); gnxt_10 = S.grow_l(nxt, lds, nbuf, 128 + R0) + (unsigned)(C0 * 2); gnxt_11 = S.grow_l(nxt, lds, nbuf, 128 + R1) + (unsigned)(C1 * 2); }
;                     else { gnxt_00 = gcur_00; gnxt_01 = gcur_01; gnxt_10 = gcur_10; gnxt_11 = gcur_11; } } }
;                 PG_TRIP(tt, false, false, false);
;             }
;         } else {
;             for (int tt = 0; tt < nt - 4; tt += 2) PG_TRIP(tt, false, false, false);
;             PG_TRIP(nt - 4, false, true, false);
;             PG_TRIP(nt - 2, true, false, true);
;         }
;     ...
;         if (wr == 0) PG_BAR;
	s_bitset1_b32 s60, 7
	s_add_i32 s23, s60, s23
	s_ashr_i32 s59, s23, 31
	s_add_u32 s58, s8, s23
	s_addc_u32 s59, s9, s59
	s_add_i32 s23, s63, s26
	v_lshl_add_u64 v[220:221], s[58:59], 0, v[130:131]
	s_mov_b32 m0, s23
	ds_read_b128 v[188:191], v155 offset:49152
	ds_read_b128 v[192:195], v155 offset:50176
	ds_read_b128 v[196:199], v155 offset:51200
	ds_read_b128 v[200:203], v155 offset:52224
	ds_read_b128 v[204:207], v155 offset:53248
	ds_read_b128 v[208:211], v155 offset:54272
	ds_read_b128 v[212:215], v155 offset:55296
	ds_read_b128 v[216:219], v155 offset:56320
	global_load_lds_dwordx4 v[220:221], off
	s_add_i32 m0, s23, 0x2000
	s_add_i32 s23, s60, s61
	v_lshl_add_u64 v[220:221], s[58:59], 0, v[132:133]
	s_ashr_i32 s59, s23, 31
	s_add_u32 s58, s8, s23
	s_addc_u32 s59, s9, s59
	s_add_i32 s23, s64, s26
	global_load_lds_dwordx4 v[220:221], off
	v_lshl_add_u64 v[220:221], s[58:59], 0, v[130:131]
	s_mov_b32 m0, s23
	s_add_i32 s60, s60, s22
	global_load_lds_dwordx4 v[220:221], off
	s_add_i32 m0, s23, 0x2000
	s_add_u32 s22, s28, s60
	v_lshl_add_u64 v[220:221], s[58:59], 0, v[132:133]
	s_addc_u32 s23, s29, 0
	global_load_lds_dwordx4 v[220:221], off
	v_lshl_add_u64 v[220:221], s[22:23], 0, v[130:131]
	s_mov_b32 m0, s37
	s_nop 0
	global_load_lds_dwordx4 v[220:221], off
	v_lshl_add_u64 v[220:221], s[22:23], 0, v[132:133]
	s_mov_b32 m0, s38
	s_nop 0
	global_load_lds_dwordx4 v[220:221], off
	s_waitcnt vmcnt(8)
	s_waitcnt lgkmcnt(0)
	s_barrier
	v_mfma_f32_16x16x32_bf16 v[60:63], v[156:159], v[188:191], v[60:63]
	v_mfma_f32_16x16x32_bf16 v[56:59], v[164:167], v[188:191], v[56:59]
	v_mfma_f32_16x16x32_bf16 v[44:47], v[156:159], v[196:199], v[44:47]
	v_mfma_f32_16x16x32_bf16 v[40:43], v[164:167], v[196:199], v[40:43]
	v_mfma_f32_16x16x32_bf16 v[28:31], v[156:159], v[204:207], v[28:31]
	v_mfma_f32_16x16x32_bf16 v[24:27], v[164:167], v[204:207], v[24:27]
	v_mfma_f32_16x16x32_bf16 v[12:15], v[156:159], v[212:215], v[12:15]
	v_mfma_f32_16x16x32_bf16 v[8:11], v[164:167], v[212:215], v[8:11]
	v_mfma_f32_16x16x32_bf16 v[60:63], v[160:163], v[192:195], v[60:63]
	v_mfma_f32_16x16x32_bf16 v[56:59], v[168:171], v[192:195], v[56:59]
	v_mfma_f32_16x16x32_bf16 v[44:47], v[160:163], v[200:203], v[44:47]
	v_mfma_f32_16x16x32_bf16 v[40:43], v[168:171], v[200:203], v[40:43]
	v_mfma_f32_16x16x32_bf16 v[28:31], v[160:163], v[208:211], v[28:31]
	v_mfma_f32_16x16x32_bf16 v[24:27], v[168:171], v[208:211], v[24:27]
	v_mfma_f32_16x16x32_bf16 v[12:15], v[160:163], v[216:219], v[12:15]
	v_mfma_f32_16x16x32_bf16 v[8:11], v[168:171], v[216:219], v[8:11]
	v_mfma_f32_16x16x32_bf16 v[52:55], v[172:175], v[188:191], v[52:55]
	v_mfma_f32_16x16x32_bf16 v[48:51], v[180:183], v[188:191], v[48:51]
	v_mfma_f32_16x16x32_bf16 v[36:39], v[172:175], v[196:199], v[36:39]
	v_mfma_f32_16x16x32_bf16 v[32:35], v[180:183], v[196:199], v[32:35]
	v_mfma_f32_16x16x32_bf16 v[20:23], v[172:175], v[204:207], v[20:23]
	v_mfma_f32_16x16x32_bf16 v[16:19], v[180:183], v[204:207], v[16:19]
	v_mfma_f32_16x16x32_bf16 v[4:7], v[172:175], v[212:215], v[4:7]
	v_mfma_f32_16x16x32_bf16 v[0:3], v[180:183], v[212:215], v[0:3]
	v_mfma_f32_16x16x32_bf16 v[52:55], v[176:179], v[192:195], v[52:55]
	v_mfma_f32_16x16x32_bf16 v[48:51], v[184:187], v[192:195], v[48:51]
	v_mfma_f32_16x16x32_bf16 v[36:39], v[176:179], v[200:203], v[36:39]
	v_mfma_f32_16x16x32_bf16 v[32:35], v[184:187], v[200:203], v[32:35]
	v_mfma_f32_16x16x32_bf16 v[20:23], v[176:179], v[208:211], v[20:23]
	v_mfma_f32_16x16x32_bf16 v[16:19], v[184:187], v[208:211], v[16:19]
	v_mfma_f32_16x16x32_bf16 v[4:7], v[176:179], v[216:219], v[4:7]
	v_mfma_f32_16x16x32_bf16 v[0:3], v[184:187], v[216:219], v[0:3]
	s_barrier
	s_addk_i32 s10, 0x100
	s_add_i32 s19, s19, 2
	s_cmp_gt_u32 s19, 13
	s_cbranch_scc0 .LBB0_2522
	s_and_b64 vcc, exec, s[6:7]
	s_cbranch_vccz .LBB0_2525
	s_barrier
